# back-edge rotation: K-loop counter/pointer updates and exit test hoisted above the loop-back barrier (14 GEMM loops)
# baseline (speedup 1.0000x reference)
.LBB0_261:
	ds_read_b128 v[144:147], v141
	ds_read_b128 v[148:151], v141 offset:1024
	ds_read_b128 v[152:155], v141 offset:2048
	ds_read_b128 v[156:159], v141 offset:3072
	ds_read_b128 v[160:163], v142
	ds_read_b128 v[164:167], v142 offset:1024
	ds_read_b128 v[168:171], v142 offset:2048
	ds_read_b128 v[172:175], v142 offset:3072
	s_add_i32 s0, s67, s10
	s_add_u32 s0, s4, s0
	s_addc_u32 s1, s5, 0
	s_add_i32 m0, s22, 0xc000
	s_add_i32 s30, s22, 0xe000
	s_add_i32 s31, s10, 0xfff80080
	s_cmp_eq_u32 s18, 28
	s_cselect_b32 s19, s45, s67
	s_cselect_b32 s68, s44, s66
	v_lshl_add_u64 v[208:209], s[0:1], 0, v[128:129]
	ds_read_b128 v[176:179], v143
	ds_read_b128 v[180:183], v143 offset:1024
	ds_read_b128 v[184:187], v143 offset:2048
	ds_read_b128 v[188:191], v143 offset:3072
	ds_read_b128 v[192:195], v143 offset:4096
	ds_read_b128 v[196:199], v143 offset:5120
	ds_read_b128 v[200:203], v143 offset:6144
	ds_read_b128 v[204:207], v143 offset:7168
	global_load_lds_dwordx4 v[208:209], off
	v_lshl_add_u64 v[208:209], s[0:1], 0, v[130:131]
	s_mov_b32 m0, s30
	s_nop 0
	global_load_lds_dwordx4 v[208:209], off
	s_waitcnt vmcnt(8)
	s_waitcnt lgkmcnt(0)
	s_barrier
	s_waitcnt lgkmcnt(0)
	v_mfma_f32_16x16x32_bf16 v[124:127], v[144:147], v[176:179], v[124:127]
	v_mfma_f32_16x16x32_bf16 v[120:123], v[152:155], v[176:179], v[120:123]
	v_mfma_f32_16x16x32_bf16 v[116:119], v[144:147], v[184:187], v[116:119]
	v_mfma_f32_16x16x32_bf16 v[112:115], v[152:155], v[184:187], v[112:115]
	v_mfma_f32_16x16x32_bf16 v[108:111], v[144:147], v[192:195], v[108:111]
	v_mfma_f32_16x16x32_bf16 v[100:103], v[152:155], v[192:195], v[100:103]
	v_mfma_f32_16x16x32_bf16 v[92:95], v[144:147], v[200:203], v[92:95]
	v_mfma_f32_16x16x32_bf16 v[84:87], v[152:155], v[200:203], v[84:87]
	v_mfma_f32_16x16x32_bf16 v[124:127], v[148:151], v[180:183], v[124:127]
	v_mfma_f32_16x16x32_bf16 v[120:123], v[156:159], v[180:183], v[120:123]
	v_mfma_f32_16x16x32_bf16 v[116:119], v[148:151], v[188:191], v[116:119]
	v_mfma_f32_16x16x32_bf16 v[112:115], v[156:159], v[188:191], v[112:115]
	v_mfma_f32_16x16x32_bf16 v[108:111], v[148:151], v[196:199], v[108:111]
	v_mfma_f32_16x16x32_bf16 v[100:103], v[156:159], v[196:199], v[100:103]
	v_mfma_f32_16x16x32_bf16 v[92:95], v[148:151], v[204:207], v[92:95]
	v_mfma_f32_16x16x32_bf16 v[84:87], v[156:159], v[204:207], v[84:87]
	v_mfma_f32_16x16x32_bf16 v[104:107], v[160:163], v[176:179], v[104:107]
	v_mfma_f32_16x16x32_bf16 v[96:99], v[168:171], v[176:179], v[96:99]
	v_mfma_f32_16x16x32_bf16 v[88:91], v[160:163], v[184:187], v[88:91]
	v_mfma_f32_16x16x32_bf16 v[80:83], v[168:171], v[184:187], v[80:83]
	v_mfma_f32_16x16x32_bf16 v[76:79], v[160:163], v[192:195], v[76:79]
	v_mfma_f32_16x16x32_bf16 v[72:75], v[168:171], v[192:195], v[72:75]
	v_mfma_f32_16x16x32_bf16 v[68:71], v[160:163], v[200:203], v[68:71]
	v_mfma_f32_16x16x32_bf16 v[64:67], v[168:171], v[200:203], v[64:67]
	v_mfma_f32_16x16x32_bf16 v[104:107], v[164:167], v[180:183], v[104:107]
	v_mfma_f32_16x16x32_bf16 v[96:99], v[172:175], v[180:183], v[96:99]
	v_mfma_f32_16x16x32_bf16 v[88:91], v[164:167], v[188:191], v[88:91]
	v_mfma_f32_16x16x32_bf16 v[80:83], v[172:175], v[188:191], v[80:83]
	v_mfma_f32_16x16x32_bf16 v[76:79], v[164:167], v[196:199], v[76:79]
	v_mfma_f32_16x16x32_bf16 v[72:75], v[172:175], v[196:199], v[72:75]
	v_mfma_f32_16x16x32_bf16 v[68:71], v[164:167], v[204:207], v[68:71]
	v_mfma_f32_16x16x32_bf16 v[64:67], v[172:175], v[204:207], v[64:67]
	s_barrier
	s_cselect_b32 s30, 0, s31
	s_add_i32 s0, s30, s68
	s_ashr_i32 s1, s0, 31
	s_add_u32 s0, s6, s0
	s_addc_u32 s1, s7, s1
	s_add_i32 s31, s38, s27
	v_lshl_add_u64 v[208:209], s[0:1], 0, v[128:129]
	s_mov_b32 m0, s31
	ds_read_b128 v[176:179], v143 offset:16384
	ds_read_b128 v[180:183], v143 offset:17408
	ds_read_b128 v[184:187], v143 offset:18432
	ds_read_b128 v[188:191], v143 offset:19456
	ds_read_b128 v[192:195], v143 offset:20480
	ds_read_b128 v[196:199], v143 offset:21504
	ds_read_b128 v[200:203], v143 offset:22528
	ds_read_b128 v[204:207], v143 offset:23552
	global_load_lds_dwordx4 v[208:209], off
	s_add_i32 m0, s31, 0x2000
	s_add_i32 s31, s68, 0x80000
	v_lshl_add_u64 v[208:209], s[0:1], 0, v[130:131]
	s_add_i32 s0, s31, s30
	s_ashr_i32 s1, s0, 31
	s_add_u32 s0, s6, s0
	s_addc_u32 s1, s7, s1
	s_add_i32 s69, s39, s27
	global_load_lds_dwordx4 v[208:209], off
	v_lshl_add_u64 v[208:209], s[0:1], 0, v[128:129]
	s_mov_b32 m0, s69
	s_nop 0
	global_load_lds_dwordx4 v[208:209], off
	s_add_i32 m0, s69, 0x2000
	s_add_i32 s69, s30, s19
	v_lshl_add_u64 v[208:209], s[0:1], 0, v[130:131]
	s_add_u32 s0, s4, s69
	s_addc_u32 s1, s5, 0
	global_load_lds_dwordx4 v[208:209], off
	v_lshl_add_u64 v[208:209], s[0:1], 0, v[128:129]
	s_mov_b32 m0, s22
	s_nop 0
	global_load_lds_dwordx4 v[208:209], off
	v_lshl_add_u64 v[208:209], s[0:1], 0, v[130:131]
	s_mov_b32 m0, s23
	s_nop 0
	global_load_lds_dwordx4 v[208:209], off
	s_waitcnt vmcnt(8)
	s_waitcnt lgkmcnt(0)
	s_barrier
	s_waitcnt lgkmcnt(0)
	v_mfma_f32_16x16x32_bf16 v[60:63], v[144:147], v[176:179], v[60:63]
	v_mfma_f32_16x16x32_bf16 v[56:59], v[152:155], v[176:179], v[56:59]
	v_mfma_f32_16x16x32_bf16 v[52:55], v[144:147], v[184:187], v[52:55]
	v_mfma_f32_16x16x32_bf16 v[48:51], v[152:155], v[184:187], v[48:51]
	v_mfma_f32_16x16x32_bf16 v[44:47], v[144:147], v[192:195], v[44:47]
	v_mfma_f32_16x16x32_bf16 v[36:39], v[152:155], v[192:195], v[36:39]
	v_mfma_f32_16x16x32_bf16 v[28:31], v[144:147], v[200:203], v[28:31]
	v_mfma_f32_16x16x32_bf16 v[20:23], v[152:155], v[200:203], v[20:23]
	v_mfma_f32_16x16x32_bf16 v[60:63], v[148:151], v[180:183], v[60:63]
	v_mfma_f32_16x16x32_bf16 v[56:59], v[156:159], v[180:183], v[56:59]
	v_mfma_f32_16x16x32_bf16 v[52:55], v[148:151], v[188:191], v[52:55]
	v_mfma_f32_16x16x32_bf16 v[48:51], v[156:159], v[188:191], v[48:51]
	v_mfma_f32_16x16x32_bf16 v[44:47], v[148:151], v[196:199], v[44:47]
	v_mfma_f32_16x16x32_bf16 v[36:39], v[156:159], v[196:199], v[36:39]
	v_mfma_f32_16x16x32_bf16 v[28:31], v[148:151], v[204:207], v[28:31]
	v_mfma_f32_16x16x32_bf16 v[20:23], v[156:159], v[204:207], v[20:23]
	v_mfma_f32_16x16x32_bf16 v[40:43], v[160:163], v[176:179], v[40:43]
	v_mfma_f32_16x16x32_bf16 v[32:35], v[168:171], v[176:179], v[32:35]
	v_mfma_f32_16x16x32_bf16 v[24:27], v[160:163], v[184:187], v[24:27]
	v_mfma_f32_16x16x32_bf16 v[16:19], v[168:171], v[184:187], v[16:19]
	v_mfma_f32_16x16x32_bf16 v[12:15], v[160:163], v[192:195], v[12:15]
	v_mfma_f32_16x16x32_bf16 v[8:11], v[168:171], v[192:195], v[8:11]
	v_mfma_f32_16x16x32_bf16 v[4:7], v[160:163], v[200:203], v[4:7]
	v_mfma_f32_16x16x32_bf16 v[0:3], v[168:171], v[200:203], v[0:3]
	v_mfma_f32_16x16x32_bf16 v[40:43], v[164:167], v[180:183], v[40:43]
	v_mfma_f32_16x16x32_bf16 v[32:35], v[172:175], v[180:183], v[32:35]
	v_mfma_f32_16x16x32_bf16 v[24:27], v[164:167], v[188:191], v[24:27]
	v_mfma_f32_16x16x32_bf16 v[16:19], v[172:175], v[188:191], v[16:19]
	v_mfma_f32_16x16x32_bf16 v[12:15], v[164:167], v[196:199], v[12:15]
	v_mfma_f32_16x16x32_bf16 v[8:11], v[172:175], v[196:199], v[8:11]
	v_mfma_f32_16x16x32_bf16 v[4:7], v[164:167], v[204:207], v[4:7]
	v_mfma_f32_16x16x32_bf16 v[0:3], v[172:175], v[204:207], v[0:3]
	s_barrier
	s_add_i32 s70, 0, 0x18000
	s_add_i32 s71, 0, 0x1c000
	v_add_u32_e32 v156, s70, v140
	v_add_u32_e32 v172, s71, v140
	ds_read_b128 v[144:147], v156
	ds_read_b128 v[148:151], v156 offset:1024
	ds_read_b128 v[152:155], v156 offset:2048
	ds_read_b128 v[156:159], v156 offset:3072
	ds_read_b128 v[160:163], v172
	ds_read_b128 v[164:167], v172 offset:1024
	ds_read_b128 v[168:171], v172 offset:2048
	ds_read_b128 v[172:175], v172 offset:3072
	s_add_i32 s69, s69, 0x80000
	s_add_u32 s0, s4, s69
	s_addc_u32 s1, s5, 0
	s_mov_b32 m0, s24
	v_lshl_add_u64 v[208:209], s[0:1], 0, v[128:129]
	ds_read_b128 v[176:179], v143 offset:32768
	ds_read_b128 v[180:183], v143 offset:33792
	ds_read_b128 v[184:187], v143 offset:34816
	ds_read_b128 v[188:191], v143 offset:35840
	ds_read_b128 v[192:195], v143 offset:36864
	ds_read_b128 v[196:199], v143 offset:37888
	ds_read_b128 v[200:203], v143 offset:38912
	ds_read_b128 v[204:207], v143 offset:39936
	global_load_lds_dwordx4 v[208:209], off
	v_lshl_add_u64 v[208:209], s[0:1], 0, v[130:131]
	s_mov_b32 m0, s25
	s_nop 0
	global_load_lds_dwordx4 v[208:209], off
	s_waitcnt vmcnt(8)
	s_waitcnt lgkmcnt(0)
	s_barrier
	s_waitcnt lgkmcnt(0)
	v_mfma_f32_16x16x32_bf16 v[124:127], v[144:147], v[176:179], v[124:127]
	v_mfma_f32_16x16x32_bf16 v[120:123], v[152:155], v[176:179], v[120:123]
	v_mfma_f32_16x16x32_bf16 v[116:119], v[144:147], v[184:187], v[116:119]
	v_mfma_f32_16x16x32_bf16 v[112:115], v[152:155], v[184:187], v[112:115]
	v_mfma_f32_16x16x32_bf16 v[108:111], v[144:147], v[192:195], v[108:111]
	v_mfma_f32_16x16x32_bf16 v[100:103], v[152:155], v[192:195], v[100:103]
	v_mfma_f32_16x16x32_bf16 v[92:95], v[144:147], v[200:203], v[92:95]
	v_mfma_f32_16x16x32_bf16 v[84:87], v[152:155], v[200:203], v[84:87]
	v_mfma_f32_16x16x32_bf16 v[124:127], v[148:151], v[180:183], v[124:127]
	v_mfma_f32_16x16x32_bf16 v[120:123], v[156:159], v[180:183], v[120:123]
	v_mfma_f32_16x16x32_bf16 v[116:119], v[148:151], v[188:191], v[116:119]
	v_mfma_f32_16x16x32_bf16 v[112:115], v[156:159], v[188:191], v[112:115]
	v_mfma_f32_16x16x32_bf16 v[108:111], v[148:151], v[196:199], v[108:111]
	v_mfma_f32_16x16x32_bf16 v[100:103], v[156:159], v[196:199], v[100:103]
	v_mfma_f32_16x16x32_bf16 v[92:95], v[148:151], v[204:207], v[92:95]
	v_mfma_f32_16x16x32_bf16 v[84:87], v[156:159], v[204:207], v[84:87]
	v_mfma_f32_16x16x32_bf16 v[104:107], v[160:163], v[176:179], v[104:107]
	v_mfma_f32_16x16x32_bf16 v[96:99], v[168:171], v[176:179], v[96:99]
	v_mfma_f32_16x16x32_bf16 v[88:91], v[160:163], v[184:187], v[88:91]
	v_mfma_f32_16x16x32_bf16 v[80:83], v[168:171], v[184:187], v[80:83]
	v_mfma_f32_16x16x32_bf16 v[76:79], v[160:163], v[192:195], v[76:79]
	v_mfma_f32_16x16x32_bf16 v[72:75], v[168:171], v[192:195], v[72:75]
	v_mfma_f32_16x16x32_bf16 v[68:71], v[160:163], v[200:203], v[68:71]
	v_mfma_f32_16x16x32_bf16 v[64:67], v[168:171], v[200:203], v[64:67]
	v_mfma_f32_16x16x32_bf16 v[104:107], v[164:167], v[180:183], v[104:107]
	v_mfma_f32_16x16x32_bf16 v[96:99], v[172:175], v[180:183], v[96:99]
	v_mfma_f32_16x16x32_bf16 v[88:91], v[164:167], v[188:191], v[88:91]
	v_mfma_f32_16x16x32_bf16 v[80:83], v[172:175], v[188:191], v[80:83]
	v_mfma_f32_16x16x32_bf16 v[76:79], v[164:167], v[196:199], v[76:79]
	v_mfma_f32_16x16x32_bf16 v[72:75], v[172:175], v[196:199], v[72:75]
	v_mfma_f32_16x16x32_bf16 v[68:71], v[164:167], v[204:207], v[68:71]
	v_mfma_f32_16x16x32_bf16 v[64:67], v[172:175], v[204:207], v[64:67]
	s_barrier
; template <class Epi, class Sched, class Hook = NoHook>
; __device__ __forceinline__ void gemm_phase_w(LAS unsigned char* lds, const Sched& S, const Epi& E, int wave_id, const Hook& HK = Hook()) {
;     ...
;         if constexpr (!SEG2) {
;             for (int tt = 0; tt < nt; tt += 2) {
;                 if constexpr (GATHER) { if (tt == nt - 2) {
;                     if (has_next) { gnxt_00 = S.grow_l(nxt, lds, nbuf, R0) + (unsigned)(C0 * 2); gnxt_01 = S.grow_l(nxt, lds, nbuf, R1) + (unsigned)(C1 * 2); gnxt_10 = S.grow_l(nxt, lds, nbuf, 128 + R0) + (unsigned)(C0 * 2); gnxt_11 = S.grow_l(nxt, lds, nbuf, 128 + R1) + (unsigned)(C1 * 2); }
;                     else { gnxt_00 = gcur_00; gnxt_01 = gcur_01; gnxt_10 = gcur_10; gnxt_11 = gcur_11; } } }
;                 PG_TRIP(tt, false, false, false);
;             }
	s_bitset1_b32 s30, 7
	s_add_i32 s0, s30, s68
	s_ashr_i32 s1, s0, 31
	s_add_u32 s0, s6, s0
	s_addc_u32 s1, s7, s1
	s_add_i32 s68, s70, s27
	v_lshl_add_u64 v[208:209], s[0:1], 0, v[128:129]
	s_mov_b32 m0, s68
	ds_read_b128 v[176:179], v143 offset:49152
	ds_read_b128 v[180:183], v143 offset:50176
	ds_read_b128 v[184:187], v143 offset:51200
	ds_read_b128 v[188:191], v143 offset:52224
	ds_read_b128 v[192:195], v143 offset:53248
	ds_read_b128 v[196:199], v143 offset:54272
	ds_read_b128 v[200:203], v143 offset:55296
	ds_read_b128 v[204:207], v143 offset:56320
	global_load_lds_dwordx4 v[208:209], off
	v_lshl_add_u64 v[208:209], s[0:1], 0, v[130:131]
	s_add_i32 s0, s30, s31
	s_add_i32 m0, s68, 0x2000
	s_ashr_i32 s1, s0, 31
	s_add_u32 s0, s6, s0
	s_addc_u32 s1, s7, s1
	s_add_i32 s31, s71, s27
	global_load_lds_dwordx4 v[208:209], off
	v_lshl_add_u64 v[208:209], s[0:1], 0, v[128:129]
	s_mov_b32 m0, s31
	s_add_i32 s30, s30, s19
	global_load_lds_dwordx4 v[208:209], off
	s_add_i32 m0, s31, 0x2000
	v_lshl_add_u64 v[208:209], s[0:1], 0, v[130:131]
	s_add_u32 s0, s4, s30
	s_addc_u32 s1, s5, 0
	global_load_lds_dwordx4 v[208:209], off
	v_lshl_add_u64 v[208:209], s[0:1], 0, v[128:129]
	s_mov_b32 m0, s36
	s_nop 0
	global_load_lds_dwordx4 v[208:209], off
	v_lshl_add_u64 v[208:209], s[0:1], 0, v[130:131]
	s_mov_b32 m0, s37
	s_nop 0
	global_load_lds_dwordx4 v[208:209], off
	s_waitcnt vmcnt(8)
	s_waitcnt lgkmcnt(0)
	s_barrier
	s_waitcnt lgkmcnt(0)
	v_mfma_f32_16x16x32_bf16 v[60:63], v[144:147], v[176:179], v[60:63]
	v_mfma_f32_16x16x32_bf16 v[56:59], v[152:155], v[176:179], v[56:59]
	v_mfma_f32_16x16x32_bf16 v[52:55], v[144:147], v[184:187], v[52:55]
	v_mfma_f32_16x16x32_bf16 v[48:51], v[152:155], v[184:187], v[48:51]
	v_mfma_f32_16x16x32_bf16 v[44:47], v[144:147], v[192:195], v[44:47]
	v_mfma_f32_16x16x32_bf16 v[36:39], v[152:155], v[192:195], v[36:39]
	v_mfma_f32_16x16x32_bf16 v[28:31], v[144:147], v[200:203], v[28:31]
	v_mfma_f32_16x16x32_bf16 v[20:23], v[152:155], v[200:203], v[20:23]
	v_mfma_f32_16x16x32_bf16 v[60:63], v[148:151], v[180:183], v[60:63]
	v_mfma_f32_16x16x32_bf16 v[56:59], v[156:159], v[180:183], v[56:59]
	v_mfma_f32_16x16x32_bf16 v[52:55], v[148:151], v[188:191], v[52:55]
	v_mfma_f32_16x16x32_bf16 v[48:51], v[156:159], v[188:191], v[48:51]
	v_mfma_f32_16x16x32_bf16 v[44:47], v[148:151], v[196:199], v[44:47]
	v_mfma_f32_16x16x32_bf16 v[36:39], v[156:159], v[196:199], v[36:39]
	v_mfma_f32_16x16x32_bf16 v[28:31], v[148:151], v[204:207], v[28:31]
	v_mfma_f32_16x16x32_bf16 v[20:23], v[156:159], v[204:207], v[20:23]
	v_mfma_f32_16x16x32_bf16 v[40:43], v[160:163], v[176:179], v[40:43]
	v_mfma_f32_16x16x32_bf16 v[32:35], v[168:171], v[176:179], v[32:35]
	v_mfma_f32_16x16x32_bf16 v[24:27], v[160:163], v[184:187], v[24:27]
	v_mfma_f32_16x16x32_bf16 v[16:19], v[168:171], v[184:187], v[16:19]
	v_mfma_f32_16x16x32_bf16 v[12:15], v[160:163], v[192:195], v[12:15]
	v_mfma_f32_16x16x32_bf16 v[8:11], v[168:171], v[192:195], v[8:11]
	v_mfma_f32_16x16x32_bf16 v[4:7], v[160:163], v[200:203], v[4:7]
	v_mfma_f32_16x16x32_bf16 v[0:3], v[168:171], v[200:203], v[0:3]
	v_mfma_f32_16x16x32_bf16 v[40:43], v[164:167], v[180:183], v[40:43]
	v_mfma_f32_16x16x32_bf16 v[32:35], v[172:175], v[180:183], v[32:35]
	v_mfma_f32_16x16x32_bf16 v[24:27], v[164:167], v[188:191], v[24:27]
	v_mfma_f32_16x16x32_bf16 v[16:19], v[172:175], v[188:191], v[16:19]
	v_mfma_f32_16x16x32_bf16 v[12:15], v[164:167], v[196:199], v[12:15]
	v_mfma_f32_16x16x32_bf16 v[8:11], v[172:175], v[196:199], v[8:11]
	v_mfma_f32_16x16x32_bf16 v[4:7], v[164:167], v[204:207], v[4:7]
	v_mfma_f32_16x16x32_bf16 v[0:3], v[172:175], v[204:207], v[0:3]
	s_addk_i32 s10, 0x100
	s_add_i32 s18, s18, 2
	s_cmp_gt_u32 s18, 29
	s_barrier
	s_cbranch_scc0 .LBB0_261
	s_and_b64 vcc, exec, s[14:15]
	s_cbranch_vccz .LBB0_264
	s_barrier

.LBB0_386:
	ds_read_b128 v[142:145], v139
	ds_read_b128 v[146:149], v139 offset:1024
	ds_read_b128 v[150:153], v139 offset:2048
	ds_read_b128 v[154:157], v139 offset:3072
	ds_read_b128 v[158:161], v140
	ds_read_b128 v[162:165], v140 offset:1024
	ds_read_b128 v[166:169], v140 offset:2048
	ds_read_b128 v[170:173], v140 offset:3072
	s_add_i32 s0, s45, s10
	s_add_u32 s0, s4, s0
	s_addc_u32 s1, s5, 0
	s_add_i32 m0, s23, 0xc000
	s_add_i32 s61, s23, 0xe000
	s_add_i32 s66, s10, 0xfff80080
	s_cmp_eq_u32 s18, 28
	s_cselect_b32 s19, s41, s45
	s_cselect_b32 s60, s40, s44
	v_lshl_add_u64 v[206:207], s[0:1], 0, v[128:129]
	ds_read_b128 v[174:177], v141
	ds_read_b128 v[178:181], v141 offset:1024
	ds_read_b128 v[182:185], v141 offset:2048
	ds_read_b128 v[186:189], v141 offset:3072
	ds_read_b128 v[190:193], v141 offset:4096
	ds_read_b128 v[194:197], v141 offset:5120
	ds_read_b128 v[198:201], v141 offset:6144
	ds_read_b128 v[202:205], v141 offset:7168
	global_load_lds_dwordx4 v[206:207], off
	v_lshl_add_u64 v[206:207], s[0:1], 0, v[130:131]
	s_mov_b32 m0, s61
	s_nop 0
	global_load_lds_dwordx4 v[206:207], off
	s_waitcnt vmcnt(8)
	s_waitcnt lgkmcnt(0)
	s_barrier
	s_waitcnt lgkmcnt(0)
	v_mfma_f32_16x16x32_bf16 v[124:127], v[142:145], v[174:177], v[124:127]
	v_mfma_f32_16x16x32_bf16 v[120:123], v[150:153], v[174:177], v[120:123]
	v_mfma_f32_16x16x32_bf16 v[116:119], v[142:145], v[182:185], v[116:119]
	v_mfma_f32_16x16x32_bf16 v[112:115], v[150:153], v[182:185], v[112:115]
	v_mfma_f32_16x16x32_bf16 v[108:111], v[142:145], v[190:193], v[108:111]
	v_mfma_f32_16x16x32_bf16 v[100:103], v[150:153], v[190:193], v[100:103]
	v_mfma_f32_16x16x32_bf16 v[92:95], v[142:145], v[198:201], v[92:95]
	v_mfma_f32_16x16x32_bf16 v[84:87], v[150:153], v[198:201], v[84:87]
	v_mfma_f32_16x16x32_bf16 v[124:127], v[146:149], v[178:181], v[124:127]
	v_mfma_f32_16x16x32_bf16 v[120:123], v[154:157], v[178:181], v[120:123]
	v_mfma_f32_16x16x32_bf16 v[116:119], v[146:149], v[186:189], v[116:119]
	v_mfma_f32_16x16x32_bf16 v[112:115], v[154:157], v[186:189], v[112:115]
	v_mfma_f32_16x16x32_bf16 v[108:111], v[146:149], v[194:197], v[108:111]
	v_mfma_f32_16x16x32_bf16 v[100:103], v[154:157], v[194:197], v[100:103]
	v_mfma_f32_16x16x32_bf16 v[92:95], v[146:149], v[202:205], v[92:95]
	v_mfma_f32_16x16x32_bf16 v[84:87], v[154:157], v[202:205], v[84:87]
	v_mfma_f32_16x16x32_bf16 v[104:107], v[158:161], v[174:177], v[104:107]
	v_mfma_f32_16x16x32_bf16 v[96:99], v[166:169], v[174:177], v[96:99]
	v_mfma_f32_16x16x32_bf16 v[88:91], v[158:161], v[182:185], v[88:91]
	v_mfma_f32_16x16x32_bf16 v[80:83], v[166:169], v[182:185], v[80:83]
	v_mfma_f32_16x16x32_bf16 v[76:79], v[158:161], v[190:193], v[76:79]
	v_mfma_f32_16x16x32_bf16 v[72:75], v[166:169], v[190:193], v[72:75]
	v_mfma_f32_16x16x32_bf16 v[68:71], v[158:161], v[198:201], v[68:71]
	v_mfma_f32_16x16x32_bf16 v[64:67], v[166:169], v[198:201], v[64:67]
	v_mfma_f32_16x16x32_bf16 v[104:107], v[162:165], v[178:181], v[104:107]
	v_mfma_f32_16x16x32_bf16 v[96:99], v[170:173], v[178:181], v[96:99]
	v_mfma_f32_16x16x32_bf16 v[88:91], v[162:165], v[186:189], v[88:91]
	v_mfma_f32_16x16x32_bf16 v[80:83], v[170:173], v[186:189], v[80:83]
	v_mfma_f32_16x16x32_bf16 v[76:79], v[162:165], v[194:197], v[76:79]
	v_mfma_f32_16x16x32_bf16 v[72:75], v[170:173], v[194:197], v[72:75]
	v_mfma_f32_16x16x32_bf16 v[68:71], v[162:165], v[202:205], v[68:71]
	v_mfma_f32_16x16x32_bf16 v[64:67], v[170:173], v[202:205], v[64:67]
	s_barrier
	s_cselect_b32 s61, 0, s66
	s_add_i32 s0, s61, s60
	s_ashr_i32 s1, s0, 31
	s_add_u32 s0, s6, s0
	s_addc_u32 s1, s7, s1
	s_add_i32 s66, s30, s27
	v_lshl_add_u64 v[206:207], s[0:1], 0, v[128:129]
	s_mov_b32 m0, s66
	ds_read_b128 v[174:177], v141 offset:16384
	ds_read_b128 v[178:181], v141 offset:17408
	ds_read_b128 v[182:185], v141 offset:18432
	ds_read_b128 v[186:189], v141 offset:19456
	ds_read_b128 v[190:193], v141 offset:20480
	ds_read_b128 v[194:197], v141 offset:21504
	ds_read_b128 v[198:201], v141 offset:22528
	ds_read_b128 v[202:205], v141 offset:23552
	global_load_lds_dwordx4 v[206:207], off
	s_add_i32 m0, s66, 0x2000
	s_add_i32 s66, s60, 0x80000
	v_lshl_add_u64 v[206:207], s[0:1], 0, v[130:131]
	s_add_i32 s0, s66, s61
	s_ashr_i32 s1, s0, 31
	s_add_u32 s0, s6, s0
	s_addc_u32 s1, s7, s1
	s_add_i32 s67, s31, s27
	global_load_lds_dwordx4 v[206:207], off
	v_lshl_add_u64 v[206:207], s[0:1], 0, v[128:129]
	s_mov_b32 m0, s67
	s_nop 0
	global_load_lds_dwordx4 v[206:207], off
	s_add_i32 m0, s67, 0x2000
	s_add_i32 s67, s61, s19
	v_lshl_add_u64 v[206:207], s[0:1], 0, v[130:131]
	s_add_u32 s0, s4, s67
	s_addc_u32 s1, s5, 0
	global_load_lds_dwordx4 v[206:207], off
	v_lshl_add_u64 v[206:207], s[0:1], 0, v[128:129]
	s_mov_b32 m0, s23
	s_nop 0
	global_load_lds_dwordx4 v[206:207], off
	v_lshl_add_u64 v[206:207], s[0:1], 0, v[130:131]
	s_mov_b32 m0, s24
	s_nop 0
	global_load_lds_dwordx4 v[206:207], off
	s_waitcnt vmcnt(8)
	s_waitcnt lgkmcnt(0)
	s_barrier
	s_waitcnt lgkmcnt(0)
	v_mfma_f32_16x16x32_bf16 v[60:63], v[142:145], v[174:177], v[60:63]
	v_mfma_f32_16x16x32_bf16 v[56:59], v[150:153], v[174:177], v[56:59]
	v_mfma_f32_16x16x32_bf16 v[52:55], v[142:145], v[182:185], v[52:55]
	v_mfma_f32_16x16x32_bf16 v[48:51], v[150:153], v[182:185], v[48:51]
	v_mfma_f32_16x16x32_bf16 v[44:47], v[142:145], v[190:193], v[44:47]
	v_mfma_f32_16x16x32_bf16 v[36:39], v[150:153], v[190:193], v[36:39]
	v_mfma_f32_16x16x32_bf16 v[28:31], v[142:145], v[198:201], v[28:31]
	v_mfma_f32_16x16x32_bf16 v[20:23], v[150:153], v[198:201], v[20:23]
	v_mfma_f32_16x16x32_bf16 v[60:63], v[146:149], v[178:181], v[60:63]
	v_mfma_f32_16x16x32_bf16 v[56:59], v[154:157], v[178:181], v[56:59]
	v_mfma_f32_16x16x32_bf16 v[52:55], v[146:149], v[186:189], v[52:55]
	v_mfma_f32_16x16x32_bf16 v[48:51], v[154:157], v[186:189], v[48:51]
	v_mfma_f32_16x16x32_bf16 v[44:47], v[146:149], v[194:197], v[44:47]
	v_mfma_f32_16x16x32_bf16 v[36:39], v[154:157], v[194:197], v[36:39]
	v_mfma_f32_16x16x32_bf16 v[28:31], v[146:149], v[202:205], v[28:31]
	v_mfma_f32_16x16x32_bf16 v[20:23], v[154:157], v[202:205], v[20:23]
	v_mfma_f32_16x16x32_bf16 v[40:43], v[158:161], v[174:177], v[40:43]
	v_mfma_f32_16x16x32_bf16 v[32:35], v[166:169], v[174:177], v[32:35]
	v_mfma_f32_16x16x32_bf16 v[24:27], v[158:161], v[182:185], v[24:27]
	v_mfma_f32_16x16x32_bf16 v[16:19], v[166:169], v[182:185], v[16:19]
	v_mfma_f32_16x16x32_bf16 v[12:15], v[158:161], v[190:193], v[12:15]
	v_mfma_f32_16x16x32_bf16 v[8:11], v[166:169], v[190:193], v[8:11]
	v_mfma_f32_16x16x32_bf16 v[4:7], v[158:161], v[198:201], v[4:7]
	v_mfma_f32_16x16x32_bf16 v[0:3], v[166:169], v[198:201], v[0:3]
	v_mfma_f32_16x16x32_bf16 v[40:43], v[162:165], v[178:181], v[40:43]
	v_mfma_f32_16x16x32_bf16 v[32:35], v[170:173], v[178:181], v[32:35]
	v_mfma_f32_16x16x32_bf16 v[24:27], v[162:165], v[186:189], v[24:27]
	v_mfma_f32_16x16x32_bf16 v[16:19], v[170:173], v[186:189], v[16:19]
	v_mfma_f32_16x16x32_bf16 v[12:15], v[162:165], v[194:197], v[12:15]
	v_mfma_f32_16x16x32_bf16 v[8:11], v[170:173], v[194:197], v[8:11]
	v_mfma_f32_16x16x32_bf16 v[4:7], v[162:165], v[202:205], v[4:7]
	v_mfma_f32_16x16x32_bf16 v[0:3], v[170:173], v[202:205], v[0:3]
	s_barrier
	s_add_i32 s68, 0, 0x18000
	s_add_i32 s69, 0, 0x1c000
	v_add_u32_e32 v154, s68, v138
	v_add_u32_e32 v170, s69, v138
	ds_read_b128 v[142:145], v154
	ds_read_b128 v[146:149], v154 offset:1024
	ds_read_b128 v[150:153], v154 offset:2048
	ds_read_b128 v[154:157], v154 offset:3072
	ds_read_b128 v[158:161], v170
	ds_read_b128 v[162:165], v170 offset:1024
	ds_read_b128 v[166:169], v170 offset:2048
	ds_read_b128 v[170:173], v170 offset:3072
	s_add_i32 s67, s67, 0x80000
	s_add_u32 s0, s4, s67
	s_addc_u32 s1, s5, 0
	s_mov_b32 m0, s25
	v_lshl_add_u64 v[206:207], s[0:1], 0, v[128:129]
	ds_read_b128 v[174:177], v141 offset:32768
	ds_read_b128 v[178:181], v141 offset:33792
	ds_read_b128 v[182:185], v141 offset:34816
	ds_read_b128 v[186:189], v141 offset:35840
	ds_read_b128 v[190:193], v141 offset:36864
	ds_read_b128 v[194:197], v141 offset:37888
	ds_read_b128 v[198:201], v141 offset:38912
	ds_read_b128 v[202:205], v141 offset:39936
	global_load_lds_dwordx4 v[206:207], off
	v_lshl_add_u64 v[206:207], s[0:1], 0, v[130:131]
	s_mov_b32 m0, s33
	s_nop 0
	global_load_lds_dwordx4 v[206:207], off
	s_waitcnt vmcnt(8)
	s_waitcnt lgkmcnt(0)
	s_barrier
	s_waitcnt lgkmcnt(0)
	v_mfma_f32_16x16x32_bf16 v[124:127], v[142:145], v[174:177], v[124:127]
	v_mfma_f32_16x16x32_bf16 v[120:123], v[150:153], v[174:177], v[120:123]
	v_mfma_f32_16x16x32_bf16 v[116:119], v[142:145], v[182:185], v[116:119]
	v_mfma_f32_16x16x32_bf16 v[112:115], v[150:153], v[182:185], v[112:115]
	v_mfma_f32_16x16x32_bf16 v[108:111], v[142:145], v[190:193], v[108:111]
	v_mfma_f32_16x16x32_bf16 v[100:103], v[150:153], v[190:193], v[100:103]
	v_mfma_f32_16x16x32_bf16 v[92:95], v[142:145], v[198:201], v[92:95]
	v_mfma_f32_16x16x32_bf16 v[84:87], v[150:153], v[198:201], v[84:87]
	v_mfma_f32_16x16x32_bf16 v[124:127], v[146:149], v[178:181], v[124:127]
	v_mfma_f32_16x16x32_bf16 v[120:123], v[154:157], v[178:181], v[120:123]
	v_mfma_f32_16x16x32_bf16 v[116:119], v[146:149], v[186:189], v[116:119]
	v_mfma_f32_16x16x32_bf16 v[112:115], v[154:157], v[186:189], v[112:115]
	v_mfma_f32_16x16x32_bf16 v[108:111], v[146:149], v[194:197], v[108:111]
	v_mfma_f32_16x16x32_bf16 v[100:103], v[154:157], v[194:197], v[100:103]
	v_mfma_f32_16x16x32_bf16 v[92:95], v[146:149], v[202:205], v[92:95]
	v_mfma_f32_16x16x32_bf16 v[84:87], v[154:157], v[202:205], v[84:87]
	v_mfma_f32_16x16x32_bf16 v[104:107], v[158:161], v[174:177], v[104:107]
	v_mfma_f32_16x16x32_bf16 v[96:99], v[166:169], v[174:177], v[96:99]
	v_mfma_f32_16x16x32_bf16 v[88:91], v[158:161], v[182:185], v[88:91]
	v_mfma_f32_16x16x32_bf16 v[80:83], v[166:169], v[182:185], v[80:83]
	v_mfma_f32_16x16x32_bf16 v[76:79], v[158:161], v[190:193], v[76:79]
	v_mfma_f32_16x16x32_bf16 v[72:75], v[166:169], v[190:193], v[72:75]
	v_mfma_f32_16x16x32_bf16 v[68:71], v[158:161], v[198:201], v[68:71]
	v_mfma_f32_16x16x32_bf16 v[64:67], v[166:169], v[198:201], v[64:67]
	v_mfma_f32_16x16x32_bf16 v[104:107], v[162:165], v[178:181], v[104:107]
	v_mfma_f32_16x16x32_bf16 v[96:99], v[170:173], v[178:181], v[96:99]
	v_mfma_f32_16x16x32_bf16 v[88:91], v[162:165], v[186:189], v[88:91]
	v_mfma_f32_16x16x32_bf16 v[80:83], v[170:173], v[186:189], v[80:83]
	v_mfma_f32_16x16x32_bf16 v[76:79], v[162:165], v[194:197], v[76:79]
	v_mfma_f32_16x16x32_bf16 v[72:75], v[170:173], v[194:197], v[72:75]
	v_mfma_f32_16x16x32_bf16 v[68:71], v[162:165], v[202:205], v[68:71]
	v_mfma_f32_16x16x32_bf16 v[64:67], v[170:173], v[202:205], v[64:67]
	s_barrier
; template <class Epi, class Sched, class Hook = NoHook>
; __device__ __forceinline__ void gemm_phase_w(LAS unsigned char* lds, const Sched& S, const Epi& E, int wave_id, const Hook& HK = Hook()) {
;     ...
;         if constexpr (!SEG2) {
;             for (int tt = 0; tt < nt; tt += 2) {
;                 if constexpr (GATHER) { if (tt == nt - 2) {
;                     if (has_next) { gnxt_00 = S.grow_l(nxt, lds, nbuf, R0) + (unsigned)(C0 * 2); gnxt_01 = S.grow_l(nxt, lds, nbuf, R1) + (unsigned)(C1 * 2); gnxt_10 = S.grow_l(nxt, lds, nbuf, 128 + R0) + (unsigned)(C0 * 2); gnxt_11 = S.grow_l(nxt, lds, nbuf, 128 + R1) + (unsigned)(C1 * 2); }
;                     else { gnxt_00 = gcur_00; gnxt_01 = gcur_01; gnxt_10 = gcur_10; gnxt_11 = gcur_11; } } }
;                 PG_TRIP(tt, false, false, false);
;             }
	s_bitset1_b32 s61, 7
	s_add_i32 s0, s61, s60
	s_ashr_i32 s1, s0, 31
	s_add_u32 s0, s6, s0
	s_addc_u32 s1, s7, s1
	s_add_i32 s60, s68, s27
	v_lshl_add_u64 v[206:207], s[0:1], 0, v[128:129]
	s_mov_b32 m0, s60
	ds_read_b128 v[174:177], v141 offset:49152
	ds_read_b128 v[178:181], v141 offset:50176
	ds_read_b128 v[182:185], v141 offset:51200
	ds_read_b128 v[186:189], v141 offset:52224
	ds_read_b128 v[190:193], v141 offset:53248
	ds_read_b128 v[194:197], v141 offset:54272
	ds_read_b128 v[198:201], v141 offset:55296
	ds_read_b128 v[202:205], v141 offset:56320
	global_load_lds_dwordx4 v[206:207], off
	v_lshl_add_u64 v[206:207], s[0:1], 0, v[130:131]
	s_add_i32 s0, s61, s66
	s_add_i32 m0, s60, 0x2000
	s_ashr_i32 s1, s0, 31
	s_add_u32 s0, s6, s0
	s_addc_u32 s1, s7, s1
	s_add_i32 s60, s69, s27
	global_load_lds_dwordx4 v[206:207], off
	v_lshl_add_u64 v[206:207], s[0:1], 0, v[128:129]
	s_mov_b32 m0, s60
	s_add_i32 s61, s61, s19
	global_load_lds_dwordx4 v[206:207], off
	s_add_i32 m0, s60, 0x2000
	v_lshl_add_u64 v[206:207], s[0:1], 0, v[130:131]
	s_add_u32 s0, s4, s61
	s_addc_u32 s1, s5, 0
	global_load_lds_dwordx4 v[206:207], off
	v_lshl_add_u64 v[206:207], s[0:1], 0, v[128:129]
	s_mov_b32 m0, s34
	s_nop 0
	global_load_lds_dwordx4 v[206:207], off
	v_lshl_add_u64 v[206:207], s[0:1], 0, v[130:131]
	s_mov_b32 m0, s35
	s_nop 0
	global_load_lds_dwordx4 v[206:207], off
	s_waitcnt vmcnt(8)
	s_waitcnt lgkmcnt(0)
	s_barrier
	s_waitcnt lgkmcnt(0)
	v_mfma_f32_16x16x32_bf16 v[60:63], v[142:145], v[174:177], v[60:63]
	v_mfma_f32_16x16x32_bf16 v[56:59], v[150:153], v[174:177], v[56:59]
	v_mfma_f32_16x16x32_bf16 v[52:55], v[142:145], v[182:185], v[52:55]
	v_mfma_f32_16x16x32_bf16 v[48:51], v[150:153], v[182:185], v[48:51]
	v_mfma_f32_16x16x32_bf16 v[44:47], v[142:145], v[190:193], v[44:47]
	v_mfma_f32_16x16x32_bf16 v[36:39], v[150:153], v[190:193], v[36:39]
	v_mfma_f32_16x16x32_bf16 v[28:31], v[142:145], v[198:201], v[28:31]
	v_mfma_f32_16x16x32_bf16 v[20:23], v[150:153], v[198:201], v[20:23]
	v_mfma_f32_16x16x32_bf16 v[60:63], v[146:149], v[178:181], v[60:63]
	v_mfma_f32_16x16x32_bf16 v[56:59], v[154:157], v[178:181], v[56:59]
	v_mfma_f32_16x16x32_bf16 v[52:55], v[146:149], v[186:189], v[52:55]
	v_mfma_f32_16x16x32_bf16 v[48:51], v[154:157], v[186:189], v[48:51]
	v_mfma_f32_16x16x32_bf16 v[44:47], v[146:149], v[194:197], v[44:47]
	v_mfma_f32_16x16x32_bf16 v[36:39], v[154:157], v[194:197], v[36:39]
	v_mfma_f32_16x16x32_bf16 v[28:31], v[146:149], v[202:205], v[28:31]
	v_mfma_f32_16x16x32_bf16 v[20:23], v[154:157], v[202:205], v[20:23]
	v_mfma_f32_16x16x32_bf16 v[40:43], v[158:161], v[174:177], v[40:43]
	v_mfma_f32_16x16x32_bf16 v[32:35], v[166:169], v[174:177], v[32:35]
	v_mfma_f32_16x16x32_bf16 v[24:27], v[158:161], v[182:185], v[24:27]
	v_mfma_f32_16x16x32_bf16 v[16:19], v[166:169], v[182:185], v[16:19]
	v_mfma_f32_16x16x32_bf16 v[12:15], v[158:161], v[190:193], v[12:15]
	v_mfma_f32_16x16x32_bf16 v[8:11], v[166:169], v[190:193], v[8:11]
	v_mfma_f32_16x16x32_bf16 v[4:7], v[158:161], v[198:201], v[4:7]
	v_mfma_f32_16x16x32_bf16 v[0:3], v[166:169], v[198:201], v[0:3]
	v_mfma_f32_16x16x32_bf16 v[40:43], v[162:165], v[178:181], v[40:43]
	v_mfma_f32_16x16x32_bf16 v[32:35], v[170:173], v[178:181], v[32:35]
	v_mfma_f32_16x16x32_bf16 v[24:27], v[162:165], v[186:189], v[24:27]
	v_mfma_f32_16x16x32_bf16 v[16:19], v[170:173], v[186:189], v[16:19]
	v_mfma_f32_16x16x32_bf16 v[12:15], v[162:165], v[194:197], v[12:15]
	v_mfma_f32_16x16x32_bf16 v[8:11], v[170:173], v[194:197], v[8:11]
	v_mfma_f32_16x16x32_bf16 v[4:7], v[162:165], v[202:205], v[4:7]
	v_mfma_f32_16x16x32_bf16 v[0:3], v[170:173], v[202:205], v[0:3]
	s_addk_i32 s10, 0x100
	s_add_i32 s18, s18, 2
	s_cmp_gt_u32 s18, 29
	s_barrier
	s_cbranch_scc0 .LBB0_386
	s_and_b64 vcc, exec, s[14:15]
	s_cbranch_vccz .LBB0_389
	s_barrier

.LBB0_654:
	ds_read_b128 v[116:119], v157
	ds_read_b128 v[120:123], v157 offset:1024
	ds_read_b128 v[128:131], v157 offset:2048
	ds_read_b128 v[132:135], v157 offset:3072
	ds_read_b128 v[150:153], v158
	ds_read_b128 v[160:163], v158 offset:1024
	ds_read_b128 v[164:167], v158 offset:2048
	ds_read_b128 v[168:171], v158 offset:3072
	s_add_i32 s40, s39, s18
	s_add_u32 s42, s4, s40
	s_addc_u32 s43, s5, 0
	s_add_i32 m0, s23, 0xc000
	s_add_i32 s44, s23, 0xe000
	s_add_i32 s45, s18, 0xfff80080
	s_cmp_eq_u32 s19, 28
	s_cselect_b32 s40, s35, s39
	s_cselect_b32 s41, s34, s38
	v_lshl_add_u64 v[204:205], s[42:43], 0, v[144:145]
	ds_read_b128 v[172:175], v159
	ds_read_b128 v[176:179], v159 offset:1024
	ds_read_b128 v[180:183], v159 offset:2048
	ds_read_b128 v[184:187], v159 offset:3072
	ds_read_b128 v[188:191], v159 offset:4096
	ds_read_b128 v[192:195], v159 offset:5120
	ds_read_b128 v[196:199], v159 offset:6144
	ds_read_b128 v[200:203], v159 offset:7168
	global_load_lds_dwordx4 v[204:205], off
	v_lshl_add_u64 v[204:205], s[42:43], 0, v[146:147]
	s_mov_b32 m0, s44
	s_nop 0
	global_load_lds_dwordx4 v[204:205], off
	s_waitcnt vmcnt(8)
	s_waitcnt lgkmcnt(0)
	s_barrier
	s_waitcnt lgkmcnt(0)
	v_mfma_f32_16x16x32_bf16 v[140:143], v[116:119], v[172:175], v[140:143]
	v_mfma_f32_16x16x32_bf16 v[136:139], v[128:131], v[172:175], v[136:139]
	v_mfma_f32_16x16x32_bf16 v[112:115], v[116:119], v[180:183], v[112:115]
	v_mfma_f32_16x16x32_bf16 v[104:107], v[128:131], v[180:183], v[104:107]
	v_mfma_f32_16x16x32_bf16 v[96:99], v[116:119], v[188:191], v[96:99]
	v_mfma_f32_16x16x32_bf16 v[88:91], v[128:131], v[188:191], v[88:91]
	v_mfma_f32_16x16x32_bf16 v[80:83], v[116:119], v[196:199], v[80:83]
	v_mfma_f32_16x16x32_bf16 v[72:75], v[128:131], v[196:199], v[72:75]
	v_mfma_f32_16x16x32_bf16 v[140:143], v[120:123], v[176:179], v[140:143]
	v_mfma_f32_16x16x32_bf16 v[136:139], v[132:135], v[176:179], v[136:139]
	v_mfma_f32_16x16x32_bf16 v[112:115], v[120:123], v[184:187], v[112:115]
	v_mfma_f32_16x16x32_bf16 v[104:107], v[132:135], v[184:187], v[104:107]
	v_mfma_f32_16x16x32_bf16 v[96:99], v[120:123], v[192:195], v[96:99]
	v_mfma_f32_16x16x32_bf16 v[88:91], v[132:135], v[192:195], v[88:91]
	v_mfma_f32_16x16x32_bf16 v[80:83], v[120:123], v[200:203], v[80:83]
	v_mfma_f32_16x16x32_bf16 v[72:75], v[132:135], v[200:203], v[72:75]
	v_mfma_f32_16x16x32_bf16 v[124:127], v[150:153], v[172:175], v[124:127]
	v_mfma_f32_16x16x32_bf16 v[108:111], v[164:167], v[172:175], v[108:111]
	v_mfma_f32_16x16x32_bf16 v[100:103], v[150:153], v[180:183], v[100:103]
	v_mfma_f32_16x16x32_bf16 v[92:95], v[164:167], v[180:183], v[92:95]
	v_mfma_f32_16x16x32_bf16 v[84:87], v[150:153], v[188:191], v[84:87]
	v_mfma_f32_16x16x32_bf16 v[76:79], v[164:167], v[188:191], v[76:79]
	v_mfma_f32_16x16x32_bf16 v[68:71], v[150:153], v[196:199], v[68:71]
	v_mfma_f32_16x16x32_bf16 v[64:67], v[164:167], v[196:199], v[64:67]
	v_mfma_f32_16x16x32_bf16 v[124:127], v[160:163], v[176:179], v[124:127]
	v_mfma_f32_16x16x32_bf16 v[108:111], v[168:171], v[176:179], v[108:111]
	v_mfma_f32_16x16x32_bf16 v[100:103], v[160:163], v[184:187], v[100:103]
	v_mfma_f32_16x16x32_bf16 v[92:95], v[168:171], v[184:187], v[92:95]
	v_mfma_f32_16x16x32_bf16 v[84:87], v[160:163], v[192:195], v[84:87]
	v_mfma_f32_16x16x32_bf16 v[76:79], v[168:171], v[192:195], v[76:79]
	v_mfma_f32_16x16x32_bf16 v[68:71], v[160:163], v[200:203], v[68:71]
	v_mfma_f32_16x16x32_bf16 v[64:67], v[168:171], v[200:203], v[64:67]
	s_barrier
	s_cselect_b32 s44, 0, s45
	s_add_i32 s42, s44, s41
	s_ashr_i32 s43, s42, 31
	s_add_u32 s42, s20, s42
	s_addc_u32 s43, s21, s43
	s_add_i32 s45, s29, s22
	v_lshl_add_u64 v[204:205], s[42:43], 0, v[144:145]
	s_mov_b32 m0, s45
	ds_read_b128 v[172:175], v159 offset:16384
	ds_read_b128 v[176:179], v159 offset:17408
	ds_read_b128 v[180:183], v159 offset:18432
	ds_read_b128 v[184:187], v159 offset:19456
	ds_read_b128 v[188:191], v159 offset:20480
	ds_read_b128 v[192:195], v159 offset:21504
	ds_read_b128 v[196:199], v159 offset:22528
	ds_read_b128 v[200:203], v159 offset:23552
	global_load_lds_dwordx4 v[204:205], off
	s_add_i32 m0, s45, 0x2000
	s_add_i32 s45, s41, 0x80000
	v_lshl_add_u64 v[204:205], s[42:43], 0, v[146:147]
	s_add_i32 s42, s45, s44
	s_ashr_i32 s43, s42, 31
	s_add_u32 s42, s20, s42
	s_addc_u32 s43, s21, s43
	s_add_i32 s58, s30, s22
	global_load_lds_dwordx4 v[204:205], off
	v_lshl_add_u64 v[204:205], s[42:43], 0, v[144:145]
	s_mov_b32 m0, s58
	s_nop 0
	global_load_lds_dwordx4 v[204:205], off
	s_add_i32 m0, s58, 0x2000
	s_add_i32 s58, s44, s40
	v_lshl_add_u64 v[204:205], s[42:43], 0, v[146:147]
	s_add_u32 s42, s4, s58
	s_addc_u32 s43, s5, 0
	global_load_lds_dwordx4 v[204:205], off
	v_lshl_add_u64 v[204:205], s[42:43], 0, v[144:145]
	s_mov_b32 m0, s23
	s_nop 0
	global_load_lds_dwordx4 v[204:205], off
	v_lshl_add_u64 v[204:205], s[42:43], 0, v[146:147]
	s_mov_b32 m0, s24
	s_nop 0
	global_load_lds_dwordx4 v[204:205], off
	s_waitcnt vmcnt(8)
	s_waitcnt lgkmcnt(0)
	s_barrier
	s_waitcnt lgkmcnt(0)
	v_mfma_f32_16x16x32_bf16 v[60:63], v[116:119], v[172:175], v[60:63]
	v_mfma_f32_16x16x32_bf16 v[56:59], v[128:131], v[172:175], v[56:59]
	v_mfma_f32_16x16x32_bf16 v[48:51], v[116:119], v[180:183], v[48:51]
	v_mfma_f32_16x16x32_bf16 v[40:43], v[128:131], v[180:183], v[40:43]
	v_mfma_f32_16x16x32_bf16 v[32:35], v[116:119], v[188:191], v[32:35]
	v_mfma_f32_16x16x32_bf16 v[24:27], v[128:131], v[188:191], v[24:27]
	v_mfma_f32_16x16x32_bf16 v[16:19], v[116:119], v[196:199], v[16:19]
	v_mfma_f32_16x16x32_bf16 v[8:11], v[128:131], v[196:199], v[8:11]
	v_mfma_f32_16x16x32_bf16 v[60:63], v[120:123], v[176:179], v[60:63]
	v_mfma_f32_16x16x32_bf16 v[56:59], v[132:135], v[176:179], v[56:59]
	v_mfma_f32_16x16x32_bf16 v[48:51], v[120:123], v[184:187], v[48:51]
	v_mfma_f32_16x16x32_bf16 v[40:43], v[132:135], v[184:187], v[40:43]
	v_mfma_f32_16x16x32_bf16 v[32:35], v[120:123], v[192:195], v[32:35]
	v_mfma_f32_16x16x32_bf16 v[24:27], v[132:135], v[192:195], v[24:27]
	v_mfma_f32_16x16x32_bf16 v[16:19], v[120:123], v[200:203], v[16:19]
	v_mfma_f32_16x16x32_bf16 v[8:11], v[132:135], v[200:203], v[8:11]
	v_mfma_f32_16x16x32_bf16 v[52:55], v[150:153], v[172:175], v[52:55]
	v_mfma_f32_16x16x32_bf16 v[44:47], v[164:167], v[172:175], v[44:47]
	v_mfma_f32_16x16x32_bf16 v[36:39], v[150:153], v[180:183], v[36:39]
	v_mfma_f32_16x16x32_bf16 v[28:31], v[164:167], v[180:183], v[28:31]
	v_mfma_f32_16x16x32_bf16 v[20:23], v[150:153], v[188:191], v[20:23]
	v_mfma_f32_16x16x32_bf16 v[12:15], v[164:167], v[188:191], v[12:15]
	v_mfma_f32_16x16x32_bf16 v[4:7], v[150:153], v[196:199], v[4:7]
	v_mfma_f32_16x16x32_bf16 v[0:3], v[164:167], v[196:199], v[0:3]
	v_mfma_f32_16x16x32_bf16 v[52:55], v[160:163], v[176:179], v[52:55]
	v_mfma_f32_16x16x32_bf16 v[44:47], v[168:171], v[176:179], v[44:47]
	v_mfma_f32_16x16x32_bf16 v[36:39], v[160:163], v[184:187], v[36:39]
	v_mfma_f32_16x16x32_bf16 v[28:31], v[168:171], v[184:187], v[28:31]
	v_mfma_f32_16x16x32_bf16 v[20:23], v[160:163], v[192:195], v[20:23]
	v_mfma_f32_16x16x32_bf16 v[12:15], v[168:171], v[192:195], v[12:15]
	v_mfma_f32_16x16x32_bf16 v[4:7], v[160:163], v[200:203], v[4:7]
	v_mfma_f32_16x16x32_bf16 v[0:3], v[168:171], v[200:203], v[0:3]
	s_barrier
	s_add_i32 s59, 0, 0x18000
	s_add_i32 s60, 0, 0x1c000
	v_add_u32_e32 v132, s59, v155
	v_add_u32_e32 v168, s60, v155
	ds_read_b128 v[116:119], v132
	ds_read_b128 v[120:123], v132 offset:1024
	ds_read_b128 v[128:131], v132 offset:2048
	ds_read_b128 v[132:135], v132 offset:3072
	ds_read_b128 v[150:153], v168
	ds_read_b128 v[160:163], v168 offset:1024
	ds_read_b128 v[164:167], v168 offset:2048
	ds_read_b128 v[168:171], v168 offset:3072
	s_add_i32 s58, s58, 0x80000
	s_add_u32 s42, s4, s58
	s_addc_u32 s43, s5, 0
	s_mov_b32 m0, s25
	v_lshl_add_u64 v[204:205], s[42:43], 0, v[144:145]
	ds_read_b128 v[172:175], v159 offset:32768
	ds_read_b128 v[176:179], v159 offset:33792
	ds_read_b128 v[180:183], v159 offset:34816
	ds_read_b128 v[184:187], v159 offset:35840
	ds_read_b128 v[188:191], v159 offset:36864
	ds_read_b128 v[192:195], v159 offset:37888
	ds_read_b128 v[196:199], v159 offset:38912
	ds_read_b128 v[200:203], v159 offset:39936
	global_load_lds_dwordx4 v[204:205], off
	v_lshl_add_u64 v[204:205], s[42:43], 0, v[146:147]
	s_mov_b32 m0, s26
	s_nop 0
	global_load_lds_dwordx4 v[204:205], off
	s_waitcnt vmcnt(8)
	s_waitcnt lgkmcnt(0)
	s_barrier
	s_waitcnt lgkmcnt(0)
	v_mfma_f32_16x16x32_bf16 v[140:143], v[116:119], v[172:175], v[140:143]
	v_mfma_f32_16x16x32_bf16 v[136:139], v[128:131], v[172:175], v[136:139]
	v_mfma_f32_16x16x32_bf16 v[112:115], v[116:119], v[180:183], v[112:115]
	v_mfma_f32_16x16x32_bf16 v[104:107], v[128:131], v[180:183], v[104:107]
	v_mfma_f32_16x16x32_bf16 v[96:99], v[116:119], v[188:191], v[96:99]
	v_mfma_f32_16x16x32_bf16 v[88:91], v[128:131], v[188:191], v[88:91]
	v_mfma_f32_16x16x32_bf16 v[80:83], v[116:119], v[196:199], v[80:83]
	v_mfma_f32_16x16x32_bf16 v[72:75], v[128:131], v[196:199], v[72:75]
	v_mfma_f32_16x16x32_bf16 v[140:143], v[120:123], v[176:179], v[140:143]
	v_mfma_f32_16x16x32_bf16 v[136:139], v[132:135], v[176:179], v[136:139]
	v_mfma_f32_16x16x32_bf16 v[112:115], v[120:123], v[184:187], v[112:115]
	v_mfma_f32_16x16x32_bf16 v[104:107], v[132:135], v[184:187], v[104:107]
	v_mfma_f32_16x16x32_bf16 v[96:99], v[120:123], v[192:195], v[96:99]
	v_mfma_f32_16x16x32_bf16 v[88:91], v[132:135], v[192:195], v[88:91]
	v_mfma_f32_16x16x32_bf16 v[80:83], v[120:123], v[200:203], v[80:83]
	v_mfma_f32_16x16x32_bf16 v[72:75], v[132:135], v[200:203], v[72:75]
	v_mfma_f32_16x16x32_bf16 v[124:127], v[150:153], v[172:175], v[124:127]
	v_mfma_f32_16x16x32_bf16 v[108:111], v[164:167], v[172:175], v[108:111]
	v_mfma_f32_16x16x32_bf16 v[100:103], v[150:153], v[180:183], v[100:103]
	v_mfma_f32_16x16x32_bf16 v[92:95], v[164:167], v[180:183], v[92:95]
	v_mfma_f32_16x16x32_bf16 v[84:87], v[150:153], v[188:191], v[84:87]
	v_mfma_f32_16x16x32_bf16 v[76:79], v[164:167], v[188:191], v[76:79]
	v_mfma_f32_16x16x32_bf16 v[68:71], v[150:153], v[196:199], v[68:71]
	v_mfma_f32_16x16x32_bf16 v[64:67], v[164:167], v[196:199], v[64:67]
	v_mfma_f32_16x16x32_bf16 v[124:127], v[160:163], v[176:179], v[124:127]
	v_mfma_f32_16x16x32_bf16 v[108:111], v[168:171], v[176:179], v[108:111]
	v_mfma_f32_16x16x32_bf16 v[100:103], v[160:163], v[184:187], v[100:103]
	v_mfma_f32_16x16x32_bf16 v[92:95], v[168:171], v[184:187], v[92:95]
	v_mfma_f32_16x16x32_bf16 v[84:87], v[160:163], v[192:195], v[84:87]
	v_mfma_f32_16x16x32_bf16 v[76:79], v[168:171], v[192:195], v[76:79]
	v_mfma_f32_16x16x32_bf16 v[68:71], v[160:163], v[200:203], v[68:71]
	v_mfma_f32_16x16x32_bf16 v[64:67], v[168:171], v[200:203], v[64:67]
	s_barrier
; template <class Epi, class Sched, class Hook = NoHook>
; __device__ __forceinline__ void gemm_phase_w(LAS unsigned char* lds, const Sched& S, const Epi& E, int wave_id, const Hook& HK = Hook()) {
;     ...
;         if constexpr (!SEG2) {
;             for (int tt = 0; tt < nt; tt += 2) {
;                 if constexpr (GATHER) { if (tt == nt - 2) {
;                     if (has_next) { gnxt_00 = S.grow_l(nxt, lds, nbuf, R0) + (unsigned)(C0 * 2); gnxt_01 = S.grow_l(nxt, lds, nbuf, R1) + (unsigned)(C1 * 2); gnxt_10 = S.grow_l(nxt, lds, nbuf, 128 + R0) + (unsigned)(C0 * 2); gnxt_11 = S.grow_l(nxt, lds, nbuf, 128 + R1) + (unsigned)(C1 * 2); }
;                     else { gnxt_00 = gcur_00; gnxt_01 = gcur_01; gnxt_10 = gcur_10; gnxt_11 = gcur_11; } } }
;                 PG_TRIP(tt, false, false, false);
;             }
	s_bitset1_b32 s44, 7
	s_add_i32 s41, s44, s41
	s_ashr_i32 s43, s41, 31
	s_add_u32 s42, s20, s41
	s_addc_u32 s43, s21, s43
	s_add_i32 s41, s59, s22
	v_lshl_add_u64 v[204:205], s[42:43], 0, v[144:145]
	s_mov_b32 m0, s41
	ds_read_b128 v[172:175], v159 offset:49152
	ds_read_b128 v[176:179], v159 offset:50176
	ds_read_b128 v[180:183], v159 offset:51200
	ds_read_b128 v[184:187], v159 offset:52224
	ds_read_b128 v[188:191], v159 offset:53248
	ds_read_b128 v[192:195], v159 offset:54272
	ds_read_b128 v[196:199], v159 offset:55296
	ds_read_b128 v[200:203], v159 offset:56320
	global_load_lds_dwordx4 v[204:205], off
	s_add_i32 m0, s41, 0x2000
	s_add_i32 s41, s44, s45
	v_lshl_add_u64 v[204:205], s[42:43], 0, v[146:147]
	s_ashr_i32 s43, s41, 31
	s_add_u32 s42, s20, s41
	s_addc_u32 s43, s21, s43
	s_add_i32 s41, s60, s22
	global_load_lds_dwordx4 v[204:205], off
	v_lshl_add_u64 v[204:205], s[42:43], 0, v[144:145]
	s_mov_b32 m0, s41
	s_add_i32 s44, s44, s40
	global_load_lds_dwordx4 v[204:205], off
	s_add_i32 m0, s41, 0x2000
	s_add_u32 s40, s4, s44
	v_lshl_add_u64 v[204:205], s[42:43], 0, v[146:147]
	s_addc_u32 s41, s5, 0
	global_load_lds_dwordx4 v[204:205], off
	v_lshl_add_u64 v[204:205], s[40:41], 0, v[144:145]
	s_mov_b32 m0, s28
	s_nop 0
	global_load_lds_dwordx4 v[204:205], off
	v_lshl_add_u64 v[204:205], s[40:41], 0, v[146:147]
	s_mov_b32 m0, s6
	s_nop 0
	global_load_lds_dwordx4 v[204:205], off
	s_waitcnt vmcnt(8)
	s_waitcnt lgkmcnt(0)
	s_barrier
	s_waitcnt lgkmcnt(0)
	v_mfma_f32_16x16x32_bf16 v[60:63], v[116:119], v[172:175], v[60:63]
	v_mfma_f32_16x16x32_bf16 v[56:59], v[128:131], v[172:175], v[56:59]
	v_mfma_f32_16x16x32_bf16 v[48:51], v[116:119], v[180:183], v[48:51]
	v_mfma_f32_16x16x32_bf16 v[40:43], v[128:131], v[180:183], v[40:43]
	v_mfma_f32_16x16x32_bf16 v[32:35], v[116:119], v[188:191], v[32:35]
	v_mfma_f32_16x16x32_bf16 v[24:27], v[128:131], v[188:191], v[24:27]
	v_mfma_f32_16x16x32_bf16 v[16:19], v[116:119], v[196:199], v[16:19]
	v_mfma_f32_16x16x32_bf16 v[8:11], v[128:131], v[196:199], v[8:11]
	v_mfma_f32_16x16x32_bf16 v[60:63], v[120:123], v[176:179], v[60:63]
	v_mfma_f32_16x16x32_bf16 v[56:59], v[132:135], v[176:179], v[56:59]
	v_mfma_f32_16x16x32_bf16 v[48:51], v[120:123], v[184:187], v[48:51]
	v_mfma_f32_16x16x32_bf16 v[40:43], v[132:135], v[184:187], v[40:43]
	v_mfma_f32_16x16x32_bf16 v[32:35], v[120:123], v[192:195], v[32:35]
	v_mfma_f32_16x16x32_bf16 v[24:27], v[132:135], v[192:195], v[24:27]
	v_mfma_f32_16x16x32_bf16 v[16:19], v[120:123], v[200:203], v[16:19]
	v_mfma_f32_16x16x32_bf16 v[8:11], v[132:135], v[200:203], v[8:11]
	v_mfma_f32_16x16x32_bf16 v[52:55], v[150:153], v[172:175], v[52:55]
	v_mfma_f32_16x16x32_bf16 v[44:47], v[164:167], v[172:175], v[44:47]
	v_mfma_f32_16x16x32_bf16 v[36:39], v[150:153], v[180:183], v[36:39]
	v_mfma_f32_16x16x32_bf16 v[28:31], v[164:167], v[180:183], v[28:31]
	v_mfma_f32_16x16x32_bf16 v[20:23], v[150:153], v[188:191], v[20:23]
	v_mfma_f32_16x16x32_bf16 v[12:15], v[164:167], v[188:191], v[12:15]
	v_mfma_f32_16x16x32_bf16 v[4:7], v[150:153], v[196:199], v[4:7]
	v_mfma_f32_16x16x32_bf16 v[0:3], v[164:167], v[196:199], v[0:3]
	v_mfma_f32_16x16x32_bf16 v[52:55], v[160:163], v[176:179], v[52:55]
	v_mfma_f32_16x16x32_bf16 v[44:47], v[168:171], v[176:179], v[44:47]
	v_mfma_f32_16x16x32_bf16 v[36:39], v[160:163], v[184:187], v[36:39]
	v_mfma_f32_16x16x32_bf16 v[28:31], v[168:171], v[184:187], v[28:31]
	v_mfma_f32_16x16x32_bf16 v[20:23], v[160:163], v[192:195], v[20:23]
	v_mfma_f32_16x16x32_bf16 v[12:15], v[168:171], v[192:195], v[12:15]
	v_mfma_f32_16x16x32_bf16 v[4:7], v[160:163], v[200:203], v[4:7]
	v_mfma_f32_16x16x32_bf16 v[0:3], v[168:171], v[200:203], v[0:3]
	s_addk_i32 s18, 0x100
	s_add_i32 s19, s19, 2
	s_cmp_gt_u32 s19, 29
	s_barrier
	s_cbranch_scc0 .LBB0_654
	s_and_b64 vcc, exec, s[14:15]
	s_cbranch_vccz .LBB0_657
	s_barrier

.LBB0_827:
	v_add_u32_e32 v147, s73, v166
	ds_read_b128 v[186:189], v147
	ds_read_b128 v[190:193], v147 offset:1024
	ds_read_b128 v[194:197], v147 offset:2048
	ds_read_b128 v[198:201], v147 offset:3072
	v_add_u32_e32 v147, s74, v166
	ds_read_b128 v[202:205], v147
	ds_read_b128 v[206:209], v147 offset:1024
	ds_read_b128 v[210:213], v147 offset:2048
	ds_read_b128 v[214:217], v147 offset:3072
	v_lshl_add_u64 v[250:251], s[38:39], 0, v[130:131]
	s_add_i32 m0, s62, 0xc000
	ds_read_b128 v[218:221], v182
	ds_read_b128 v[222:225], v182 offset:1024
	ds_read_b128 v[226:229], v182 offset:2048
	ds_read_b128 v[230:233], v182 offset:3072
	ds_read_b128 v[234:237], v182 offset:4096
	ds_read_b128 v[238:241], v182 offset:5120
	ds_read_b128 v[242:245], v182 offset:6144
	ds_read_b128 v[246:249], v182 offset:7168
	global_load_lds_dwordx4 v[250:251], off
	v_lshl_add_u64 v[250:251], s[38:39], 0, v[132:133]
	s_add_i32 m0, s62, 0xe000
	s_nop 0
	global_load_lds_dwordx4 v[250:251], off
	s_waitcnt vmcnt(8)
	s_waitcnt lgkmcnt(0)
	s_barrier
	s_waitcnt lgkmcnt(0)
	v_mfma_f32_16x16x32_bf16 v[124:127], v[186:189], v[218:221], v[124:127]
	v_mfma_f32_16x16x32_bf16 v[120:123], v[194:197], v[218:221], v[120:123]
	v_mfma_f32_16x16x32_bf16 v[108:111], v[186:189], v[226:229], v[108:111]
	v_mfma_f32_16x16x32_bf16 v[104:107], v[194:197], v[226:229], v[104:107]
	v_mfma_f32_16x16x32_bf16 v[92:95], v[186:189], v[234:237], v[92:95]
	v_mfma_f32_16x16x32_bf16 v[88:91], v[194:197], v[234:237], v[88:91]
	v_mfma_f32_16x16x32_bf16 v[76:79], v[186:189], v[242:245], v[76:79]
	v_mfma_f32_16x16x32_bf16 v[72:75], v[194:197], v[242:245], v[72:75]
	v_mfma_f32_16x16x32_bf16 v[124:127], v[190:193], v[222:225], v[124:127]
	v_mfma_f32_16x16x32_bf16 v[120:123], v[198:201], v[222:225], v[120:123]
	v_mfma_f32_16x16x32_bf16 v[108:111], v[190:193], v[230:233], v[108:111]
	v_mfma_f32_16x16x32_bf16 v[104:107], v[198:201], v[230:233], v[104:107]
	v_mfma_f32_16x16x32_bf16 v[92:95], v[190:193], v[238:241], v[92:95]
	v_mfma_f32_16x16x32_bf16 v[88:91], v[198:201], v[238:241], v[88:91]
	v_mfma_f32_16x16x32_bf16 v[76:79], v[190:193], v[246:249], v[76:79]
	v_mfma_f32_16x16x32_bf16 v[72:75], v[198:201], v[246:249], v[72:75]
	v_mfma_f32_16x16x32_bf16 v[116:119], v[202:205], v[218:221], v[116:119]
	v_mfma_f32_16x16x32_bf16 v[112:115], v[210:213], v[218:221], v[112:115]
	v_mfma_f32_16x16x32_bf16 v[100:103], v[202:205], v[226:229], v[100:103]
	v_mfma_f32_16x16x32_bf16 v[96:99], v[210:213], v[226:229], v[96:99]
	v_mfma_f32_16x16x32_bf16 v[84:87], v[202:205], v[234:237], v[84:87]
	v_mfma_f32_16x16x32_bf16 v[80:83], v[210:213], v[234:237], v[80:83]
	v_mfma_f32_16x16x32_bf16 v[68:71], v[202:205], v[242:245], v[68:71]
	v_mfma_f32_16x16x32_bf16 v[64:67], v[210:213], v[242:245], v[64:67]
	v_mfma_f32_16x16x32_bf16 v[116:119], v[206:209], v[222:225], v[116:119]
	v_mfma_f32_16x16x32_bf16 v[112:115], v[214:217], v[222:225], v[112:115]
	v_mfma_f32_16x16x32_bf16 v[100:103], v[206:209], v[230:233], v[100:103]
	v_mfma_f32_16x16x32_bf16 v[96:99], v[214:217], v[230:233], v[96:99]
	v_mfma_f32_16x16x32_bf16 v[84:87], v[206:209], v[238:241], v[84:87]
	v_mfma_f32_16x16x32_bf16 v[80:83], v[214:217], v[238:241], v[80:83]
	v_mfma_f32_16x16x32_bf16 v[68:71], v[206:209], v[246:249], v[68:71]
	v_mfma_f32_16x16x32_bf16 v[64:67], v[214:217], v[246:249], v[64:67]
	s_barrier
	s_and_b64 s[40:41], s[40:41], exec
	s_cselect_b32 s22, 0, s97
	s_add_i32 s48, vcc_lo, s22
	s_ashr_i32 s41, s48, 31
	s_add_u32 s40, s16, s48
	s_addc_u32 s41, s17, s41
	s_add_i32 s49, s73, s44
	v_lshl_add_u64 v[250:251], s[40:41], 0, v[136:137]
	s_mov_b32 m0, s49
	s_add_i32 s48, s48, 0x80000
	ds_read_b128 v[218:221], v182 offset:16384
	ds_read_b128 v[222:225], v182 offset:17408
	ds_read_b128 v[226:229], v182 offset:18432
	ds_read_b128 v[230:233], v182 offset:19456
	ds_read_b128 v[234:237], v182 offset:20480
	ds_read_b128 v[238:241], v182 offset:21504
	ds_read_b128 v[242:245], v182 offset:22528
	ds_read_b128 v[246:249], v182 offset:23552
	global_load_lds_dwordx4 v[250:251], off
	v_lshl_add_u64 v[250:251], s[40:41], 0, v[138:139]
	s_add_i32 m0, s49, 0x2000
	s_ashr_i32 s41, s48, 31
	s_add_u32 s40, s16, s48
	s_addc_u32 s41, s17, s41
	s_add_i32 s48, s74, s44
	global_load_lds_dwordx4 v[250:251], off
	v_lshl_add_u64 v[250:251], s[40:41], 0, v[136:137]
	s_mov_b32 m0, s48
	v_mov_b32_e32 v147, v141
	global_load_lds_dwordx4 v[250:251], off
	s_add_i32 m0, s48, 0x2000
	v_lshl_add_u64 v[250:251], s[40:41], 0, v[138:139]
	s_add_u32 s40, s14, s22
	global_load_lds_dwordx4 v[250:251], off
	s_addc_u32 s41, s15, 0
	s_mov_b32 m0, s62
	s_nop 0
	global_load_lds_dwordx4 v140, s[40:41]
	s_mov_b32 m0, s63
	s_nop 0
	global_load_lds_dwordx4 v146, s[40:41]
	s_waitcnt vmcnt(8)
	s_waitcnt lgkmcnt(0)
	s_barrier
	s_waitcnt lgkmcnt(0)
	v_mfma_f32_16x16x32_bf16 v[60:63], v[186:189], v[218:221], v[60:63]
	v_mfma_f32_16x16x32_bf16 v[56:59], v[194:197], v[218:221], v[56:59]
	v_mfma_f32_16x16x32_bf16 v[44:47], v[186:189], v[226:229], v[44:47]
	v_mfma_f32_16x16x32_bf16 v[40:43], v[194:197], v[226:229], v[40:43]
	v_mfma_f32_16x16x32_bf16 v[28:31], v[186:189], v[234:237], v[28:31]
	v_mfma_f32_16x16x32_bf16 v[24:27], v[194:197], v[234:237], v[24:27]
	v_mfma_f32_16x16x32_bf16 v[12:15], v[186:189], v[242:245], v[12:15]
	v_mfma_f32_16x16x32_bf16 v[8:11], v[194:197], v[242:245], v[8:11]
	v_mfma_f32_16x16x32_bf16 v[60:63], v[190:193], v[222:225], v[60:63]
	v_mfma_f32_16x16x32_bf16 v[56:59], v[198:201], v[222:225], v[56:59]
	v_mfma_f32_16x16x32_bf16 v[44:47], v[190:193], v[230:233], v[44:47]
	v_mfma_f32_16x16x32_bf16 v[40:43], v[198:201], v[230:233], v[40:43]
	v_mfma_f32_16x16x32_bf16 v[28:31], v[190:193], v[238:241], v[28:31]
	v_mfma_f32_16x16x32_bf16 v[24:27], v[198:201], v[238:241], v[24:27]
	v_mfma_f32_16x16x32_bf16 v[12:15], v[190:193], v[246:249], v[12:15]
	v_mfma_f32_16x16x32_bf16 v[8:11], v[198:201], v[246:249], v[8:11]
	v_mfma_f32_16x16x32_bf16 v[52:55], v[202:205], v[218:221], v[52:55]
	v_mfma_f32_16x16x32_bf16 v[48:51], v[210:213], v[218:221], v[48:51]
	v_mfma_f32_16x16x32_bf16 v[36:39], v[202:205], v[226:229], v[36:39]
	v_mfma_f32_16x16x32_bf16 v[32:35], v[210:213], v[226:229], v[32:35]
	v_mfma_f32_16x16x32_bf16 v[20:23], v[202:205], v[234:237], v[20:23]
	v_mfma_f32_16x16x32_bf16 v[16:19], v[210:213], v[234:237], v[16:19]
	v_mfma_f32_16x16x32_bf16 v[4:7], v[202:205], v[242:245], v[4:7]
	v_mfma_f32_16x16x32_bf16 v[0:3], v[210:213], v[242:245], v[0:3]
	v_mfma_f32_16x16x32_bf16 v[52:55], v[206:209], v[222:225], v[52:55]
	v_mfma_f32_16x16x32_bf16 v[48:51], v[214:217], v[222:225], v[48:51]
	v_mfma_f32_16x16x32_bf16 v[36:39], v[206:209], v[230:233], v[36:39]
	v_mfma_f32_16x16x32_bf16 v[32:35], v[214:217], v[230:233], v[32:35]
	v_mfma_f32_16x16x32_bf16 v[20:23], v[206:209], v[238:241], v[20:23]
	v_mfma_f32_16x16x32_bf16 v[16:19], v[214:217], v[238:241], v[16:19]
	v_mfma_f32_16x16x32_bf16 v[4:7], v[206:209], v[246:249], v[4:7]
	v_mfma_f32_16x16x32_bf16 v[0:3], v[214:217], v[246:249], v[0:3]
	s_barrier
	s_add_i32 s48, 0, 0x18000
	v_add_u32_e32 v185, s48, v166
	s_add_i32 s49, 0, 0x1c000
	ds_read_b128 v[186:189], v185
	ds_read_b128 v[190:193], v185 offset:1024
	ds_read_b128 v[194:197], v185 offset:2048
	ds_read_b128 v[198:201], v185 offset:3072
	v_add_u32_e32 v185, s49, v166
	ds_read_b128 v[202:205], v185
	ds_read_b128 v[206:209], v185 offset:1024
	ds_read_b128 v[210:213], v185 offset:2048
	ds_read_b128 v[214:217], v185 offset:3072
	s_mov_b32 m0, s66
	v_lshl_add_u64 v[148:149], s[40:41], 0, v[148:149]
	ds_read_b128 v[218:221], v182 offset:32768
	ds_read_b128 v[222:225], v182 offset:33792
	ds_read_b128 v[226:229], v182 offset:34816
	ds_read_b128 v[230:233], v182 offset:35840
	ds_read_b128 v[234:237], v182 offset:36864
	ds_read_b128 v[238:241], v182 offset:37888
	ds_read_b128 v[242:245], v182 offset:38912
	ds_read_b128 v[246:249], v182 offset:39936
	global_load_lds_dwordx4 v[148:149], off
	v_lshl_add_u64 v[148:149], s[40:41], 0, v[150:151]
	s_mov_b32 m0, s67
	s_nop 0
	global_load_lds_dwordx4 v[148:149], off
	s_waitcnt vmcnt(8)
	s_waitcnt lgkmcnt(0)
	s_barrier
	s_waitcnt lgkmcnt(0)
	v_mfma_f32_16x16x32_bf16 v[124:127], v[186:189], v[218:221], v[124:127]
	v_mfma_f32_16x16x32_bf16 v[120:123], v[194:197], v[218:221], v[120:123]
	v_mfma_f32_16x16x32_bf16 v[108:111], v[186:189], v[226:229], v[108:111]
	v_mfma_f32_16x16x32_bf16 v[104:107], v[194:197], v[226:229], v[104:107]
	v_mfma_f32_16x16x32_bf16 v[92:95], v[186:189], v[234:237], v[92:95]
	v_mfma_f32_16x16x32_bf16 v[88:91], v[194:197], v[234:237], v[88:91]
	v_mfma_f32_16x16x32_bf16 v[76:79], v[186:189], v[242:245], v[76:79]
	v_mfma_f32_16x16x32_bf16 v[72:75], v[194:197], v[242:245], v[72:75]
	v_mfma_f32_16x16x32_bf16 v[124:127], v[190:193], v[222:225], v[124:127]
	v_mfma_f32_16x16x32_bf16 v[120:123], v[198:201], v[222:225], v[120:123]
	v_mfma_f32_16x16x32_bf16 v[108:111], v[190:193], v[230:233], v[108:111]
	v_mfma_f32_16x16x32_bf16 v[104:107], v[198:201], v[230:233], v[104:107]
	v_mfma_f32_16x16x32_bf16 v[92:95], v[190:193], v[238:241], v[92:95]
	v_mfma_f32_16x16x32_bf16 v[88:91], v[198:201], v[238:241], v[88:91]
	v_mfma_f32_16x16x32_bf16 v[76:79], v[190:193], v[246:249], v[76:79]
	v_mfma_f32_16x16x32_bf16 v[72:75], v[198:201], v[246:249], v[72:75]
	v_mfma_f32_16x16x32_bf16 v[116:119], v[202:205], v[218:221], v[116:119]
	v_mfma_f32_16x16x32_bf16 v[112:115], v[210:213], v[218:221], v[112:115]
	v_mfma_f32_16x16x32_bf16 v[100:103], v[202:205], v[226:229], v[100:103]
	v_mfma_f32_16x16x32_bf16 v[96:99], v[210:213], v[226:229], v[96:99]
	v_mfma_f32_16x16x32_bf16 v[84:87], v[202:205], v[234:237], v[84:87]
	v_mfma_f32_16x16x32_bf16 v[80:83], v[210:213], v[234:237], v[80:83]
	v_mfma_f32_16x16x32_bf16 v[68:71], v[202:205], v[242:245], v[68:71]
	v_mfma_f32_16x16x32_bf16 v[64:67], v[210:213], v[242:245], v[64:67]
	v_mfma_f32_16x16x32_bf16 v[116:119], v[206:209], v[222:225], v[116:119]
	v_mfma_f32_16x16x32_bf16 v[112:115], v[214:217], v[222:225], v[112:115]
	v_mfma_f32_16x16x32_bf16 v[100:103], v[206:209], v[230:233], v[100:103]
	v_mfma_f32_16x16x32_bf16 v[96:99], v[214:217], v[230:233], v[96:99]
	v_mfma_f32_16x16x32_bf16 v[84:87], v[206:209], v[238:241], v[84:87]
	v_mfma_f32_16x16x32_bf16 v[80:83], v[214:217], v[238:241], v[80:83]
	v_mfma_f32_16x16x32_bf16 v[68:71], v[206:209], v[246:249], v[68:71]
	v_mfma_f32_16x16x32_bf16 v[64:67], v[214:217], v[246:249], v[64:67]
	s_barrier
; template <class Epi, class Sched, class Hook = NoHook>
; __device__ __forceinline__ void gemm_phase_w(LAS unsigned char* lds, const Sched& S, const Epi& E, int wave_id, const Hook& HK = Hook()) {
;     ...
;         if constexpr (!SEG2) {
;             for (int tt = 0; tt < nt; tt += 2) {
;                 if constexpr (GATHER) { if (tt == nt - 2) {
;                     if (has_next) { gnxt_00 = S.grow_l(nxt, lds, nbuf, R0) + (unsigned)(C0 * 2); gnxt_01 = S.grow_l(nxt, lds, nbuf, R1) + (unsigned)(C1 * 2); gnxt_10 = S.grow_l(nxt, lds, nbuf, 128 + R0) + (unsigned)(C0 * 2); gnxt_11 = S.grow_l(nxt, lds, nbuf, 128 + R1) + (unsigned)(C1 * 2); }
;                     else { gnxt_00 = gcur_00; gnxt_01 = gcur_01; gnxt_10 = gcur_10; gnxt_11 = gcur_11; } } }
;                 PG_TRIP(tt, false, false, false);
;             }
	s_bitset1_b32 s22, 7
	s_add_i32 vcc_lo, vcc_lo, s22
	s_ashr_i32 s41, vcc_lo, 31
	s_add_u32 s40, s16, vcc_lo
	s_addc_u32 s41, s17, s41
	s_add_i32 s48, s48, s44
	v_lshl_add_u64 v[246:247], s[40:41], 0, v[136:137]
	s_mov_b32 m0, s48
	s_add_i32 vcc_lo, vcc_lo, 0x80000
	ds_read_b128 v[148:151], v182 offset:49152
	ds_read_b128 v[218:221], v182 offset:50176
	ds_read_b128 v[222:225], v182 offset:51200
	ds_read_b128 v[226:229], v182 offset:52224
	ds_read_b128 v[230:233], v182 offset:53248
	ds_read_b128 v[234:237], v182 offset:54272
	ds_read_b128 v[238:241], v182 offset:55296
	ds_read_b128 v[242:245], v182 offset:56320
	global_load_lds_dwordx4 v[246:247], off
	v_lshl_add_u64 v[246:247], s[40:41], 0, v[138:139]
	s_add_i32 m0, s48, 0x2000
	s_ashr_i32 s41, vcc_lo, 31
	s_add_u32 s40, s16, vcc_lo
	s_addc_u32 s41, s17, s41
	s_add_i32 s48, s49, s44
	global_load_lds_dwordx4 v[246:247], off
	v_lshl_add_u64 v[246:247], s[40:41], 0, v[136:137]
	s_mov_b32 m0, s48
	v_lshl_add_u64 v[146:147], s[14:15], 0, v[146:147]
	global_load_lds_dwordx4 v[246:247], off
	v_lshl_add_u64 v[246:247], s[40:41], 0, v[138:139]
	s_add_i32 m0, s48, 0x2000
	v_lshl_add_u64 v[146:147], v[146:147], 0, s[22:23]
	global_load_lds_dwordx4 v[246:247], off
	v_lshl_add_u64 v[246:247], s[14:15], 0, v[140:141]
	v_lshl_add_u64 v[246:247], v[246:247], 0, s[22:23]
	s_mov_b32 m0, s68
	s_nop 0
	global_load_lds_dwordx4 v[246:247], off
	s_mov_b32 m0, s69
	s_nop 0
	global_load_lds_dwordx4 v[146:147], off
	s_waitcnt vmcnt(8)
	s_waitcnt lgkmcnt(0)
	s_barrier
	s_waitcnt lgkmcnt(0)
	v_mfma_f32_16x16x32_bf16 v[60:63], v[186:189], v[148:151], v[60:63]
	v_mfma_f32_16x16x32_bf16 v[56:59], v[194:197], v[148:151], v[56:59]
	v_mfma_f32_16x16x32_bf16 v[44:47], v[186:189], v[222:225], v[44:47]
	v_mfma_f32_16x16x32_bf16 v[40:43], v[194:197], v[222:225], v[40:43]
	v_mfma_f32_16x16x32_bf16 v[28:31], v[186:189], v[230:233], v[28:31]
	v_mfma_f32_16x16x32_bf16 v[24:27], v[194:197], v[230:233], v[24:27]
	v_mfma_f32_16x16x32_bf16 v[12:15], v[186:189], v[238:241], v[12:15]
	v_mfma_f32_16x16x32_bf16 v[8:11], v[194:197], v[238:241], v[8:11]
	v_mfma_f32_16x16x32_bf16 v[60:63], v[190:193], v[218:221], v[60:63]
	v_mfma_f32_16x16x32_bf16 v[56:59], v[198:201], v[218:221], v[56:59]
	v_mfma_f32_16x16x32_bf16 v[44:47], v[190:193], v[226:229], v[44:47]
	v_mfma_f32_16x16x32_bf16 v[40:43], v[198:201], v[226:229], v[40:43]
	v_mfma_f32_16x16x32_bf16 v[28:31], v[190:193], v[234:237], v[28:31]
	v_mfma_f32_16x16x32_bf16 v[24:27], v[198:201], v[234:237], v[24:27]
	v_mfma_f32_16x16x32_bf16 v[12:15], v[190:193], v[242:245], v[12:15]
	v_mfma_f32_16x16x32_bf16 v[8:11], v[198:201], v[242:245], v[8:11]
	v_mfma_f32_16x16x32_bf16 v[52:55], v[202:205], v[148:151], v[52:55]
	v_mfma_f32_16x16x32_bf16 v[48:51], v[210:213], v[148:151], v[48:51]
	v_mfma_f32_16x16x32_bf16 v[36:39], v[202:205], v[222:225], v[36:39]
	v_mfma_f32_16x16x32_bf16 v[32:35], v[210:213], v[222:225], v[32:35]
	v_mfma_f32_16x16x32_bf16 v[20:23], v[202:205], v[230:233], v[20:23]
	v_mfma_f32_16x16x32_bf16 v[16:19], v[210:213], v[230:233], v[16:19]
	v_mfma_f32_16x16x32_bf16 v[4:7], v[202:205], v[238:241], v[4:7]
	v_mfma_f32_16x16x32_bf16 v[0:3], v[210:213], v[238:241], v[0:3]
	v_mfma_f32_16x16x32_bf16 v[52:55], v[206:209], v[218:221], v[52:55]
	v_mfma_f32_16x16x32_bf16 v[48:51], v[214:217], v[218:221], v[48:51]
	v_mfma_f32_16x16x32_bf16 v[36:39], v[206:209], v[226:229], v[36:39]
	v_mfma_f32_16x16x32_bf16 v[32:35], v[214:217], v[226:229], v[32:35]
	v_mfma_f32_16x16x32_bf16 v[20:23], v[206:209], v[234:237], v[20:23]
	v_mfma_f32_16x16x32_bf16 v[16:19], v[214:217], v[234:237], v[16:19]
	v_mfma_f32_16x16x32_bf16 v[4:7], v[206:209], v[242:245], v[4:7]
	v_mfma_f32_16x16x32_bf16 v[0:3], v[214:217], v[242:245], v[0:3]
	s_add_i32 s89, s89, 2
	s_addk_i32 s97, 0x100
	s_add_u32 s38, s38, 0x100
	s_addc_u32 s39, s39, 0
	s_cmp_gt_u32 s89, 29
	s_barrier
	s_cbranch_scc1 .LBB0_831

.LBB0_1082:
	v_add_u32_e32 v147, s49, v163
	ds_read_b128 v[182:185], v147
	ds_read_b128 v[186:189], v147 offset:1024
	ds_read_b128 v[190:193], v147 offset:2048
	ds_read_b128 v[194:197], v147 offset:3072
	v_add_u32_e32 v147, s58, v163
	ds_read_b128 v[198:201], v147
	ds_read_b128 v[202:205], v147 offset:1024
	ds_read_b128 v[206:209], v147 offset:2048
	ds_read_b128 v[210:213], v147 offset:3072
	v_lshl_add_u64 v[246:247], s[38:39], 0, v[130:131]
	s_add_i32 m0, s63, 0xc000
	ds_read_b128 v[214:217], v179
	ds_read_b128 v[218:221], v179 offset:1024
	ds_read_b128 v[222:225], v179 offset:2048
	ds_read_b128 v[226:229], v179 offset:3072
	ds_read_b128 v[230:233], v179 offset:4096
	ds_read_b128 v[234:237], v179 offset:5120
	ds_read_b128 v[238:241], v179 offset:6144
	ds_read_b128 v[242:245], v179 offset:7168
	global_load_lds_dwordx4 v[246:247], off
	v_lshl_add_u64 v[246:247], s[38:39], 0, v[132:133]
	s_add_i32 m0, s63, 0xe000
	s_nop 0
	global_load_lds_dwordx4 v[246:247], off
	s_waitcnt vmcnt(8)
	s_waitcnt lgkmcnt(0)
	s_barrier
	s_waitcnt lgkmcnt(0)
	v_mfma_f32_16x16x32_bf16 v[124:127], v[182:185], v[214:217], v[124:127]
	v_mfma_f32_16x16x32_bf16 v[120:123], v[190:193], v[214:217], v[120:123]
	v_mfma_f32_16x16x32_bf16 v[108:111], v[182:185], v[222:225], v[108:111]
	v_mfma_f32_16x16x32_bf16 v[104:107], v[190:193], v[222:225], v[104:107]
	v_mfma_f32_16x16x32_bf16 v[92:95], v[182:185], v[230:233], v[92:95]
	v_mfma_f32_16x16x32_bf16 v[88:91], v[190:193], v[230:233], v[88:91]
	v_mfma_f32_16x16x32_bf16 v[76:79], v[182:185], v[238:241], v[76:79]
	v_mfma_f32_16x16x32_bf16 v[72:75], v[190:193], v[238:241], v[72:75]
	v_mfma_f32_16x16x32_bf16 v[124:127], v[186:189], v[218:221], v[124:127]
	v_mfma_f32_16x16x32_bf16 v[120:123], v[194:197], v[218:221], v[120:123]
	v_mfma_f32_16x16x32_bf16 v[108:111], v[186:189], v[226:229], v[108:111]
	v_mfma_f32_16x16x32_bf16 v[104:107], v[194:197], v[226:229], v[104:107]
	v_mfma_f32_16x16x32_bf16 v[92:95], v[186:189], v[234:237], v[92:95]
	v_mfma_f32_16x16x32_bf16 v[88:91], v[194:197], v[234:237], v[88:91]
	v_mfma_f32_16x16x32_bf16 v[76:79], v[186:189], v[242:245], v[76:79]
	v_mfma_f32_16x16x32_bf16 v[72:75], v[194:197], v[242:245], v[72:75]
	v_mfma_f32_16x16x32_bf16 v[116:119], v[198:201], v[214:217], v[116:119]
	v_mfma_f32_16x16x32_bf16 v[112:115], v[206:209], v[214:217], v[112:115]
	v_mfma_f32_16x16x32_bf16 v[100:103], v[198:201], v[222:225], v[100:103]
	v_mfma_f32_16x16x32_bf16 v[96:99], v[206:209], v[222:225], v[96:99]
	v_mfma_f32_16x16x32_bf16 v[84:87], v[198:201], v[230:233], v[84:87]
	v_mfma_f32_16x16x32_bf16 v[80:83], v[206:209], v[230:233], v[80:83]
	v_mfma_f32_16x16x32_bf16 v[68:71], v[198:201], v[238:241], v[68:71]
	v_mfma_f32_16x16x32_bf16 v[64:67], v[206:209], v[238:241], v[64:67]
	v_mfma_f32_16x16x32_bf16 v[116:119], v[202:205], v[218:221], v[116:119]
	v_mfma_f32_16x16x32_bf16 v[112:115], v[210:213], v[218:221], v[112:115]
	v_mfma_f32_16x16x32_bf16 v[100:103], v[202:205], v[226:229], v[100:103]
	v_mfma_f32_16x16x32_bf16 v[96:99], v[210:213], v[226:229], v[96:99]
	v_mfma_f32_16x16x32_bf16 v[84:87], v[202:205], v[234:237], v[84:87]
	v_mfma_f32_16x16x32_bf16 v[80:83], v[210:213], v[234:237], v[80:83]
	v_mfma_f32_16x16x32_bf16 v[68:71], v[202:205], v[242:245], v[68:71]
	v_mfma_f32_16x16x32_bf16 v[64:67], v[210:213], v[242:245], v[64:67]
	s_barrier
	s_and_b64 s[40:41], s[40:41], exec
	s_cselect_b32 s22, 0, s78
	s_add_i32 s84, s79, s22
	s_ashr_i32 s41, s84, 31
	s_add_u32 s40, s16, s84
	s_addc_u32 s41, s17, s41
	s_add_i32 s85, s49, s44
	v_lshl_add_u64 v[246:247], s[40:41], 0, v[136:137]
	s_mov_b32 m0, s85
	s_add_i32 s84, s84, 0x80000
	ds_read_b128 v[214:217], v179 offset:16384
	ds_read_b128 v[218:221], v179 offset:17408
	ds_read_b128 v[222:225], v179 offset:18432
	ds_read_b128 v[226:229], v179 offset:19456
	ds_read_b128 v[230:233], v179 offset:20480
	ds_read_b128 v[234:237], v179 offset:21504
	ds_read_b128 v[238:241], v179 offset:22528
	ds_read_b128 v[242:245], v179 offset:23552
	global_load_lds_dwordx4 v[246:247], off
	v_lshl_add_u64 v[246:247], s[40:41], 0, v[138:139]
	s_add_i32 m0, s85, 0x2000
	s_ashr_i32 s41, s84, 31
	s_add_u32 s40, s16, s84
	s_addc_u32 s41, s17, s41
	s_add_i32 s84, s58, s44
	global_load_lds_dwordx4 v[246:247], off
	v_lshl_add_u64 v[246:247], s[40:41], 0, v[136:137]
	s_mov_b32 m0, s84
	v_mov_b32_e32 v147, v141
	global_load_lds_dwordx4 v[246:247], off
	s_add_i32 m0, s84, 0x2000
	v_lshl_add_u64 v[246:247], s[40:41], 0, v[138:139]
	s_add_u32 s40, s14, s22
	global_load_lds_dwordx4 v[246:247], off
	s_addc_u32 s41, s15, 0
	s_mov_b32 m0, s63
	s_nop 0
	global_load_lds_dwordx4 v140, s[40:41]
	s_mov_b32 m0, s66
	s_nop 0
	global_load_lds_dwordx4 v146, s[40:41]
	s_waitcnt vmcnt(8)
	s_waitcnt lgkmcnt(0)
	s_barrier
	s_waitcnt lgkmcnt(0)
	v_mfma_f32_16x16x32_bf16 v[60:63], v[182:185], v[214:217], v[60:63]
	v_mfma_f32_16x16x32_bf16 v[56:59], v[190:193], v[214:217], v[56:59]
	v_mfma_f32_16x16x32_bf16 v[44:47], v[182:185], v[222:225], v[44:47]
	v_mfma_f32_16x16x32_bf16 v[40:43], v[190:193], v[222:225], v[40:43]
	v_mfma_f32_16x16x32_bf16 v[28:31], v[182:185], v[230:233], v[28:31]
	v_mfma_f32_16x16x32_bf16 v[24:27], v[190:193], v[230:233], v[24:27]
	v_mfma_f32_16x16x32_bf16 v[12:15], v[182:185], v[238:241], v[12:15]
	v_mfma_f32_16x16x32_bf16 v[8:11], v[190:193], v[238:241], v[8:11]
	v_mfma_f32_16x16x32_bf16 v[60:63], v[186:189], v[218:221], v[60:63]
	v_mfma_f32_16x16x32_bf16 v[56:59], v[194:197], v[218:221], v[56:59]
	v_mfma_f32_16x16x32_bf16 v[44:47], v[186:189], v[226:229], v[44:47]
	v_mfma_f32_16x16x32_bf16 v[40:43], v[194:197], v[226:229], v[40:43]
	v_mfma_f32_16x16x32_bf16 v[28:31], v[186:189], v[234:237], v[28:31]
	v_mfma_f32_16x16x32_bf16 v[24:27], v[194:197], v[234:237], v[24:27]
	v_mfma_f32_16x16x32_bf16 v[12:15], v[186:189], v[242:245], v[12:15]
	v_mfma_f32_16x16x32_bf16 v[8:11], v[194:197], v[242:245], v[8:11]
	v_mfma_f32_16x16x32_bf16 v[52:55], v[198:201], v[214:217], v[52:55]
	v_mfma_f32_16x16x32_bf16 v[48:51], v[206:209], v[214:217], v[48:51]
	v_mfma_f32_16x16x32_bf16 v[36:39], v[198:201], v[222:225], v[36:39]
	v_mfma_f32_16x16x32_bf16 v[32:35], v[206:209], v[222:225], v[32:35]
	v_mfma_f32_16x16x32_bf16 v[20:23], v[198:201], v[230:233], v[20:23]
	v_mfma_f32_16x16x32_bf16 v[16:19], v[206:209], v[230:233], v[16:19]
	v_mfma_f32_16x16x32_bf16 v[4:7], v[198:201], v[238:241], v[4:7]
	v_mfma_f32_16x16x32_bf16 v[0:3], v[206:209], v[238:241], v[0:3]
	v_mfma_f32_16x16x32_bf16 v[52:55], v[202:205], v[218:221], v[52:55]
	v_mfma_f32_16x16x32_bf16 v[48:51], v[210:213], v[218:221], v[48:51]
	v_mfma_f32_16x16x32_bf16 v[36:39], v[202:205], v[226:229], v[36:39]
	v_mfma_f32_16x16x32_bf16 v[32:35], v[210:213], v[226:229], v[32:35]
	v_mfma_f32_16x16x32_bf16 v[20:23], v[202:205], v[234:237], v[20:23]
	v_mfma_f32_16x16x32_bf16 v[16:19], v[210:213], v[234:237], v[16:19]
	v_mfma_f32_16x16x32_bf16 v[4:7], v[202:205], v[242:245], v[4:7]
	v_mfma_f32_16x16x32_bf16 v[0:3], v[210:213], v[242:245], v[0:3]
	s_barrier
	s_add_i32 s84, 0, 0x18000
	s_add_i32 s85, 0, 0x1c000
	v_add_u32_e32 v194, s84, v163
	v_add_u32_e32 v210, s85, v163
	ds_read_b128 v[182:185], v194
	ds_read_b128 v[186:189], v194 offset:1024
	ds_read_b128 v[190:193], v194 offset:2048
	ds_read_b128 v[194:197], v194 offset:3072
	ds_read_b128 v[198:201], v210
	ds_read_b128 v[202:205], v210 offset:1024
	ds_read_b128 v[206:209], v210 offset:2048
	ds_read_b128 v[210:213], v210 offset:3072
	s_mov_b32 m0, s67
	v_lshl_add_u64 v[148:149], s[40:41], 0, v[148:149]
	ds_read_b128 v[214:217], v179 offset:32768
	ds_read_b128 v[218:221], v179 offset:33792
	ds_read_b128 v[222:225], v179 offset:34816
	ds_read_b128 v[226:229], v179 offset:35840
	ds_read_b128 v[230:233], v179 offset:36864
	ds_read_b128 v[234:237], v179 offset:37888
	ds_read_b128 v[238:241], v179 offset:38912
	ds_read_b128 v[242:245], v179 offset:39936
	global_load_lds_dwordx4 v[148:149], off
	v_lshl_add_u64 v[148:149], s[40:41], 0, v[150:151]
	s_mov_b32 m0, s68
	s_nop 0
	global_load_lds_dwordx4 v[148:149], off
	s_waitcnt vmcnt(8)
	s_waitcnt lgkmcnt(0)
	s_barrier
	s_waitcnt lgkmcnt(0)
	v_mfma_f32_16x16x32_bf16 v[124:127], v[182:185], v[214:217], v[124:127]
	v_mfma_f32_16x16x32_bf16 v[120:123], v[190:193], v[214:217], v[120:123]
	v_mfma_f32_16x16x32_bf16 v[108:111], v[182:185], v[222:225], v[108:111]
	v_mfma_f32_16x16x32_bf16 v[104:107], v[190:193], v[222:225], v[104:107]
	v_mfma_f32_16x16x32_bf16 v[92:95], v[182:185], v[230:233], v[92:95]
	v_mfma_f32_16x16x32_bf16 v[88:91], v[190:193], v[230:233], v[88:91]
	v_mfma_f32_16x16x32_bf16 v[76:79], v[182:185], v[238:241], v[76:79]
	v_mfma_f32_16x16x32_bf16 v[72:75], v[190:193], v[238:241], v[72:75]
	v_mfma_f32_16x16x32_bf16 v[124:127], v[186:189], v[218:221], v[124:127]
	v_mfma_f32_16x16x32_bf16 v[120:123], v[194:197], v[218:221], v[120:123]
	v_mfma_f32_16x16x32_bf16 v[108:111], v[186:189], v[226:229], v[108:111]
	v_mfma_f32_16x16x32_bf16 v[104:107], v[194:197], v[226:229], v[104:107]
	v_mfma_f32_16x16x32_bf16 v[92:95], v[186:189], v[234:237], v[92:95]
	v_mfma_f32_16x16x32_bf16 v[88:91], v[194:197], v[234:237], v[88:91]
	v_mfma_f32_16x16x32_bf16 v[76:79], v[186:189], v[242:245], v[76:79]
	v_mfma_f32_16x16x32_bf16 v[72:75], v[194:197], v[242:245], v[72:75]
	v_mfma_f32_16x16x32_bf16 v[116:119], v[198:201], v[214:217], v[116:119]
	v_mfma_f32_16x16x32_bf16 v[112:115], v[206:209], v[214:217], v[112:115]
	v_mfma_f32_16x16x32_bf16 v[100:103], v[198:201], v[222:225], v[100:103]
	v_mfma_f32_16x16x32_bf16 v[96:99], v[206:209], v[222:225], v[96:99]
	v_mfma_f32_16x16x32_bf16 v[84:87], v[198:201], v[230:233], v[84:87]
	v_mfma_f32_16x16x32_bf16 v[80:83], v[206:209], v[230:233], v[80:83]
	v_mfma_f32_16x16x32_bf16 v[68:71], v[198:201], v[238:241], v[68:71]
	v_mfma_f32_16x16x32_bf16 v[64:67], v[206:209], v[238:241], v[64:67]
	v_mfma_f32_16x16x32_bf16 v[116:119], v[202:205], v[218:221], v[116:119]
	v_mfma_f32_16x16x32_bf16 v[112:115], v[210:213], v[218:221], v[112:115]
	v_mfma_f32_16x16x32_bf16 v[100:103], v[202:205], v[226:229], v[100:103]
	v_mfma_f32_16x16x32_bf16 v[96:99], v[210:213], v[226:229], v[96:99]
	v_mfma_f32_16x16x32_bf16 v[84:87], v[202:205], v[234:237], v[84:87]
	v_mfma_f32_16x16x32_bf16 v[80:83], v[210:213], v[234:237], v[80:83]
	v_mfma_f32_16x16x32_bf16 v[68:71], v[202:205], v[242:245], v[68:71]
	v_mfma_f32_16x16x32_bf16 v[64:67], v[210:213], v[242:245], v[64:67]
	s_barrier
; template <class Epi, class Sched, class Hook = NoHook>
; __device__ __forceinline__ void gemm_phase_w(LAS unsigned char* lds, const Sched& S, const Epi& E, int wave_id, const Hook& HK = Hook()) {
;     ...
;         if constexpr (!SEG2) {
;             for (int tt = 0; tt < nt; tt += 2) {
;                 if constexpr (GATHER) { if (tt == nt - 2) {
;                     if (has_next) { gnxt_00 = S.grow_l(nxt, lds, nbuf, R0) + (unsigned)(C0 * 2); gnxt_01 = S.grow_l(nxt, lds, nbuf, R1) + (unsigned)(C1 * 2); gnxt_10 = S.grow_l(nxt, lds, nbuf, 128 + R0) + (unsigned)(C0 * 2); gnxt_11 = S.grow_l(nxt, lds, nbuf, 128 + R1) + (unsigned)(C1 * 2); }
;                     else { gnxt_00 = gcur_00; gnxt_01 = gcur_01; gnxt_10 = gcur_10; gnxt_11 = gcur_11; } } }
;                 PG_TRIP(tt, false, false, false);
;             }
	s_bitset1_b32 s22, 7
	s_add_i32 s79, s79, s22
	s_ashr_i32 s41, s79, 31
	s_add_u32 s40, s16, s79
	s_addc_u32 s41, s17, s41
	s_add_i32 s84, s84, s44
	v_lshl_add_u64 v[242:243], s[40:41], 0, v[136:137]
	s_mov_b32 m0, s84
	s_add_i32 s79, s79, 0x80000
	ds_read_b128 v[148:151], v179 offset:49152
	ds_read_b128 v[214:217], v179 offset:50176
	ds_read_b128 v[218:221], v179 offset:51200
	ds_read_b128 v[222:225], v179 offset:52224
	ds_read_b128 v[226:229], v179 offset:53248
	ds_read_b128 v[230:233], v179 offset:54272
	ds_read_b128 v[234:237], v179 offset:55296
	ds_read_b128 v[238:241], v179 offset:56320
	global_load_lds_dwordx4 v[242:243], off
	v_lshl_add_u64 v[242:243], s[40:41], 0, v[138:139]
	s_add_i32 m0, s84, 0x2000
	s_ashr_i32 s41, s79, 31
	s_add_u32 s40, s16, s79
	s_addc_u32 s41, s17, s41
	s_add_i32 s79, s85, s44
	global_load_lds_dwordx4 v[242:243], off
	v_lshl_add_u64 v[242:243], s[40:41], 0, v[136:137]
	s_mov_b32 m0, s79
	v_lshl_add_u64 v[146:147], s[14:15], 0, v[146:147]
	global_load_lds_dwordx4 v[242:243], off
	v_lshl_add_u64 v[242:243], s[40:41], 0, v[138:139]
	s_add_i32 m0, s79, 0x2000
	v_lshl_add_u64 v[146:147], v[146:147], 0, s[22:23]
	global_load_lds_dwordx4 v[242:243], off
	v_lshl_add_u64 v[242:243], s[14:15], 0, v[140:141]
	v_lshl_add_u64 v[242:243], v[242:243], 0, s[22:23]
	s_mov_b32 m0, s59
	s_nop 0
	global_load_lds_dwordx4 v[242:243], off
	s_mov_b32 m0, s69
	s_nop 0
	global_load_lds_dwordx4 v[146:147], off
	s_waitcnt vmcnt(8)
	s_waitcnt lgkmcnt(0)
	s_barrier
	s_waitcnt lgkmcnt(0)
	v_mfma_f32_16x16x32_bf16 v[60:63], v[182:185], v[148:151], v[60:63]
	v_mfma_f32_16x16x32_bf16 v[56:59], v[190:193], v[148:151], v[56:59]
	v_mfma_f32_16x16x32_bf16 v[44:47], v[182:185], v[218:221], v[44:47]
	v_mfma_f32_16x16x32_bf16 v[40:43], v[190:193], v[218:221], v[40:43]
	v_mfma_f32_16x16x32_bf16 v[28:31], v[182:185], v[226:229], v[28:31]
	v_mfma_f32_16x16x32_bf16 v[24:27], v[190:193], v[226:229], v[24:27]
	v_mfma_f32_16x16x32_bf16 v[12:15], v[182:185], v[234:237], v[12:15]
	v_mfma_f32_16x16x32_bf16 v[8:11], v[190:193], v[234:237], v[8:11]
	v_mfma_f32_16x16x32_bf16 v[60:63], v[186:189], v[214:217], v[60:63]
	v_mfma_f32_16x16x32_bf16 v[56:59], v[194:197], v[214:217], v[56:59]
	v_mfma_f32_16x16x32_bf16 v[44:47], v[186:189], v[222:225], v[44:47]
	v_mfma_f32_16x16x32_bf16 v[40:43], v[194:197], v[222:225], v[40:43]
	v_mfma_f32_16x16x32_bf16 v[28:31], v[186:189], v[230:233], v[28:31]
	v_mfma_f32_16x16x32_bf16 v[24:27], v[194:197], v[230:233], v[24:27]
	v_mfma_f32_16x16x32_bf16 v[12:15], v[186:189], v[238:241], v[12:15]
	v_mfma_f32_16x16x32_bf16 v[8:11], v[194:197], v[238:241], v[8:11]
	v_mfma_f32_16x16x32_bf16 v[52:55], v[198:201], v[148:151], v[52:55]
	v_mfma_f32_16x16x32_bf16 v[48:51], v[206:209], v[148:151], v[48:51]
	v_mfma_f32_16x16x32_bf16 v[36:39], v[198:201], v[218:221], v[36:39]
	v_mfma_f32_16x16x32_bf16 v[32:35], v[206:209], v[218:221], v[32:35]
	v_mfma_f32_16x16x32_bf16 v[20:23], v[198:201], v[226:229], v[20:23]
	v_mfma_f32_16x16x32_bf16 v[16:19], v[206:209], v[226:229], v[16:19]
	v_mfma_f32_16x16x32_bf16 v[4:7], v[198:201], v[234:237], v[4:7]
	v_mfma_f32_16x16x32_bf16 v[0:3], v[206:209], v[234:237], v[0:3]
	v_mfma_f32_16x16x32_bf16 v[52:55], v[202:205], v[214:217], v[52:55]
	v_mfma_f32_16x16x32_bf16 v[48:51], v[210:213], v[214:217], v[48:51]
	v_mfma_f32_16x16x32_bf16 v[36:39], v[202:205], v[222:225], v[36:39]
	v_mfma_f32_16x16x32_bf16 v[32:35], v[210:213], v[222:225], v[32:35]
	v_mfma_f32_16x16x32_bf16 v[20:23], v[202:205], v[230:233], v[20:23]
	v_mfma_f32_16x16x32_bf16 v[16:19], v[210:213], v[230:233], v[16:19]
	v_mfma_f32_16x16x32_bf16 v[4:7], v[202:205], v[238:241], v[4:7]
	v_mfma_f32_16x16x32_bf16 v[0:3], v[210:213], v[238:241], v[0:3]
	s_add_i32 s77, s77, 2
	s_addk_i32 s78, 0x100
	s_add_u32 s38, s38, 0x100
	s_addc_u32 s39, s39, 0
	s_cmp_gt_u32 s77, 29
	s_barrier
	s_cbranch_scc1 .LBB0_1086

.LBB0_1194:
	ds_read_b128 v[160:163], v156
	ds_read_b128 v[164:167], v156 offset:1024
	ds_read_b128 v[168:171], v156 offset:2048
	ds_read_b128 v[172:175], v156 offset:3072
	ds_read_b128 v[176:179], v157
	ds_read_b128 v[180:183], v157 offset:1024
	ds_read_b128 v[184:187], v157 offset:2048
	ds_read_b128 v[188:191], v157 offset:3072
	s_add_i32 s22, s68, s12
	s_add_u32 s36, s28, s22
	s_addc_u32 s37, s29, 0
	s_add_i32 m0, s26, 0xc000
	s_add_i32 s71, s26, 0xe000
	s_add_i32 s72, s12, 0xfffc0080
	s_cmp_eq_u32 s19, 12
	s_cselect_b32 s22, s63, s68
	s_cselect_b32 s23, s66, s69
	v_lshl_add_u64 v[224:225], s[36:37], 0, v[130:131]
	ds_read_b128 v[192:195], v158
	ds_read_b128 v[196:199], v158 offset:1024
	ds_read_b128 v[200:203], v158 offset:2048
	ds_read_b128 v[204:207], v158 offset:3072
	ds_read_b128 v[208:211], v158 offset:4096
	ds_read_b128 v[212:215], v158 offset:5120
	ds_read_b128 v[216:219], v158 offset:6144
	ds_read_b128 v[220:223], v158 offset:7168
	global_load_lds_dwordx4 v[224:225], off
	v_lshl_add_u64 v[224:225], s[36:37], 0, v[132:133]
	s_mov_b32 m0, s71
	s_nop 0
	global_load_lds_dwordx4 v[224:225], off
	s_waitcnt vmcnt(8)
	s_waitcnt lgkmcnt(0)
	s_barrier
	s_waitcnt lgkmcnt(0)
	v_mfma_f32_16x16x32_bf16 v[124:127], v[160:163], v[192:195], v[124:127]
	v_mfma_f32_16x16x32_bf16 v[120:123], v[168:171], v[192:195], v[120:123]
	v_mfma_f32_16x16x32_bf16 v[108:111], v[160:163], v[200:203], v[108:111]
	v_mfma_f32_16x16x32_bf16 v[104:107], v[168:171], v[200:203], v[104:107]
	v_mfma_f32_16x16x32_bf16 v[92:95], v[160:163], v[208:211], v[92:95]
	v_mfma_f32_16x16x32_bf16 v[88:91], v[168:171], v[208:211], v[88:91]
	v_mfma_f32_16x16x32_bf16 v[76:79], v[160:163], v[216:219], v[76:79]
	v_mfma_f32_16x16x32_bf16 v[72:75], v[168:171], v[216:219], v[72:75]
	v_mfma_f32_16x16x32_bf16 v[124:127], v[164:167], v[196:199], v[124:127]
	v_mfma_f32_16x16x32_bf16 v[120:123], v[172:175], v[196:199], v[120:123]
	v_mfma_f32_16x16x32_bf16 v[108:111], v[164:167], v[204:207], v[108:111]
	v_mfma_f32_16x16x32_bf16 v[104:107], v[172:175], v[204:207], v[104:107]
	v_mfma_f32_16x16x32_bf16 v[92:95], v[164:167], v[212:215], v[92:95]
	v_mfma_f32_16x16x32_bf16 v[88:91], v[172:175], v[212:215], v[88:91]
	v_mfma_f32_16x16x32_bf16 v[76:79], v[164:167], v[220:223], v[76:79]
	v_mfma_f32_16x16x32_bf16 v[72:75], v[172:175], v[220:223], v[72:75]
	v_mfma_f32_16x16x32_bf16 v[116:119], v[176:179], v[192:195], v[116:119]
	v_mfma_f32_16x16x32_bf16 v[112:115], v[184:187], v[192:195], v[112:115]
	v_mfma_f32_16x16x32_bf16 v[100:103], v[176:179], v[200:203], v[100:103]
	v_mfma_f32_16x16x32_bf16 v[96:99], v[184:187], v[200:203], v[96:99]
	v_mfma_f32_16x16x32_bf16 v[84:87], v[176:179], v[208:211], v[84:87]
	v_mfma_f32_16x16x32_bf16 v[80:83], v[184:187], v[208:211], v[80:83]
	v_mfma_f32_16x16x32_bf16 v[68:71], v[176:179], v[216:219], v[68:71]
	v_mfma_f32_16x16x32_bf16 v[64:67], v[184:187], v[216:219], v[64:67]
	v_mfma_f32_16x16x32_bf16 v[116:119], v[180:183], v[196:199], v[116:119]
	v_mfma_f32_16x16x32_bf16 v[112:115], v[188:191], v[196:199], v[112:115]
	v_mfma_f32_16x16x32_bf16 v[100:103], v[180:183], v[204:207], v[100:103]
	v_mfma_f32_16x16x32_bf16 v[96:99], v[188:191], v[204:207], v[96:99]
	v_mfma_f32_16x16x32_bf16 v[84:87], v[180:183], v[212:215], v[84:87]
	v_mfma_f32_16x16x32_bf16 v[80:83], v[188:191], v[212:215], v[80:83]
	v_mfma_f32_16x16x32_bf16 v[68:71], v[180:183], v[220:223], v[68:71]
	v_mfma_f32_16x16x32_bf16 v[64:67], v[188:191], v[220:223], v[64:67]
	s_barrier
	s_cselect_b32 s71, 0, s72
	s_add_i32 s36, s71, s23
	s_ashr_i32 s37, s36, 31
	s_add_u32 s36, s10, s36
	s_addc_u32 s37, s11, s37
	s_add_i32 s72, s49, s34
	v_lshl_add_u64 v[224:225], s[36:37], 0, v[130:131]
	s_mov_b32 m0, s72
	ds_read_b128 v[192:195], v158 offset:16384
	ds_read_b128 v[196:199], v158 offset:17408
	ds_read_b128 v[200:203], v158 offset:18432
	ds_read_b128 v[204:207], v158 offset:19456
	ds_read_b128 v[208:211], v158 offset:20480
	ds_read_b128 v[212:215], v158 offset:21504
	ds_read_b128 v[216:219], v158 offset:22528
	ds_read_b128 v[220:223], v158 offset:23552
	global_load_lds_dwordx4 v[224:225], off
	s_add_i32 m0, s72, 0x2000
	s_add_i32 s72, s23, 0x40000
	v_lshl_add_u64 v[224:225], s[36:37], 0, v[132:133]
	s_add_i32 s36, s72, s71
	s_ashr_i32 s37, s36, 31
	s_add_u32 s36, s10, s36
	s_addc_u32 s37, s11, s37
	s_add_i32 s73, s58, s34
	global_load_lds_dwordx4 v[224:225], off
	v_lshl_add_u64 v[224:225], s[36:37], 0, v[130:131]
	s_mov_b32 m0, s73
	s_nop 0
	global_load_lds_dwordx4 v[224:225], off
	s_add_i32 m0, s73, 0x2000
	s_add_i32 s73, s71, s22
	v_lshl_add_u64 v[224:225], s[36:37], 0, v[132:133]
	s_add_u32 s36, s28, s73
	s_addc_u32 s37, s29, 0
	global_load_lds_dwordx4 v[224:225], off
	v_lshl_add_u64 v[224:225], s[36:37], 0, v[130:131]
	s_mov_b32 m0, s26
	s_nop 0
	global_load_lds_dwordx4 v[224:225], off
	v_lshl_add_u64 v[224:225], s[36:37], 0, v[132:133]
	s_mov_b32 m0, s27
	s_nop 0
	global_load_lds_dwordx4 v[224:225], off
	s_waitcnt vmcnt(8)
	s_waitcnt lgkmcnt(0)
	s_barrier
	s_waitcnt lgkmcnt(0)
	v_mfma_f32_16x16x32_bf16 v[60:63], v[160:163], v[192:195], v[60:63]
	v_mfma_f32_16x16x32_bf16 v[56:59], v[168:171], v[192:195], v[56:59]
	v_mfma_f32_16x16x32_bf16 v[44:47], v[160:163], v[200:203], v[44:47]
	v_mfma_f32_16x16x32_bf16 v[40:43], v[168:171], v[200:203], v[40:43]
	v_mfma_f32_16x16x32_bf16 v[28:31], v[160:163], v[208:211], v[28:31]
	v_mfma_f32_16x16x32_bf16 v[24:27], v[168:171], v[208:211], v[24:27]
	v_mfma_f32_16x16x32_bf16 v[12:15], v[160:163], v[216:219], v[12:15]
	v_mfma_f32_16x16x32_bf16 v[8:11], v[168:171], v[216:219], v[8:11]
	v_mfma_f32_16x16x32_bf16 v[60:63], v[164:167], v[196:199], v[60:63]
	v_mfma_f32_16x16x32_bf16 v[56:59], v[172:175], v[196:199], v[56:59]
	v_mfma_f32_16x16x32_bf16 v[44:47], v[164:167], v[204:207], v[44:47]
	v_mfma_f32_16x16x32_bf16 v[40:43], v[172:175], v[204:207], v[40:43]
	v_mfma_f32_16x16x32_bf16 v[28:31], v[164:167], v[212:215], v[28:31]
	v_mfma_f32_16x16x32_bf16 v[24:27], v[172:175], v[212:215], v[24:27]
	v_mfma_f32_16x16x32_bf16 v[12:15], v[164:167], v[220:223], v[12:15]
	v_mfma_f32_16x16x32_bf16 v[8:11], v[172:175], v[220:223], v[8:11]
	v_mfma_f32_16x16x32_bf16 v[52:55], v[176:179], v[192:195], v[52:55]
	v_mfma_f32_16x16x32_bf16 v[48:51], v[184:187], v[192:195], v[48:51]
	v_mfma_f32_16x16x32_bf16 v[36:39], v[176:179], v[200:203], v[36:39]
	v_mfma_f32_16x16x32_bf16 v[32:35], v[184:187], v[200:203], v[32:35]
	v_mfma_f32_16x16x32_bf16 v[20:23], v[176:179], v[208:211], v[20:23]
	v_mfma_f32_16x16x32_bf16 v[16:19], v[184:187], v[208:211], v[16:19]
	v_mfma_f32_16x16x32_bf16 v[4:7], v[176:179], v[216:219], v[4:7]
	v_mfma_f32_16x16x32_bf16 v[0:3], v[184:187], v[216:219], v[0:3]
	v_mfma_f32_16x16x32_bf16 v[52:55], v[180:183], v[196:199], v[52:55]
	v_mfma_f32_16x16x32_bf16 v[48:51], v[188:191], v[196:199], v[48:51]
	v_mfma_f32_16x16x32_bf16 v[36:39], v[180:183], v[204:207], v[36:39]
	v_mfma_f32_16x16x32_bf16 v[32:35], v[188:191], v[204:207], v[32:35]
	v_mfma_f32_16x16x32_bf16 v[20:23], v[180:183], v[212:215], v[20:23]
	v_mfma_f32_16x16x32_bf16 v[16:19], v[188:191], v[212:215], v[16:19]
	v_mfma_f32_16x16x32_bf16 v[4:7], v[180:183], v[220:223], v[4:7]
	v_mfma_f32_16x16x32_bf16 v[0:3], v[188:191], v[220:223], v[0:3]
	s_barrier
	s_add_i32 s74, 0, 0x18000
	v_add_u32_e32 v159, s74, v140
	s_add_i32 s75, 0, 0x1c000
	ds_read_b128 v[160:163], v159
	ds_read_b128 v[164:167], v159 offset:1024
	ds_read_b128 v[168:171], v159 offset:2048
	ds_read_b128 v[172:175], v159 offset:3072
	v_add_u32_e32 v159, s75, v140
	ds_read_b128 v[176:179], v159
	ds_read_b128 v[180:183], v159 offset:1024
	ds_read_b128 v[184:187], v159 offset:2048
	ds_read_b128 v[188:191], v159 offset:3072
	s_add_i32 s73, s73, 0x40000
	s_add_u32 s36, s28, s73
	s_addc_u32 s37, s29, 0
	s_mov_b32 m0, s33
	v_lshl_add_u64 v[224:225], s[36:37], 0, v[130:131]
	ds_read_b128 v[192:195], v158 offset:32768
	ds_read_b128 v[196:199], v158 offset:33792
	ds_read_b128 v[200:203], v158 offset:34816
	ds_read_b128 v[204:207], v158 offset:35840
	ds_read_b128 v[208:211], v158 offset:36864
	ds_read_b128 v[212:215], v158 offset:37888
	ds_read_b128 v[216:219], v158 offset:38912
	ds_read_b128 v[220:223], v158 offset:39936
	global_load_lds_dwordx4 v[224:225], off
	v_lshl_add_u64 v[224:225], s[36:37], 0, v[132:133]
	s_mov_b32 m0, s41
	s_nop 0
	global_load_lds_dwordx4 v[224:225], off
	s_waitcnt vmcnt(8)
	s_waitcnt lgkmcnt(0)
	s_barrier
	s_waitcnt lgkmcnt(0)
	v_mfma_f32_16x16x32_bf16 v[124:127], v[160:163], v[192:195], v[124:127]
	v_mfma_f32_16x16x32_bf16 v[120:123], v[168:171], v[192:195], v[120:123]
	v_mfma_f32_16x16x32_bf16 v[108:111], v[160:163], v[200:203], v[108:111]
	v_mfma_f32_16x16x32_bf16 v[104:107], v[168:171], v[200:203], v[104:107]
	v_mfma_f32_16x16x32_bf16 v[92:95], v[160:163], v[208:211], v[92:95]
	v_mfma_f32_16x16x32_bf16 v[88:91], v[168:171], v[208:211], v[88:91]
	v_mfma_f32_16x16x32_bf16 v[76:79], v[160:163], v[216:219], v[76:79]
	v_mfma_f32_16x16x32_bf16 v[72:75], v[168:171], v[216:219], v[72:75]
	v_mfma_f32_16x16x32_bf16 v[124:127], v[164:167], v[196:199], v[124:127]
	v_mfma_f32_16x16x32_bf16 v[120:123], v[172:175], v[196:199], v[120:123]
	v_mfma_f32_16x16x32_bf16 v[108:111], v[164:167], v[204:207], v[108:111]
	v_mfma_f32_16x16x32_bf16 v[104:107], v[172:175], v[204:207], v[104:107]
	v_mfma_f32_16x16x32_bf16 v[92:95], v[164:167], v[212:215], v[92:95]
	v_mfma_f32_16x16x32_bf16 v[88:91], v[172:175], v[212:215], v[88:91]
	v_mfma_f32_16x16x32_bf16 v[76:79], v[164:167], v[220:223], v[76:79]
	v_mfma_f32_16x16x32_bf16 v[72:75], v[172:175], v[220:223], v[72:75]
	v_mfma_f32_16x16x32_bf16 v[116:119], v[176:179], v[192:195], v[116:119]
	v_mfma_f32_16x16x32_bf16 v[112:115], v[184:187], v[192:195], v[112:115]
	v_mfma_f32_16x16x32_bf16 v[100:103], v[176:179], v[200:203], v[100:103]
	v_mfma_f32_16x16x32_bf16 v[96:99], v[184:187], v[200:203], v[96:99]
	v_mfma_f32_16x16x32_bf16 v[84:87], v[176:179], v[208:211], v[84:87]
	v_mfma_f32_16x16x32_bf16 v[80:83], v[184:187], v[208:211], v[80:83]
	v_mfma_f32_16x16x32_bf16 v[68:71], v[176:179], v[216:219], v[68:71]
	v_mfma_f32_16x16x32_bf16 v[64:67], v[184:187], v[216:219], v[64:67]
	v_mfma_f32_16x16x32_bf16 v[116:119], v[180:183], v[196:199], v[116:119]
	v_mfma_f32_16x16x32_bf16 v[112:115], v[188:191], v[196:199], v[112:115]
	v_mfma_f32_16x16x32_bf16 v[100:103], v[180:183], v[204:207], v[100:103]
	v_mfma_f32_16x16x32_bf16 v[96:99], v[188:191], v[204:207], v[96:99]
	v_mfma_f32_16x16x32_bf16 v[84:87], v[180:183], v[212:215], v[84:87]
	v_mfma_f32_16x16x32_bf16 v[80:83], v[188:191], v[212:215], v[80:83]
	v_mfma_f32_16x16x32_bf16 v[68:71], v[180:183], v[220:223], v[68:71]
	v_mfma_f32_16x16x32_bf16 v[64:67], v[188:191], v[220:223], v[64:67]
	s_barrier
; template <class Epi, class Sched, class Hook = NoHook>
; __device__ __forceinline__ void gemm_phase_w(LAS unsigned char* lds, const Sched& S, const Epi& E, int wave_id, const Hook& HK = Hook()) {
;     ...
;         if constexpr (!SEG2) {
;             for (int tt = 0; tt < nt; tt += 2) {
;                 if constexpr (GATHER) { if (tt == nt - 2) {
;                     if (has_next) { gnxt_00 = S.grow_l(nxt, lds, nbuf, R0) + (unsigned)(C0 * 2); gnxt_01 = S.grow_l(nxt, lds, nbuf, R1) + (unsigned)(C1 * 2); gnxt_10 = S.grow_l(nxt, lds, nbuf, 128 + R0) + (unsigned)(C0 * 2); gnxt_11 = S.grow_l(nxt, lds, nbuf, 128 + R1) + (unsigned)(C1 * 2); }
;                     else { gnxt_00 = gcur_00; gnxt_01 = gcur_01; gnxt_10 = gcur_10; gnxt_11 = gcur_11; } } }
;                 PG_TRIP(tt, false, false, false);
;             }
	s_bitset1_b32 s71, 7
	s_add_i32 s23, s71, s23
	s_ashr_i32 s37, s23, 31
	s_add_u32 s36, s10, s23
	s_addc_u32 s37, s11, s37
	s_add_i32 s23, s74, s34
	v_lshl_add_u64 v[224:225], s[36:37], 0, v[130:131]
	s_mov_b32 m0, s23
	ds_read_b128 v[192:195], v158 offset:49152
	ds_read_b128 v[196:199], v158 offset:50176
	ds_read_b128 v[200:203], v158 offset:51200
	ds_read_b128 v[204:207], v158 offset:52224
	ds_read_b128 v[208:211], v158 offset:53248
	ds_read_b128 v[212:215], v158 offset:54272
	ds_read_b128 v[216:219], v158 offset:55296
	ds_read_b128 v[220:223], v158 offset:56320
	global_load_lds_dwordx4 v[224:225], off
	s_add_i32 m0, s23, 0x2000
	s_add_i32 s23, s71, s72
	v_lshl_add_u64 v[224:225], s[36:37], 0, v[132:133]
	s_ashr_i32 s37, s23, 31
	s_add_u32 s36, s10, s23
	s_addc_u32 s37, s11, s37
	s_add_i32 s23, s75, s34
	global_load_lds_dwordx4 v[224:225], off
	v_lshl_add_u64 v[224:225], s[36:37], 0, v[130:131]
	s_mov_b32 m0, s23
	s_add_i32 s71, s71, s22
	global_load_lds_dwordx4 v[224:225], off
	s_add_i32 m0, s23, 0x2000
	s_add_u32 s22, s28, s71
	v_lshl_add_u64 v[224:225], s[36:37], 0, v[132:133]
	s_addc_u32 s23, s29, 0
	global_load_lds_dwordx4 v[224:225], off
	v_lshl_add_u64 v[224:225], s[22:23], 0, v[130:131]
	s_mov_b32 m0, s42
	s_nop 0
	global_load_lds_dwordx4 v[224:225], off
	v_lshl_add_u64 v[224:225], s[22:23], 0, v[132:133]
	s_mov_b32 m0, s43
	s_nop 0
	global_load_lds_dwordx4 v[224:225], off
	s_waitcnt vmcnt(8)
	s_waitcnt lgkmcnt(0)
	s_barrier
	s_waitcnt lgkmcnt(0)
	v_mfma_f32_16x16x32_bf16 v[60:63], v[160:163], v[192:195], v[60:63]
	v_mfma_f32_16x16x32_bf16 v[56:59], v[168:171], v[192:195], v[56:59]
	v_mfma_f32_16x16x32_bf16 v[44:47], v[160:163], v[200:203], v[44:47]
	v_mfma_f32_16x16x32_bf16 v[40:43], v[168:171], v[200:203], v[40:43]
	v_mfma_f32_16x16x32_bf16 v[28:31], v[160:163], v[208:211], v[28:31]
	v_mfma_f32_16x16x32_bf16 v[24:27], v[168:171], v[208:211], v[24:27]
	v_mfma_f32_16x16x32_bf16 v[12:15], v[160:163], v[216:219], v[12:15]
	v_mfma_f32_16x16x32_bf16 v[8:11], v[168:171], v[216:219], v[8:11]
	v_mfma_f32_16x16x32_bf16 v[60:63], v[164:167], v[196:199], v[60:63]
	v_mfma_f32_16x16x32_bf16 v[56:59], v[172:175], v[196:199], v[56:59]
	v_mfma_f32_16x16x32_bf16 v[44:47], v[164:167], v[204:207], v[44:47]
	v_mfma_f32_16x16x32_bf16 v[40:43], v[172:175], v[204:207], v[40:43]
	v_mfma_f32_16x16x32_bf16 v[28:31], v[164:167], v[212:215], v[28:31]
	v_mfma_f32_16x16x32_bf16 v[24:27], v[172:175], v[212:215], v[24:27]
	v_mfma_f32_16x16x32_bf16 v[12:15], v[164:167], v[220:223], v[12:15]
	v_mfma_f32_16x16x32_bf16 v[8:11], v[172:175], v[220:223], v[8:11]
	v_mfma_f32_16x16x32_bf16 v[52:55], v[176:179], v[192:195], v[52:55]
	v_mfma_f32_16x16x32_bf16 v[48:51], v[184:187], v[192:195], v[48:51]
	v_mfma_f32_16x16x32_bf16 v[36:39], v[176:179], v[200:203], v[36:39]
	v_mfma_f32_16x16x32_bf16 v[32:35], v[184:187], v[200:203], v[32:35]
	v_mfma_f32_16x16x32_bf16 v[20:23], v[176:179], v[208:211], v[20:23]
	v_mfma_f32_16x16x32_bf16 v[16:19], v[184:187], v[208:211], v[16:19]
	v_mfma_f32_16x16x32_bf16 v[4:7], v[176:179], v[216:219], v[4:7]
	v_mfma_f32_16x16x32_bf16 v[0:3], v[184:187], v[216:219], v[0:3]
	v_mfma_f32_16x16x32_bf16 v[52:55], v[180:183], v[196:199], v[52:55]
	v_mfma_f32_16x16x32_bf16 v[48:51], v[188:191], v[196:199], v[48:51]
	v_mfma_f32_16x16x32_bf16 v[36:39], v[180:183], v[204:207], v[36:39]
	v_mfma_f32_16x16x32_bf16 v[32:35], v[188:191], v[204:207], v[32:35]
	v_mfma_f32_16x16x32_bf16 v[20:23], v[180:183], v[212:215], v[20:23]
	v_mfma_f32_16x16x32_bf16 v[16:19], v[188:191], v[212:215], v[16:19]
	v_mfma_f32_16x16x32_bf16 v[4:7], v[180:183], v[220:223], v[4:7]
	v_mfma_f32_16x16x32_bf16 v[0:3], v[188:191], v[220:223], v[0:3]
	s_addk_i32 s12, 0x100
	s_add_i32 s19, s19, 2
	s_cmp_gt_u32 s19, 13
	s_barrier
	s_cbranch_scc0 .LBB0_1194
	s_and_b64 vcc, exec, s[0:1]
	s_cbranch_vccz .LBB0_1197
	s_barrier

.LBB0_1442:
	ds_read_b128 v[156:159], v153
	ds_read_b128 v[160:163], v153 offset:1024
	ds_read_b128 v[164:167], v153 offset:2048
	ds_read_b128 v[168:171], v153 offset:3072
	ds_read_b128 v[172:175], v154
	ds_read_b128 v[176:179], v154 offset:1024
	ds_read_b128 v[180:183], v154 offset:2048
	ds_read_b128 v[184:187], v154 offset:3072
	s_add_i32 s22, s61, s12
	s_add_u32 s66, s28, s22
	s_addc_u32 s67, s29, 0
	s_add_i32 m0, s33, 0xc000
	s_add_i32 s68, s33, 0xe000
	s_add_i32 s69, s12, 0xfffc0080
	s_cmp_eq_u32 s19, 12
	s_cselect_b32 s22, s58, s61
	s_cselect_b32 s23, s59, s62
	v_lshl_add_u64 v[220:221], s[66:67], 0, v[130:131]
	ds_read_b128 v[188:191], v155
	ds_read_b128 v[192:195], v155 offset:1024
	ds_read_b128 v[196:199], v155 offset:2048
	ds_read_b128 v[200:203], v155 offset:3072
	ds_read_b128 v[204:207], v155 offset:4096
	ds_read_b128 v[208:211], v155 offset:5120
	ds_read_b128 v[212:215], v155 offset:6144
	ds_read_b128 v[216:219], v155 offset:7168
	global_load_lds_dwordx4 v[220:221], off
	v_lshl_add_u64 v[220:221], s[66:67], 0, v[132:133]
	s_mov_b32 m0, s68
	s_nop 0
	global_load_lds_dwordx4 v[220:221], off
	s_waitcnt vmcnt(8)
	s_waitcnt lgkmcnt(0)
	s_barrier
	s_waitcnt lgkmcnt(0)
	v_mfma_f32_16x16x32_bf16 v[124:127], v[156:159], v[188:191], v[124:127]
	v_mfma_f32_16x16x32_bf16 v[120:123], v[164:167], v[188:191], v[120:123]
	v_mfma_f32_16x16x32_bf16 v[108:111], v[156:159], v[196:199], v[108:111]
	v_mfma_f32_16x16x32_bf16 v[104:107], v[164:167], v[196:199], v[104:107]
	v_mfma_f32_16x16x32_bf16 v[92:95], v[156:159], v[204:207], v[92:95]
	v_mfma_f32_16x16x32_bf16 v[88:91], v[164:167], v[204:207], v[88:91]
	v_mfma_f32_16x16x32_bf16 v[76:79], v[156:159], v[212:215], v[76:79]
	v_mfma_f32_16x16x32_bf16 v[72:75], v[164:167], v[212:215], v[72:75]
	v_mfma_f32_16x16x32_bf16 v[124:127], v[160:163], v[192:195], v[124:127]
	v_mfma_f32_16x16x32_bf16 v[120:123], v[168:171], v[192:195], v[120:123]
	v_mfma_f32_16x16x32_bf16 v[108:111], v[160:163], v[200:203], v[108:111]
	v_mfma_f32_16x16x32_bf16 v[104:107], v[168:171], v[200:203], v[104:107]
	v_mfma_f32_16x16x32_bf16 v[92:95], v[160:163], v[208:211], v[92:95]
	v_mfma_f32_16x16x32_bf16 v[88:91], v[168:171], v[208:211], v[88:91]
	v_mfma_f32_16x16x32_bf16 v[76:79], v[160:163], v[216:219], v[76:79]
	v_mfma_f32_16x16x32_bf16 v[72:75], v[168:171], v[216:219], v[72:75]
	v_mfma_f32_16x16x32_bf16 v[116:119], v[172:175], v[188:191], v[116:119]
	v_mfma_f32_16x16x32_bf16 v[112:115], v[180:183], v[188:191], v[112:115]
	v_mfma_f32_16x16x32_bf16 v[100:103], v[172:175], v[196:199], v[100:103]
	v_mfma_f32_16x16x32_bf16 v[96:99], v[180:183], v[196:199], v[96:99]
	v_mfma_f32_16x16x32_bf16 v[84:87], v[172:175], v[204:207], v[84:87]
	v_mfma_f32_16x16x32_bf16 v[80:83], v[180:183], v[204:207], v[80:83]
	v_mfma_f32_16x16x32_bf16 v[68:71], v[172:175], v[212:215], v[68:71]
	v_mfma_f32_16x16x32_bf16 v[64:67], v[180:183], v[212:215], v[64:67]
	v_mfma_f32_16x16x32_bf16 v[116:119], v[176:179], v[192:195], v[116:119]
	v_mfma_f32_16x16x32_bf16 v[112:115], v[184:187], v[192:195], v[112:115]
	v_mfma_f32_16x16x32_bf16 v[100:103], v[176:179], v[200:203], v[100:103]
	v_mfma_f32_16x16x32_bf16 v[96:99], v[184:187], v[200:203], v[96:99]
	v_mfma_f32_16x16x32_bf16 v[84:87], v[176:179], v[208:211], v[84:87]
	v_mfma_f32_16x16x32_bf16 v[80:83], v[184:187], v[208:211], v[80:83]
	v_mfma_f32_16x16x32_bf16 v[68:71], v[176:179], v[216:219], v[68:71]
	v_mfma_f32_16x16x32_bf16 v[64:67], v[184:187], v[216:219], v[64:67]
	s_barrier
	s_cselect_b32 s68, 0, s69
	s_add_i32 s66, s68, s23
	s_ashr_i32 s67, s66, 31
	s_add_u32 s66, s10, s66
	s_addc_u32 s67, s11, s67
	s_add_i32 s69, s37, s34
	v_lshl_add_u64 v[220:221], s[66:67], 0, v[130:131]
	s_mov_b32 m0, s69
	ds_read_b128 v[188:191], v155 offset:16384
	ds_read_b128 v[192:195], v155 offset:17408
	ds_read_b128 v[196:199], v155 offset:18432
	ds_read_b128 v[200:203], v155 offset:19456
	ds_read_b128 v[204:207], v155 offset:20480
	ds_read_b128 v[208:211], v155 offset:21504
	ds_read_b128 v[212:215], v155 offset:22528
	ds_read_b128 v[216:219], v155 offset:23552
	global_load_lds_dwordx4 v[220:221], off
	s_add_i32 m0, s69, 0x2000
	s_add_i32 s69, s23, 0x40000
	v_lshl_add_u64 v[220:221], s[66:67], 0, v[132:133]
	s_add_i32 s66, s69, s68
	s_ashr_i32 s67, s66, 31
	s_add_u32 s66, s10, s66
	s_addc_u32 s67, s11, s67
	s_add_i32 s70, s38, s34
	global_load_lds_dwordx4 v[220:221], off
	v_lshl_add_u64 v[220:221], s[66:67], 0, v[130:131]
	s_mov_b32 m0, s70
	s_nop 0
	global_load_lds_dwordx4 v[220:221], off
	s_add_i32 m0, s70, 0x2000
	s_add_i32 s70, s68, s22
	v_lshl_add_u64 v[220:221], s[66:67], 0, v[132:133]
	s_add_u32 s66, s28, s70
	s_addc_u32 s67, s29, 0
	global_load_lds_dwordx4 v[220:221], off
	v_lshl_add_u64 v[220:221], s[66:67], 0, v[130:131]
	s_mov_b32 m0, s33
	s_nop 0
	global_load_lds_dwordx4 v[220:221], off
	v_lshl_add_u64 v[220:221], s[66:67], 0, v[132:133]
	s_mov_b32 m0, s40
	s_nop 0
	global_load_lds_dwordx4 v[220:221], off
	s_waitcnt vmcnt(8)
	s_waitcnt lgkmcnt(0)
	s_barrier
	s_waitcnt lgkmcnt(0)
	v_mfma_f32_16x16x32_bf16 v[60:63], v[156:159], v[188:191], v[60:63]
	v_mfma_f32_16x16x32_bf16 v[56:59], v[164:167], v[188:191], v[56:59]
	v_mfma_f32_16x16x32_bf16 v[44:47], v[156:159], v[196:199], v[44:47]
	v_mfma_f32_16x16x32_bf16 v[40:43], v[164:167], v[196:199], v[40:43]
	v_mfma_f32_16x16x32_bf16 v[28:31], v[156:159], v[204:207], v[28:31]
	v_mfma_f32_16x16x32_bf16 v[24:27], v[164:167], v[204:207], v[24:27]
	v_mfma_f32_16x16x32_bf16 v[12:15], v[156:159], v[212:215], v[12:15]
	v_mfma_f32_16x16x32_bf16 v[8:11], v[164:167], v[212:215], v[8:11]
	v_mfma_f32_16x16x32_bf16 v[60:63], v[160:163], v[192:195], v[60:63]
	v_mfma_f32_16x16x32_bf16 v[56:59], v[168:171], v[192:195], v[56:59]
	v_mfma_f32_16x16x32_bf16 v[44:47], v[160:163], v[200:203], v[44:47]
	v_mfma_f32_16x16x32_bf16 v[40:43], v[168:171], v[200:203], v[40:43]
	v_mfma_f32_16x16x32_bf16 v[28:31], v[160:163], v[208:211], v[28:31]
	v_mfma_f32_16x16x32_bf16 v[24:27], v[168:171], v[208:211], v[24:27]
	v_mfma_f32_16x16x32_bf16 v[12:15], v[160:163], v[216:219], v[12:15]
	v_mfma_f32_16x16x32_bf16 v[8:11], v[168:171], v[216:219], v[8:11]
	v_mfma_f32_16x16x32_bf16 v[52:55], v[172:175], v[188:191], v[52:55]
	v_mfma_f32_16x16x32_bf16 v[48:51], v[180:183], v[188:191], v[48:51]
	v_mfma_f32_16x16x32_bf16 v[36:39], v[172:175], v[196:199], v[36:39]
	v_mfma_f32_16x16x32_bf16 v[32:35], v[180:183], v[196:199], v[32:35]
	v_mfma_f32_16x16x32_bf16 v[20:23], v[172:175], v[204:207], v[20:23]
	v_mfma_f32_16x16x32_bf16 v[16:19], v[180:183], v[204:207], v[16:19]
	v_mfma_f32_16x16x32_bf16 v[4:7], v[172:175], v[212:215], v[4:7]
	v_mfma_f32_16x16x32_bf16 v[0:3], v[180:183], v[212:215], v[0:3]
	v_mfma_f32_16x16x32_bf16 v[52:55], v[176:179], v[192:195], v[52:55]
	v_mfma_f32_16x16x32_bf16 v[48:51], v[184:187], v[192:195], v[48:51]
	v_mfma_f32_16x16x32_bf16 v[36:39], v[176:179], v[200:203], v[36:39]
	v_mfma_f32_16x16x32_bf16 v[32:35], v[184:187], v[200:203], v[32:35]
	v_mfma_f32_16x16x32_bf16 v[20:23], v[176:179], v[208:211], v[20:23]
	v_mfma_f32_16x16x32_bf16 v[16:19], v[184:187], v[208:211], v[16:19]
	v_mfma_f32_16x16x32_bf16 v[4:7], v[176:179], v[216:219], v[4:7]
	v_mfma_f32_16x16x32_bf16 v[0:3], v[184:187], v[216:219], v[0:3]
	s_barrier
	s_add_i32 s71, 0, 0x18000
	s_add_i32 s72, 0, 0x1c000
	v_add_u32_e32 v168, s71, v137
	v_add_u32_e32 v184, s72, v137
	ds_read_b128 v[156:159], v168
	ds_read_b128 v[160:163], v168 offset:1024
	ds_read_b128 v[164:167], v168 offset:2048
	ds_read_b128 v[168:171], v168 offset:3072
	ds_read_b128 v[172:175], v184
	ds_read_b128 v[176:179], v184 offset:1024
	ds_read_b128 v[180:183], v184 offset:2048
	ds_read_b128 v[184:187], v184 offset:3072
	s_add_i32 s70, s70, 0x40000
	s_add_u32 s66, s28, s70
	s_addc_u32 s67, s29, 0
	s_mov_b32 m0, s41
	v_lshl_add_u64 v[220:221], s[66:67], 0, v[130:131]
	ds_read_b128 v[188:191], v155 offset:32768
	ds_read_b128 v[192:195], v155 offset:33792
	ds_read_b128 v[196:199], v155 offset:34816
	ds_read_b128 v[200:203], v155 offset:35840
	ds_read_b128 v[204:207], v155 offset:36864
	ds_read_b128 v[208:211], v155 offset:37888
	ds_read_b128 v[212:215], v155 offset:38912
	ds_read_b128 v[216:219], v155 offset:39936
	global_load_lds_dwordx4 v[220:221], off
	v_lshl_add_u64 v[220:221], s[66:67], 0, v[132:133]
	s_mov_b32 m0, s42
	s_nop 0
	global_load_lds_dwordx4 v[220:221], off
	s_waitcnt vmcnt(8)
	s_waitcnt lgkmcnt(0)
	s_barrier
	s_waitcnt lgkmcnt(0)
	v_mfma_f32_16x16x32_bf16 v[124:127], v[156:159], v[188:191], v[124:127]
	v_mfma_f32_16x16x32_bf16 v[120:123], v[164:167], v[188:191], v[120:123]
	v_mfma_f32_16x16x32_bf16 v[108:111], v[156:159], v[196:199], v[108:111]
	v_mfma_f32_16x16x32_bf16 v[104:107], v[164:167], v[196:199], v[104:107]
	v_mfma_f32_16x16x32_bf16 v[92:95], v[156:159], v[204:207], v[92:95]
	v_mfma_f32_16x16x32_bf16 v[88:91], v[164:167], v[204:207], v[88:91]
	v_mfma_f32_16x16x32_bf16 v[76:79], v[156:159], v[212:215], v[76:79]
	v_mfma_f32_16x16x32_bf16 v[72:75], v[164:167], v[212:215], v[72:75]
	v_mfma_f32_16x16x32_bf16 v[124:127], v[160:163], v[192:195], v[124:127]
	v_mfma_f32_16x16x32_bf16 v[120:123], v[168:171], v[192:195], v[120:123]
	v_mfma_f32_16x16x32_bf16 v[108:111], v[160:163], v[200:203], v[108:111]
	v_mfma_f32_16x16x32_bf16 v[104:107], v[168:171], v[200:203], v[104:107]
	v_mfma_f32_16x16x32_bf16 v[92:95], v[160:163], v[208:211], v[92:95]
	v_mfma_f32_16x16x32_bf16 v[88:91], v[168:171], v[208:211], v[88:91]
	v_mfma_f32_16x16x32_bf16 v[76:79], v[160:163], v[216:219], v[76:79]
	v_mfma_f32_16x16x32_bf16 v[72:75], v[168:171], v[216:219], v[72:75]
	v_mfma_f32_16x16x32_bf16 v[116:119], v[172:175], v[188:191], v[116:119]
	v_mfma_f32_16x16x32_bf16 v[112:115], v[180:183], v[188:191], v[112:115]
	v_mfma_f32_16x16x32_bf16 v[100:103], v[172:175], v[196:199], v[100:103]
	v_mfma_f32_16x16x32_bf16 v[96:99], v[180:183], v[196:199], v[96:99]
	v_mfma_f32_16x16x32_bf16 v[84:87], v[172:175], v[204:207], v[84:87]
	v_mfma_f32_16x16x32_bf16 v[80:83], v[180:183], v[204:207], v[80:83]
	v_mfma_f32_16x16x32_bf16 v[68:71], v[172:175], v[212:215], v[68:71]
	v_mfma_f32_16x16x32_bf16 v[64:67], v[180:183], v[212:215], v[64:67]
	v_mfma_f32_16x16x32_bf16 v[116:119], v[176:179], v[192:195], v[116:119]
	v_mfma_f32_16x16x32_bf16 v[112:115], v[184:187], v[192:195], v[112:115]
	v_mfma_f32_16x16x32_bf16 v[100:103], v[176:179], v[200:203], v[100:103]
	v_mfma_f32_16x16x32_bf16 v[96:99], v[184:187], v[200:203], v[96:99]
	v_mfma_f32_16x16x32_bf16 v[84:87], v[176:179], v[208:211], v[84:87]
	v_mfma_f32_16x16x32_bf16 v[80:83], v[184:187], v[208:211], v[80:83]
	v_mfma_f32_16x16x32_bf16 v[68:71], v[176:179], v[216:219], v[68:71]
	v_mfma_f32_16x16x32_bf16 v[64:67], v[184:187], v[216:219], v[64:67]
	s_barrier
; #define PG_BAR __builtin_amdgcn_s_barrier()
; template <class Epi, class Sched, class Hook = NoHook>
; __device__ __forceinline__ void gemm_phase_w(LAS unsigned char* lds, const Sched& S, const Epi& E, int wave_id, const Hook& HK = Hook()) {
;     ...
;         if constexpr (!SEG2) {
;             for (int tt = 0; tt < nt; tt += 2) {
;                 if constexpr (GATHER) { if (tt == nt - 2) {
;                     if (has_next) { gnxt_00 = S.grow_l(nxt, lds, nbuf, R0) + (unsigned)(C0 * 2); gnxt_01 = S.grow_l(nxt, lds, nbuf, R1) + (unsigned)(C1 * 2); gnxt_10 = S.grow_l(nxt, lds, nbuf, 128 + R0) + (unsigned)(C0 * 2); gnxt_11 = S.grow_l(nxt, lds, nbuf, 128 + R1) + (unsigned)(C1 * 2); }
;                     else { gnxt_00 = gcur_00; gnxt_01 = gcur_01; gnxt_10 = gcur_10; gnxt_11 = gcur_11; } } }
;                 PG_TRIP(tt, false, false, false);
;             }
;         } else {
;             for (int tt = 0; tt < nt - 4; tt += 2) PG_TRIP(tt, false, false, false);
;             PG_TRIP(nt - 4, false, true, false);
;             PG_TRIP(nt - 2, true, false, true);
;         }
;     ...
;         if (wr == 0) PG_BAR;
	s_bitset1_b32 s68, 7
	s_add_i32 s23, s68, s23
	s_ashr_i32 s67, s23, 31
	s_add_u32 s66, s10, s23
	s_addc_u32 s67, s11, s67
	s_add_i32 s23, s71, s34
	v_lshl_add_u64 v[220:221], s[66:67], 0, v[130:131]
	s_mov_b32 m0, s23
	ds_read_b128 v[188:191], v155 offset:49152
	ds_read_b128 v[192:195], v155 offset:50176
	ds_read_b128 v[196:199], v155 offset:51200
	ds_read_b128 v[200:203], v155 offset:52224
	ds_read_b128 v[204:207], v155 offset:53248
	ds_read_b128 v[208:211], v155 offset:54272
	ds_read_b128 v[212:215], v155 offset:55296
	ds_read_b128 v[216:219], v155 offset:56320
	global_load_lds_dwordx4 v[220:221], off
	s_add_i32 m0, s23, 0x2000
	s_add_i32 s23, s68, s69
	v_lshl_add_u64 v[220:221], s[66:67], 0, v[132:133]
	s_ashr_i32 s67, s23, 31
	s_add_u32 s66, s10, s23
	s_addc_u32 s67, s11, s67
	s_add_i32 s23, s72, s34
	global_load_lds_dwordx4 v[220:221], off
	v_lshl_add_u64 v[220:221], s[66:67], 0, v[130:131]
	s_mov_b32 m0, s23
	s_add_i32 s68, s68, s22
	global_load_lds_dwordx4 v[220:221], off
	s_add_i32 m0, s23, 0x2000
	s_add_u32 s22, s28, s68
	v_lshl_add_u64 v[220:221], s[66:67], 0, v[132:133]
	s_addc_u32 s23, s29, 0
	global_load_lds_dwordx4 v[220:221], off
	v_lshl_add_u64 v[220:221], s[22:23], 0, v[130:131]
	s_mov_b32 m0, s39
	s_nop 0
	global_load_lds_dwordx4 v[220:221], off
	v_lshl_add_u64 v[220:221], s[22:23], 0, v[132:133]
	s_mov_b32 m0, s43
	s_nop 0
	global_load_lds_dwordx4 v[220:221], off
	s_waitcnt vmcnt(8)
	s_waitcnt lgkmcnt(0)
	s_barrier
	s_waitcnt lgkmcnt(0)
	v_mfma_f32_16x16x32_bf16 v[60:63], v[156:159], v[188:191], v[60:63]
	v_mfma_f32_16x16x32_bf16 v[56:59], v[164:167], v[188:191], v[56:59]
	v_mfma_f32_16x16x32_bf16 v[44:47], v[156:159], v[196:199], v[44:47]
	v_mfma_f32_16x16x32_bf16 v[40:43], v[164:167], v[196:199], v[40:43]
	v_mfma_f32_16x16x32_bf16 v[28:31], v[156:159], v[204:207], v[28:31]
	v_mfma_f32_16x16x32_bf16 v[24:27], v[164:167], v[204:207], v[24:27]
	v_mfma_f32_16x16x32_bf16 v[12:15], v[156:159], v[212:215], v[12:15]
	v_mfma_f32_16x16x32_bf16 v[8:11], v[164:167], v[212:215], v[8:11]
	v_mfma_f32_16x16x32_bf16 v[60:63], v[160:163], v[192:195], v[60:63]
	v_mfma_f32_16x16x32_bf16 v[56:59], v[168:171], v[192:195], v[56:59]
	v_mfma_f32_16x16x32_bf16 v[44:47], v[160:163], v[200:203], v[44:47]
	v_mfma_f32_16x16x32_bf16 v[40:43], v[168:171], v[200:203], v[40:43]
	v_mfma_f32_16x16x32_bf16 v[28:31], v[160:163], v[208:211], v[28:31]
	v_mfma_f32_16x16x32_bf16 v[24:27], v[168:171], v[208:211], v[24:27]
	v_mfma_f32_16x16x32_bf16 v[12:15], v[160:163], v[216:219], v[12:15]
	v_mfma_f32_16x16x32_bf16 v[8:11], v[168:171], v[216:219], v[8:11]
	v_mfma_f32_16x16x32_bf16 v[52:55], v[172:175], v[188:191], v[52:55]
	v_mfma_f32_16x16x32_bf16 v[48:51], v[180:183], v[188:191], v[48:51]
	v_mfma_f32_16x16x32_bf16 v[36:39], v[172:175], v[196:199], v[36:39]
	v_mfma_f32_16x16x32_bf16 v[32:35], v[180:183], v[196:199], v[32:35]
	v_mfma_f32_16x16x32_bf16 v[20:23], v[172:175], v[204:207], v[20:23]
	v_mfma_f32_16x16x32_bf16 v[16:19], v[180:183], v[204:207], v[16:19]
	v_mfma_f32_16x16x32_bf16 v[4:7], v[172:175], v[212:215], v[4:7]
	v_mfma_f32_16x16x32_bf16 v[0:3], v[180:183], v[212:215], v[0:3]
	v_mfma_f32_16x16x32_bf16 v[52:55], v[176:179], v[192:195], v[52:55]
	v_mfma_f32_16x16x32_bf16 v[48:51], v[184:187], v[192:195], v[48:51]
	v_mfma_f32_16x16x32_bf16 v[36:39], v[176:179], v[200:203], v[36:39]
	v_mfma_f32_16x16x32_bf16 v[32:35], v[184:187], v[200:203], v[32:35]
	v_mfma_f32_16x16x32_bf16 v[20:23], v[176:179], v[208:211], v[20:23]
	v_mfma_f32_16x16x32_bf16 v[16:19], v[184:187], v[208:211], v[16:19]
	v_mfma_f32_16x16x32_bf16 v[4:7], v[176:179], v[216:219], v[4:7]
	v_mfma_f32_16x16x32_bf16 v[0:3], v[184:187], v[216:219], v[0:3]
	s_addk_i32 s12, 0x100
	s_add_i32 s19, s19, 2
	s_cmp_gt_u32 s19, 13
	s_barrier
	s_cbranch_scc0 .LBB0_1442
	s_and_b64 vcc, exec, s[0:1]
	s_cbranch_vccz .LBB0_1445
	s_barrier

.LBB0_1585:
	ds_read_b128 v[82:85], v75
	ds_read_b128 v[86:89], v75 offset:1024
	ds_read_b128 v[90:93], v75 offset:2048
	ds_read_b128 v[94:97], v75 offset:3072
	s_add_i32 s61, s39, s20
	s_add_u32 s62, s8, s61
	s_addc_u32 s63, s9, 0
	s_add_i32 s61, s20, 0xfffe0080
	s_cmp_eq_u32 s21, 4
	s_cselect_b32 s66, s59, s39
	s_cselect_b32 s67, s51, s60
	s_cselect_b32 s68, s58, s38
	s_mov_b32 m0, s40
	v_lshl_add_u64 v[130:131], s[62:63], 0, v[64:65]
	ds_read_b128 v[98:101], v76
	ds_read_b128 v[102:105], v76 offset:1024
	ds_read_b128 v[106:109], v76 offset:2048
	ds_read_b128 v[110:113], v76 offset:3072
	ds_read_b128 v[114:117], v76 offset:4096
	ds_read_b128 v[118:121], v76 offset:5120
	ds_read_b128 v[122:125], v76 offset:6144
	ds_read_b128 v[126:129], v76 offset:7168
	global_load_lds_dwordx4 v[130:131], off
	v_lshl_add_u64 v[130:131], s[62:63], 0, v[66:67]
	s_mov_b32 m0, s41
	s_nop 0
	global_load_lds_dwordx4 v[130:131], off
	s_waitcnt vmcnt(8)
	s_waitcnt lgkmcnt(0)
	s_barrier
	s_waitcnt lgkmcnt(0)
	v_mfma_f32_16x16x32_bf16 v[60:63], v[82:85], v[98:101], v[60:63]
	v_mfma_f32_16x16x32_bf16 v[56:59], v[90:93], v[98:101], v[56:59]
	v_mfma_f32_16x16x32_bf16 v[52:55], v[82:85], v[106:109], v[52:55]
	v_mfma_f32_16x16x32_bf16 v[48:51], v[90:93], v[106:109], v[48:51]
	v_mfma_f32_16x16x32_bf16 v[44:47], v[82:85], v[114:117], v[44:47]
	v_mfma_f32_16x16x32_bf16 v[40:43], v[90:93], v[114:117], v[40:43]
	v_mfma_f32_16x16x32_bf16 v[36:39], v[82:85], v[122:125], v[36:39]
	v_mfma_f32_16x16x32_bf16 v[32:35], v[90:93], v[122:125], v[32:35]
	v_mfma_f32_16x16x32_bf16 v[60:63], v[86:89], v[102:105], v[60:63]
	v_mfma_f32_16x16x32_bf16 v[56:59], v[94:97], v[102:105], v[56:59]
	v_mfma_f32_16x16x32_bf16 v[52:55], v[86:89], v[110:113], v[52:55]
	v_mfma_f32_16x16x32_bf16 v[48:51], v[94:97], v[110:113], v[48:51]
	v_mfma_f32_16x16x32_bf16 v[44:47], v[86:89], v[118:121], v[44:47]
	v_mfma_f32_16x16x32_bf16 v[40:43], v[94:97], v[118:121], v[40:43]
	v_mfma_f32_16x16x32_bf16 v[36:39], v[86:89], v[126:129], v[36:39]
	v_mfma_f32_16x16x32_bf16 v[32:35], v[94:97], v[126:129], v[32:35]
	s_barrier
	s_cselect_b32 s61, 0, s61
	s_add_i32 s62, s61, s68
	s_ashr_i32 s63, s62, 31
	s_add_u32 s62, s3, s62
	s_addc_u32 s63, s22, s63
	s_mov_b32 m0, s42
	v_lshl_add_u64 v[130:131], s[62:63], 0, v[64:65]
	s_add_i32 s67, s68, s67
	ds_read_b128 v[98:101], v76 offset:16384
	ds_read_b128 v[102:105], v76 offset:17408
	ds_read_b128 v[106:109], v76 offset:18432
	ds_read_b128 v[110:113], v76 offset:19456
	ds_read_b128 v[114:117], v76 offset:20480
	ds_read_b128 v[118:121], v76 offset:21504
	ds_read_b128 v[122:125], v76 offset:22528
	ds_read_b128 v[126:129], v76 offset:23552
	global_load_lds_dwordx4 v[130:131], off
	v_lshl_add_u64 v[130:131], s[62:63], 0, v[66:67]
	s_add_i32 s62, s67, s61
	s_ashr_i32 s63, s62, 31
	s_add_u32 s62, s3, s62
	s_mov_b32 m0, s43
	s_addc_u32 s63, s22, s63
	global_load_lds_dwordx4 v[130:131], off
	v_lshl_add_u64 v[130:131], s[62:63], 0, v[64:65]
	s_mov_b32 m0, s24
	s_add_i32 s69, s61, s66
	global_load_lds_dwordx4 v[130:131], off
	v_lshl_add_u64 v[130:131], s[62:63], 0, v[66:67]
	s_add_u32 s62, s8, s69
	s_mov_b32 m0, s25
	s_addc_u32 s63, s9, 0
	global_load_lds_dwordx4 v[130:131], off
	v_lshl_add_u64 v[130:131], s[62:63], 0, v[64:65]
	s_mov_b32 m0, s23
	s_nop 0
	global_load_lds_dwordx4 v[130:131], off
	v_lshl_add_u64 v[130:131], s[62:63], 0, v[66:67]
	s_mov_b32 m0, s28
	s_nop 0
	global_load_lds_dwordx4 v[130:131], off
	s_waitcnt vmcnt(8)
	s_waitcnt lgkmcnt(0)
	s_barrier
	s_waitcnt lgkmcnt(0)
	v_mfma_f32_16x16x32_bf16 v[28:31], v[82:85], v[98:101], v[28:31]
	v_mfma_f32_16x16x32_bf16 v[24:27], v[90:93], v[98:101], v[24:27]
	v_mfma_f32_16x16x32_bf16 v[20:23], v[82:85], v[106:109], v[20:23]
	v_mfma_f32_16x16x32_bf16 v[16:19], v[90:93], v[106:109], v[16:19]
	v_mfma_f32_16x16x32_bf16 v[12:15], v[82:85], v[114:117], v[12:15]
	v_mfma_f32_16x16x32_bf16 v[8:11], v[90:93], v[114:117], v[8:11]
	v_mfma_f32_16x16x32_bf16 v[4:7], v[82:85], v[122:125], v[4:7]
	v_mfma_f32_16x16x32_bf16 v[0:3], v[90:93], v[122:125], v[0:3]
	v_mfma_f32_16x16x32_bf16 v[28:31], v[86:89], v[102:105], v[28:31]
	v_mfma_f32_16x16x32_bf16 v[24:27], v[94:97], v[102:105], v[24:27]
	v_mfma_f32_16x16x32_bf16 v[20:23], v[86:89], v[110:113], v[20:23]
	v_mfma_f32_16x16x32_bf16 v[16:19], v[94:97], v[110:113], v[16:19]
	v_mfma_f32_16x16x32_bf16 v[12:15], v[86:89], v[118:121], v[12:15]
	v_mfma_f32_16x16x32_bf16 v[8:11], v[94:97], v[118:121], v[8:11]
	v_mfma_f32_16x16x32_bf16 v[4:7], v[86:89], v[126:129], v[4:7]
	v_mfma_f32_16x16x32_bf16 v[0:3], v[94:97], v[126:129], v[0:3]
	s_barrier
; #define PG_BAR __builtin_amdgcn_s_barrier()
; template <class Epi, class Sched, class Hook = NoHook>
; __device__ __forceinline__ void gemm_phase_w(LAS unsigned char* lds, const Sched& S, const Epi& E, int wave_id, const Hook& HK = Hook()) {
;     ...
;         if constexpr (!SEG2) {
;             for (int tt = 0; tt < nt; tt += 2) {
;                 if constexpr (GATHER) { if (tt == nt - 2) {
;                     if (has_next) { gnxt_00 = S.grow_l(nxt, lds, nbuf, R0) + (unsigned)(C0 * 2); gnxt_01 = S.grow_l(nxt, lds, nbuf, R1) + (unsigned)(C1 * 2); gnxt_10 = S.grow_l(nxt, lds, nbuf, 128 + R0) + (unsigned)(C0 * 2); gnxt_11 = S.grow_l(nxt, lds, nbuf, 128 + R1) + (unsigned)(C1 * 2); }
;                     else { gnxt_00 = gcur_00; gnxt_01 = gcur_01; gnxt_10 = gcur_10; gnxt_11 = gcur_11; } } }
;                 PG_TRIP(tt, false, false, false);
;             }
;         } else {
;             for (int tt = 0; tt < nt - 4; tt += 2) PG_TRIP(tt, false, false, false);
;             PG_TRIP(nt - 4, false, true, false);
;             PG_TRIP(nt - 2, true, false, true);
;         }
;     ...
;         if (wr == 0) PG_BAR;
	ds_read_b128 v[82:85], v81
	ds_read_b128 v[86:89], v81 offset:1024
	ds_read_b128 v[90:93], v81 offset:2048
	ds_read_b128 v[94:97], v81 offset:3072
	s_add_i32 s69, s69, 0x20000
	s_add_u32 s62, s8, s69
	s_addc_u32 s63, s9, 0
	s_mov_b32 m0, s29
	v_lshl_add_u64 v[130:131], s[62:63], 0, v[64:65]
	ds_read_b128 v[98:101], v76 offset:32768
	ds_read_b128 v[102:105], v76 offset:33792
	ds_read_b128 v[106:109], v76 offset:34816
	ds_read_b128 v[110:113], v76 offset:35840
	ds_read_b128 v[114:117], v76 offset:36864
	ds_read_b128 v[118:121], v76 offset:37888
	ds_read_b128 v[122:125], v76 offset:38912
	ds_read_b128 v[126:129], v76 offset:39936
	global_load_lds_dwordx4 v[130:131], off
	v_lshl_add_u64 v[130:131], s[62:63], 0, v[66:67]
	s_mov_b32 m0, s30
	s_nop 0
	global_load_lds_dwordx4 v[130:131], off
	s_waitcnt vmcnt(8)
	s_waitcnt lgkmcnt(0)
	s_barrier
	s_waitcnt lgkmcnt(0)
	v_mfma_f32_16x16x32_bf16 v[60:63], v[82:85], v[98:101], v[60:63]
	v_mfma_f32_16x16x32_bf16 v[56:59], v[90:93], v[98:101], v[56:59]
	v_mfma_f32_16x16x32_bf16 v[52:55], v[82:85], v[106:109], v[52:55]
	v_mfma_f32_16x16x32_bf16 v[48:51], v[90:93], v[106:109], v[48:51]
	v_mfma_f32_16x16x32_bf16 v[44:47], v[82:85], v[114:117], v[44:47]
	v_mfma_f32_16x16x32_bf16 v[40:43], v[90:93], v[114:117], v[40:43]
	v_mfma_f32_16x16x32_bf16 v[36:39], v[82:85], v[122:125], v[36:39]
	v_mfma_f32_16x16x32_bf16 v[32:35], v[90:93], v[122:125], v[32:35]
	v_mfma_f32_16x16x32_bf16 v[60:63], v[86:89], v[102:105], v[60:63]
	v_mfma_f32_16x16x32_bf16 v[56:59], v[94:97], v[102:105], v[56:59]
	v_mfma_f32_16x16x32_bf16 v[52:55], v[86:89], v[110:113], v[52:55]
	v_mfma_f32_16x16x32_bf16 v[48:51], v[94:97], v[110:113], v[48:51]
	v_mfma_f32_16x16x32_bf16 v[44:47], v[86:89], v[118:121], v[44:47]
	v_mfma_f32_16x16x32_bf16 v[40:43], v[94:97], v[118:121], v[40:43]
	v_mfma_f32_16x16x32_bf16 v[36:39], v[86:89], v[126:129], v[36:39]
	v_mfma_f32_16x16x32_bf16 v[32:35], v[94:97], v[126:129], v[32:35]
	s_barrier
	s_bitset1_b32 s61, 7
	s_add_i32 s62, s61, s68
	s_ashr_i32 s63, s62, 31
	s_add_u32 s62, s3, s62
	s_addc_u32 s63, s22, s63
	s_mov_b32 m0, s44
	v_lshl_add_u64 v[130:131], s[62:63], 0, v[64:65]
	ds_read_b128 v[98:101], v76 offset:49152
	ds_read_b128 v[102:105], v76 offset:50176
	ds_read_b128 v[106:109], v76 offset:51200
	ds_read_b128 v[110:113], v76 offset:52224
	ds_read_b128 v[114:117], v76 offset:53248
	ds_read_b128 v[118:121], v76 offset:54272
	ds_read_b128 v[122:125], v76 offset:55296
	ds_read_b128 v[126:129], v76 offset:56320
	global_load_lds_dwordx4 v[130:131], off
	v_lshl_add_u64 v[130:131], s[62:63], 0, v[66:67]
	s_add_i32 s62, s61, s67
	s_ashr_i32 s63, s62, 31
	s_add_u32 s62, s3, s62
	s_mov_b32 m0, s45
	s_addc_u32 s63, s22, s63
	global_load_lds_dwordx4 v[130:131], off
	v_lshl_add_u64 v[130:131], s[62:63], 0, v[64:65]
	s_mov_b32 m0, s36
	s_add_i32 s61, s61, s66
	global_load_lds_dwordx4 v[130:131], off
	v_lshl_add_u64 v[130:131], s[62:63], 0, v[66:67]
	s_add_u32 s62, s8, s61
	s_mov_b32 m0, s37
	s_addc_u32 s63, s9, 0
	global_load_lds_dwordx4 v[130:131], off
	v_lshl_add_u64 v[130:131], s[62:63], 0, v[64:65]
	s_mov_b32 m0, s34
	s_nop 0
	global_load_lds_dwordx4 v[130:131], off
	v_lshl_add_u64 v[130:131], s[62:63], 0, v[66:67]
	s_mov_b32 m0, s35
	s_nop 0
	global_load_lds_dwordx4 v[130:131], off
	s_waitcnt vmcnt(8)
	s_waitcnt lgkmcnt(0)
	s_barrier
	s_waitcnt lgkmcnt(0)
	v_mfma_f32_16x16x32_bf16 v[28:31], v[82:85], v[98:101], v[28:31]
	v_mfma_f32_16x16x32_bf16 v[24:27], v[90:93], v[98:101], v[24:27]
	v_mfma_f32_16x16x32_bf16 v[20:23], v[82:85], v[106:109], v[20:23]
	v_mfma_f32_16x16x32_bf16 v[16:19], v[90:93], v[106:109], v[16:19]
	v_mfma_f32_16x16x32_bf16 v[12:15], v[82:85], v[114:117], v[12:15]
	v_mfma_f32_16x16x32_bf16 v[8:11], v[90:93], v[114:117], v[8:11]
	v_mfma_f32_16x16x32_bf16 v[4:7], v[82:85], v[122:125], v[4:7]
	v_mfma_f32_16x16x32_bf16 v[0:3], v[90:93], v[122:125], v[0:3]
	v_mfma_f32_16x16x32_bf16 v[28:31], v[86:89], v[102:105], v[28:31]
	v_mfma_f32_16x16x32_bf16 v[24:27], v[94:97], v[102:105], v[24:27]
	v_mfma_f32_16x16x32_bf16 v[20:23], v[86:89], v[110:113], v[20:23]
	v_mfma_f32_16x16x32_bf16 v[16:19], v[94:97], v[110:113], v[16:19]
	v_mfma_f32_16x16x32_bf16 v[12:15], v[86:89], v[118:121], v[12:15]
	v_mfma_f32_16x16x32_bf16 v[8:11], v[94:97], v[118:121], v[8:11]
	v_mfma_f32_16x16x32_bf16 v[4:7], v[86:89], v[126:129], v[4:7]
	v_mfma_f32_16x16x32_bf16 v[0:3], v[94:97], v[126:129], v[0:3]
	s_addk_i32 s20, 0x100
	s_add_i32 s21, s21, 2
	s_cmp_gt_u32 s21, 5
	s_barrier
	s_cbranch_scc0 .LBB0_1585
	s_and_b64 vcc, exec, s[16:17]
	s_cbranch_vccz .LBB0_1590
	s_barrier
	s_andn2_b64 vcc, exec, s[6:7]
	s_mov_b64 s[20:21], -1
	s_cbranch_vccz .LBB0_1591

; template <class Epi, class Sched, class Hook = NoHook>
; __device__ __forceinline__ void gemm_phase_w(LAS unsigned char* lds, const Sched& S, const Epi& E, int wave_id, const Hook& HK = Hook()) {
;     ...
;             for (int tt = 0; tt < nt - 4; tt += 2) PG_TRIP(tt, false, false, false);
.LBB0_1776:
	s_add_i32 s27, 0, 0x10000
	s_add_i32 s59, 0, 0x14000
	v_add_u32_e32 v128, s27, v171
	v_add_u32_e32 v129, s59, v171
	ds_read_b128 v[130:133], v128
	ds_read_b128 v[162:165], v128 offset:1024
	ds_read_b128 v[178:181], v128 offset:2048
	ds_read_b128 v[182:185], v128 offset:3072
	ds_read_b128 v[186:189], v129
	ds_read_b128 v[190:193], v129 offset:1024
	ds_read_b128 v[194:197], v129 offset:2048
	ds_read_b128 v[198:201], v129 offset:3072
	s_add_i32 s26, s84, s5
	s_add_u32 s60, s3, s26
	s_addc_u32 s61, s36, 0
	s_add_i32 vcc_lo, s63, 0xc000
	s_add_i32 s35, s63, 0xe000
	s_add_i32 s42, s5, 0xfffe0080
	s_cmp_eq_u32 s70, s34
	s_cselect_b32 s50, s4, s84
	s_cselect_b32 s58, s85, s97
	s_mov_b32 m0, vcc_lo
	v_lshl_add_u64 v[134:135], s[60:61], 0, v[148:149]
	ds_read_b128 v[202:205], v172
	ds_read_b128 v[206:209], v172 offset:1024
	ds_read_b128 v[210:213], v172 offset:2048
	ds_read_b128 v[214:217], v172 offset:3072
	ds_read_b128 v[218:221], v172 offset:4096
	ds_read_b128 v[222:225], v172 offset:5120
	ds_read_b128 v[226:229], v172 offset:6144
	ds_read_b128 v[230:233], v172 offset:7168
	global_load_lds_dwordx4 v[134:135], off
	v_lshl_add_u64 v[134:135], s[60:61], 0, v[146:147]
	s_mov_b32 m0, s35
	s_nop 0
	global_load_lds_dwordx4 v[134:135], off
	s_waitcnt vmcnt(8)
	s_waitcnt lgkmcnt(0)
	s_barrier
	s_waitcnt lgkmcnt(0)
	v_mfma_f32_16x16x32_bf16 v[124:127], v[130:133], v[202:205], v[124:127]
	v_mfma_f32_16x16x32_bf16 v[120:123], v[178:181], v[202:205], v[120:123]
	v_mfma_f32_16x16x32_bf16 v[116:119], v[130:133], v[210:213], v[116:119]
	v_mfma_f32_16x16x32_bf16 v[112:115], v[178:181], v[210:213], v[112:115]
	v_mfma_f32_16x16x32_bf16 v[108:111], v[130:133], v[218:221], v[108:111]
	v_mfma_f32_16x16x32_bf16 v[104:107], v[178:181], v[218:221], v[104:107]
	v_mfma_f32_16x16x32_bf16 v[100:103], v[130:133], v[226:229], v[100:103]
	v_mfma_f32_16x16x32_bf16 v[96:99], v[178:181], v[226:229], v[96:99]
	v_mfma_f32_16x16x32_bf16 v[124:127], v[162:165], v[206:209], v[124:127]
	v_mfma_f32_16x16x32_bf16 v[120:123], v[182:185], v[206:209], v[120:123]
	v_mfma_f32_16x16x32_bf16 v[116:119], v[162:165], v[214:217], v[116:119]
	v_mfma_f32_16x16x32_bf16 v[112:115], v[182:185], v[214:217], v[112:115]
	v_mfma_f32_16x16x32_bf16 v[108:111], v[162:165], v[222:225], v[108:111]
	v_mfma_f32_16x16x32_bf16 v[104:107], v[182:185], v[222:225], v[104:107]
	v_mfma_f32_16x16x32_bf16 v[100:103], v[162:165], v[230:233], v[100:103]
	v_mfma_f32_16x16x32_bf16 v[96:99], v[182:185], v[230:233], v[96:99]
	v_mfma_f32_16x16x32_bf16 v[92:95], v[186:189], v[202:205], v[92:95]
	v_mfma_f32_16x16x32_bf16 v[88:91], v[194:197], v[202:205], v[88:91]
	v_mfma_f32_16x16x32_bf16 v[84:87], v[186:189], v[210:213], v[84:87]
	v_mfma_f32_16x16x32_bf16 v[80:83], v[194:197], v[210:213], v[80:83]
	v_mfma_f32_16x16x32_bf16 v[76:79], v[186:189], v[218:221], v[76:79]
	v_mfma_f32_16x16x32_bf16 v[72:75], v[194:197], v[218:221], v[72:75]
	v_mfma_f32_16x16x32_bf16 v[68:71], v[186:189], v[226:229], v[68:71]
	v_mfma_f32_16x16x32_bf16 v[64:67], v[194:197], v[226:229], v[64:67]
	v_mfma_f32_16x16x32_bf16 v[92:95], v[190:193], v[206:209], v[92:95]
	v_mfma_f32_16x16x32_bf16 v[88:91], v[198:201], v[206:209], v[88:91]
	v_mfma_f32_16x16x32_bf16 v[84:87], v[190:193], v[214:217], v[84:87]
	v_mfma_f32_16x16x32_bf16 v[80:83], v[198:201], v[214:217], v[80:83]
	v_mfma_f32_16x16x32_bf16 v[76:79], v[190:193], v[222:225], v[76:79]
	v_mfma_f32_16x16x32_bf16 v[72:75], v[198:201], v[222:225], v[72:75]
	v_mfma_f32_16x16x32_bf16 v[68:71], v[190:193], v[230:233], v[68:71]
	v_mfma_f32_16x16x32_bf16 v[64:67], v[198:201], v[230:233], v[64:67]
	s_barrier
	s_cselect_b32 s44, 0, s42
	s_add_i32 s42, s44, s58
	s_ashr_i32 s43, s42, 31
	s_add_u32 s60, s6, s42
	s_addc_u32 s61, s7, s43
	s_add_i32 s51, s58, 0xffffff00
	s_add_i32 s27, s27, s48
	s_add_i32 s42, s51, s44
	v_lshl_add_u64 v[134:135], s[60:61], 0, v[144:145]
	s_mov_b32 m0, s27
	s_add_i32 vcc_hi, s27, 0x2000
	s_ashr_i32 s43, s42, 31
	ds_read_b128 v[202:205], v172 offset:16384
	ds_read_b128 v[206:209], v172 offset:17408
	ds_read_b128 v[210:213], v172 offset:18432
	ds_read_b128 v[214:217], v172 offset:19456
	ds_read_b128 v[218:221], v172 offset:20480
	ds_read_b128 v[222:225], v172 offset:21504
	ds_read_b128 v[226:229], v172 offset:22528
	ds_read_b128 v[230:233], v172 offset:23552
	global_load_lds_dwordx4 v[134:135], off
	v_lshl_add_u64 v[134:135], s[60:61], 0, v[142:143]
	s_add_u32 s60, s6, s42
	s_mov_b32 m0, vcc_hi
	s_addc_u32 s61, s7, s43
	s_add_i32 s59, s59, s48
	global_load_lds_dwordx4 v[134:135], off
	v_lshl_add_u64 v[134:135], s[60:61], 0, v[144:145]
	s_mov_b32 m0, s59
	s_add_i32 s49, s44, s50
	global_load_lds_dwordx4 v[134:135], off
	v_lshl_add_u64 v[134:135], s[60:61], 0, v[142:143]
	s_add_i32 s60, s59, 0x2000
	s_add_u32 s42, s3, s49
	s_mov_b32 m0, s60
	s_addc_u32 s43, s36, 0
	global_load_lds_dwordx4 v[134:135], off
	v_lshl_add_u64 v[134:135], s[42:43], 0, v[148:149]
	s_mov_b32 m0, s63
	s_nop 0
	global_load_lds_dwordx4 v[134:135], off
	v_lshl_add_u64 v[134:135], s[42:43], 0, v[146:147]
	s_mov_b32 m0, s66
	s_nop 0
	global_load_lds_dwordx4 v[134:135], off
	s_waitcnt vmcnt(8)
	s_waitcnt lgkmcnt(0)
	s_barrier
	s_waitcnt lgkmcnt(0)
	v_mfma_f32_16x16x32_bf16 v[60:63], v[130:133], v[202:205], v[60:63]
	v_mfma_f32_16x16x32_bf16 v[56:59], v[178:181], v[202:205], v[56:59]
	v_mfma_f32_16x16x32_bf16 v[52:55], v[130:133], v[210:213], v[52:55]
	v_mfma_f32_16x16x32_bf16 v[48:51], v[178:181], v[210:213], v[48:51]
	v_mfma_f32_16x16x32_bf16 v[44:47], v[130:133], v[218:221], v[44:47]
	v_mfma_f32_16x16x32_bf16 v[40:43], v[178:181], v[218:221], v[40:43]
	v_mfma_f32_16x16x32_bf16 v[36:39], v[130:133], v[226:229], v[36:39]
	v_mfma_f32_16x16x32_bf16 v[32:35], v[178:181], v[226:229], v[32:35]
	v_mfma_f32_16x16x32_bf16 v[60:63], v[162:165], v[206:209], v[60:63]
	v_mfma_f32_16x16x32_bf16 v[56:59], v[182:185], v[206:209], v[56:59]
	v_mfma_f32_16x16x32_bf16 v[52:55], v[162:165], v[214:217], v[52:55]
	v_mfma_f32_16x16x32_bf16 v[48:51], v[182:185], v[214:217], v[48:51]
	v_mfma_f32_16x16x32_bf16 v[44:47], v[162:165], v[222:225], v[44:47]
	v_mfma_f32_16x16x32_bf16 v[40:43], v[182:185], v[222:225], v[40:43]
	v_mfma_f32_16x16x32_bf16 v[36:39], v[162:165], v[230:233], v[36:39]
	v_mfma_f32_16x16x32_bf16 v[32:35], v[182:185], v[230:233], v[32:35]
	v_mfma_f32_16x16x32_bf16 v[28:31], v[186:189], v[202:205], v[28:31]
	v_mfma_f32_16x16x32_bf16 v[24:27], v[194:197], v[202:205], v[24:27]
	v_mfma_f32_16x16x32_bf16 v[20:23], v[186:189], v[210:213], v[20:23]
	v_mfma_f32_16x16x32_bf16 v[16:19], v[194:197], v[210:213], v[16:19]
	v_mfma_f32_16x16x32_bf16 v[12:15], v[186:189], v[218:221], v[12:15]
	v_mfma_f32_16x16x32_bf16 v[8:11], v[194:197], v[218:221], v[8:11]
	v_mfma_f32_16x16x32_bf16 v[4:7], v[186:189], v[226:229], v[4:7]
	v_mfma_f32_16x16x32_bf16 v[0:3], v[194:197], v[226:229], v[0:3]
	v_mfma_f32_16x16x32_bf16 v[28:31], v[190:193], v[206:209], v[28:31]
	v_mfma_f32_16x16x32_bf16 v[24:27], v[198:201], v[206:209], v[24:27]
	v_mfma_f32_16x16x32_bf16 v[20:23], v[190:193], v[214:217], v[20:23]
	v_mfma_f32_16x16x32_bf16 v[16:19], v[198:201], v[214:217], v[16:19]
	v_mfma_f32_16x16x32_bf16 v[12:15], v[190:193], v[222:225], v[12:15]
	v_mfma_f32_16x16x32_bf16 v[8:11], v[198:201], v[222:225], v[8:11]
	v_mfma_f32_16x16x32_bf16 v[4:7], v[190:193], v[230:233], v[4:7]
	v_mfma_f32_16x16x32_bf16 v[0:3], v[198:201], v[230:233], v[0:3]
	s_barrier
	s_add_i32 s61, 0, 0x18000
	s_add_i32 s26, 0, 0x1c000
	v_add_u32_e32 v130, s61, v171
	v_add_u32_e32 v131, s26, v171
	ds_read_b128 v[132:135], v130
	ds_read_b128 v[162:165], v130 offset:1024
	ds_read_b128 v[178:181], v130 offset:2048
	ds_read_b128 v[182:185], v130 offset:3072
	ds_read_b128 v[186:189], v131
	ds_read_b128 v[190:193], v131 offset:1024
	ds_read_b128 v[194:197], v131 offset:2048
	ds_read_b128 v[198:201], v131 offset:3072
	s_add_i32 s49, s49, 0x20000
	s_add_u32 s42, s3, s49
	s_addc_u32 s43, s36, 0
	s_mov_b32 m0, s67
	v_lshl_add_u64 v[166:167], s[42:43], 0, v[148:149]
	ds_read_b128 v[202:205], v172 offset:32768
	ds_read_b128 v[206:209], v172 offset:33792
	ds_read_b128 v[210:213], v172 offset:34816
	ds_read_b128 v[214:217], v172 offset:35840
	ds_read_b128 v[218:221], v172 offset:36864
	ds_read_b128 v[222:225], v172 offset:37888
	ds_read_b128 v[226:229], v172 offset:38912
	ds_read_b128 v[230:233], v172 offset:39936
	global_load_lds_dwordx4 v[166:167], off
	v_lshl_add_u64 v[166:167], s[42:43], 0, v[146:147]
	s_mov_b32 m0, s68
	s_nop 0
	global_load_lds_dwordx4 v[166:167], off
	s_waitcnt vmcnt(8)
	s_waitcnt lgkmcnt(0)
	s_barrier
	s_waitcnt lgkmcnt(0)
	v_mfma_f32_16x16x32_bf16 v[124:127], v[132:135], v[202:205], v[124:127]
	v_mfma_f32_16x16x32_bf16 v[120:123], v[178:181], v[202:205], v[120:123]
	v_mfma_f32_16x16x32_bf16 v[116:119], v[132:135], v[210:213], v[116:119]
	v_mfma_f32_16x16x32_bf16 v[112:115], v[178:181], v[210:213], v[112:115]
	v_mfma_f32_16x16x32_bf16 v[108:111], v[132:135], v[218:221], v[108:111]
	v_mfma_f32_16x16x32_bf16 v[104:107], v[178:181], v[218:221], v[104:107]
	v_mfma_f32_16x16x32_bf16 v[100:103], v[132:135], v[226:229], v[100:103]
	v_mfma_f32_16x16x32_bf16 v[96:99], v[178:181], v[226:229], v[96:99]
	v_mfma_f32_16x16x32_bf16 v[124:127], v[162:165], v[206:209], v[124:127]
	v_mfma_f32_16x16x32_bf16 v[120:123], v[182:185], v[206:209], v[120:123]
	v_mfma_f32_16x16x32_bf16 v[116:119], v[162:165], v[214:217], v[116:119]
	v_mfma_f32_16x16x32_bf16 v[112:115], v[182:185], v[214:217], v[112:115]
	v_mfma_f32_16x16x32_bf16 v[108:111], v[162:165], v[222:225], v[108:111]
	v_mfma_f32_16x16x32_bf16 v[104:107], v[182:185], v[222:225], v[104:107]
	v_mfma_f32_16x16x32_bf16 v[100:103], v[162:165], v[230:233], v[100:103]
	v_mfma_f32_16x16x32_bf16 v[96:99], v[182:185], v[230:233], v[96:99]
	v_mfma_f32_16x16x32_bf16 v[92:95], v[186:189], v[202:205], v[92:95]
	v_mfma_f32_16x16x32_bf16 v[88:91], v[194:197], v[202:205], v[88:91]
	v_mfma_f32_16x16x32_bf16 v[84:87], v[186:189], v[210:213], v[84:87]
	v_mfma_f32_16x16x32_bf16 v[80:83], v[194:197], v[210:213], v[80:83]
	v_mfma_f32_16x16x32_bf16 v[76:79], v[186:189], v[218:221], v[76:79]
	v_mfma_f32_16x16x32_bf16 v[72:75], v[194:197], v[218:221], v[72:75]
	v_mfma_f32_16x16x32_bf16 v[68:71], v[186:189], v[226:229], v[68:71]
	v_mfma_f32_16x16x32_bf16 v[64:67], v[194:197], v[226:229], v[64:67]
	v_mfma_f32_16x16x32_bf16 v[92:95], v[190:193], v[206:209], v[92:95]
	v_mfma_f32_16x16x32_bf16 v[88:91], v[198:201], v[206:209], v[88:91]
	v_mfma_f32_16x16x32_bf16 v[84:87], v[190:193], v[214:217], v[84:87]
	v_mfma_f32_16x16x32_bf16 v[80:83], v[198:201], v[214:217], v[80:83]
	v_mfma_f32_16x16x32_bf16 v[76:79], v[190:193], v[222:225], v[76:79]
	v_mfma_f32_16x16x32_bf16 v[72:75], v[198:201], v[222:225], v[72:75]
	v_mfma_f32_16x16x32_bf16 v[68:71], v[190:193], v[230:233], v[68:71]
	v_mfma_f32_16x16x32_bf16 v[64:67], v[198:201], v[230:233], v[64:67]
	s_barrier
; template <class Epi, class Sched, class Hook = NoHook>
; __device__ __forceinline__ void gemm_phase_w(LAS unsigned char* lds, const Sched& S, const Epi& E, int wave_id, const Hook& HK = Hook()) {
;     ...
;         if constexpr (!SEG2) {
;             for (int tt = 0; tt < nt; tt += 2) {
;                 if constexpr (GATHER) { if (tt == nt - 2) {
;                     if (has_next) { gnxt_00 = S.grow_l(nxt, lds, nbuf, R0) + (unsigned)(C0 * 2); gnxt_01 = S.grow_l(nxt, lds, nbuf, R1) + (unsigned)(C1 * 2); gnxt_10 = S.grow_l(nxt, lds, nbuf, 128 + R0) + (unsigned)(C0 * 2); gnxt_11 = S.grow_l(nxt, lds, nbuf, 128 + R1) + (unsigned)(C1 * 2); }
;                     else { gnxt_00 = gcur_00; gnxt_01 = gcur_01; gnxt_10 = gcur_10; gnxt_11 = gcur_11; } } }
;                 PG_TRIP(tt, false, false, false);
;             }
;         } else {
;             for (int tt = 0; tt < nt - 4; tt += 2) PG_TRIP(tt, false, false, false);
;             PG_TRIP(nt - 4, false, true, false);
	s_or_b32 s18, s44, 0x80
	s_add_i32 s19, s18, s58
	s_ashr_i32 s43, s19, 31
	s_add_u32 s42, s6, s19
	s_addc_u32 s43, s7, s43
	s_add_i32 s61, s61, s48
	v_lshl_add_u64 v[166:167], s[42:43], 0, v[144:145]
	s_mov_b32 m0, s61
	s_add_i32 s19, s18, s51
	ds_read_b128 v[202:205], v172 offset:49152
	ds_read_b128 v[206:209], v172 offset:50176
	ds_read_b128 v[210:213], v172 offset:51200
	ds_read_b128 v[214:217], v172 offset:52224
	ds_read_b128 v[218:221], v172 offset:53248
	ds_read_b128 v[222:225], v172 offset:54272
	ds_read_b128 v[226:229], v172 offset:55296
	ds_read_b128 v[230:233], v172 offset:56320
	global_load_lds_dwordx4 v[166:167], off
	v_lshl_add_u64 v[166:167], s[42:43], 0, v[142:143]
	s_add_i32 s49, s61, 0x2000
	s_ashr_i32 s43, s19, 31
	s_add_u32 s42, s6, s19
	s_mov_b32 m0, s49
	s_addc_u32 s43, s7, s43
	s_add_i32 s26, s26, s48
	global_load_lds_dwordx4 v[166:167], off
	v_lshl_add_u64 v[166:167], s[42:43], 0, v[144:145]
	s_mov_b32 m0, s26
	s_add_i32 s44, s26, 0x2000
	s_add_i32 s18, s18, s50
	global_load_lds_dwordx4 v[166:167], off
	v_lshl_add_u64 v[166:167], s[42:43], 0, v[142:143]
	s_add_u32 s42, s3, s18
	s_mov_b32 m0, s44
	s_addc_u32 s43, s36, 0
	global_load_lds_dwordx4 v[166:167], off
	v_lshl_add_u64 v[166:167], s[42:43], 0, v[148:149]
	s_mov_b32 m0, s71
	s_nop 0
	global_load_lds_dwordx4 v[166:167], off
	v_lshl_add_u64 v[166:167], s[42:43], 0, v[146:147]
	s_mov_b32 m0, s72
	s_nop 0
	global_load_lds_dwordx4 v[166:167], off
	s_waitcnt vmcnt(8)
	s_waitcnt lgkmcnt(0)
	s_barrier
	s_waitcnt lgkmcnt(0)
	v_mfma_f32_16x16x32_bf16 v[60:63], v[132:135], v[202:205], v[60:63]
	v_mfma_f32_16x16x32_bf16 v[56:59], v[178:181], v[202:205], v[56:59]
	v_mfma_f32_16x16x32_bf16 v[52:55], v[132:135], v[210:213], v[52:55]
	v_mfma_f32_16x16x32_bf16 v[48:51], v[178:181], v[210:213], v[48:51]
	v_mfma_f32_16x16x32_bf16 v[44:47], v[132:135], v[218:221], v[44:47]
	v_mfma_f32_16x16x32_bf16 v[40:43], v[178:181], v[218:221], v[40:43]
	v_mfma_f32_16x16x32_bf16 v[36:39], v[132:135], v[226:229], v[36:39]
	v_mfma_f32_16x16x32_bf16 v[32:35], v[178:181], v[226:229], v[32:35]
	v_mfma_f32_16x16x32_bf16 v[60:63], v[162:165], v[206:209], v[60:63]
	v_mfma_f32_16x16x32_bf16 v[56:59], v[182:185], v[206:209], v[56:59]
	v_mfma_f32_16x16x32_bf16 v[52:55], v[162:165], v[214:217], v[52:55]
	v_mfma_f32_16x16x32_bf16 v[48:51], v[182:185], v[214:217], v[48:51]
	v_mfma_f32_16x16x32_bf16 v[44:47], v[162:165], v[222:225], v[44:47]
	v_mfma_f32_16x16x32_bf16 v[40:43], v[182:185], v[222:225], v[40:43]
	v_mfma_f32_16x16x32_bf16 v[36:39], v[162:165], v[230:233], v[36:39]
	v_mfma_f32_16x16x32_bf16 v[32:35], v[182:185], v[230:233], v[32:35]
	v_mfma_f32_16x16x32_bf16 v[28:31], v[186:189], v[202:205], v[28:31]
	v_mfma_f32_16x16x32_bf16 v[24:27], v[194:197], v[202:205], v[24:27]
	v_mfma_f32_16x16x32_bf16 v[20:23], v[186:189], v[210:213], v[20:23]
	v_mfma_f32_16x16x32_bf16 v[16:19], v[194:197], v[210:213], v[16:19]
	v_mfma_f32_16x16x32_bf16 v[12:15], v[186:189], v[218:221], v[12:15]
	v_mfma_f32_16x16x32_bf16 v[8:11], v[194:197], v[218:221], v[8:11]
	v_mfma_f32_16x16x32_bf16 v[4:7], v[186:189], v[226:229], v[4:7]
	v_mfma_f32_16x16x32_bf16 v[0:3], v[194:197], v[226:229], v[0:3]
	v_mfma_f32_16x16x32_bf16 v[28:31], v[190:193], v[206:209], v[28:31]
	v_mfma_f32_16x16x32_bf16 v[24:27], v[198:201], v[206:209], v[24:27]
	v_mfma_f32_16x16x32_bf16 v[20:23], v[190:193], v[214:217], v[20:23]
	v_mfma_f32_16x16x32_bf16 v[16:19], v[198:201], v[214:217], v[16:19]
	v_mfma_f32_16x16x32_bf16 v[12:15], v[190:193], v[222:225], v[12:15]
	v_mfma_f32_16x16x32_bf16 v[8:11], v[198:201], v[222:225], v[8:11]
	v_mfma_f32_16x16x32_bf16 v[4:7], v[190:193], v[230:233], v[4:7]
	v_mfma_f32_16x16x32_bf16 v[0:3], v[198:201], v[230:233], v[0:3]
	s_addk_i32 s5, 0x100
	s_add_i32 s18, s34, 2
	s_add_i32 s19, s34, 4
	s_cmp_ge_u32 s19, s70
	s_mov_b32 s34, s18
	s_barrier
	s_cbranch_scc0 .LBB0_1776
	ds_read_b128 v[132:135], v128
	ds_read_b128 v[162:165], v128 offset:1024
	ds_read_b128 v[178:181], v128 offset:2048
	ds_read_b128 v[182:185], v128 offset:3072
	ds_read_b128 v[186:189], v129
	ds_read_b128 v[190:193], v129 offset:1024
	ds_read_b128 v[194:197], v129 offset:2048
	ds_read_b128 v[198:201], v129 offset:3072
	s_add_i32 s5, s73, s84
	s_add_u32 s50, s3, s5
	s_addc_u32 s51, s36, 0
	s_mov_b32 m0, vcc_lo
	v_lshl_add_u64 v[166:167], s[50:51], 0, v[148:149]
	ds_read_b128 v[202:205], v172
	ds_read_b128 v[206:209], v172 offset:1024
	ds_read_b128 v[210:213], v172 offset:2048
	ds_read_b128 v[214:217], v172 offset:3072
	ds_read_b128 v[218:221], v172 offset:4096
	ds_read_b128 v[222:225], v172 offset:5120
	ds_read_b128 v[226:229], v172 offset:6144
	ds_read_b128 v[230:233], v172 offset:7168
	global_load_lds_dwordx4 v[166:167], off
	v_lshl_add_u64 v[166:167], s[50:51], 0, v[146:147]
	s_mov_b32 m0, s35
	s_nop 0
	global_load_lds_dwordx4 v[166:167], off
	s_waitcnt vmcnt(8)
	s_waitcnt lgkmcnt(0)
	s_barrier
	s_waitcnt lgkmcnt(0)
	v_mfma_f32_16x16x32_bf16 v[124:127], v[132:135], v[202:205], v[124:127]
	v_mfma_f32_16x16x32_bf16 v[120:123], v[178:181], v[202:205], v[120:123]
	v_mfma_f32_16x16x32_bf16 v[116:119], v[132:135], v[210:213], v[116:119]
	v_mfma_f32_16x16x32_bf16 v[112:115], v[178:181], v[210:213], v[112:115]
	v_mfma_f32_16x16x32_bf16 v[108:111], v[132:135], v[218:221], v[108:111]
	v_mfma_f32_16x16x32_bf16 v[104:107], v[178:181], v[218:221], v[104:107]
	v_mfma_f32_16x16x32_bf16 v[100:103], v[132:135], v[226:229], v[100:103]
	v_mfma_f32_16x16x32_bf16 v[96:99], v[178:181], v[226:229], v[96:99]
	v_mfma_f32_16x16x32_bf16 v[124:127], v[162:165], v[206:209], v[124:127]
	v_mfma_f32_16x16x32_bf16 v[120:123], v[182:185], v[206:209], v[120:123]
	v_mfma_f32_16x16x32_bf16 v[116:119], v[162:165], v[214:217], v[116:119]
	v_mfma_f32_16x16x32_bf16 v[112:115], v[182:185], v[214:217], v[112:115]
	v_mfma_f32_16x16x32_bf16 v[108:111], v[162:165], v[222:225], v[108:111]
	v_mfma_f32_16x16x32_bf16 v[104:107], v[182:185], v[222:225], v[104:107]
	v_mfma_f32_16x16x32_bf16 v[100:103], v[162:165], v[230:233], v[100:103]
	v_mfma_f32_16x16x32_bf16 v[96:99], v[182:185], v[230:233], v[96:99]
	v_mfma_f32_16x16x32_bf16 v[92:95], v[186:189], v[202:205], v[92:95]
	v_mfma_f32_16x16x32_bf16 v[88:91], v[194:197], v[202:205], v[88:91]
	v_mfma_f32_16x16x32_bf16 v[84:87], v[186:189], v[210:213], v[84:87]
	v_mfma_f32_16x16x32_bf16 v[80:83], v[194:197], v[210:213], v[80:83]
	v_mfma_f32_16x16x32_bf16 v[76:79], v[186:189], v[218:221], v[76:79]
	v_mfma_f32_16x16x32_bf16 v[72:75], v[194:197], v[218:221], v[72:75]
	v_mfma_f32_16x16x32_bf16 v[68:71], v[186:189], v[226:229], v[68:71]
	v_mfma_f32_16x16x32_bf16 v[64:67], v[194:197], v[226:229], v[64:67]
	v_mfma_f32_16x16x32_bf16 v[92:95], v[190:193], v[206:209], v[92:95]
	v_mfma_f32_16x16x32_bf16 v[88:91], v[198:201], v[206:209], v[88:91]
	v_mfma_f32_16x16x32_bf16 v[84:87], v[190:193], v[214:217], v[84:87]
	v_mfma_f32_16x16x32_bf16 v[80:83], v[198:201], v[214:217], v[80:83]
	v_mfma_f32_16x16x32_bf16 v[76:79], v[190:193], v[222:225], v[76:79]
	v_mfma_f32_16x16x32_bf16 v[72:75], v[198:201], v[222:225], v[72:75]
	v_mfma_f32_16x16x32_bf16 v[68:71], v[190:193], v[230:233], v[68:71]
	v_mfma_f32_16x16x32_bf16 v[64:67], v[198:201], v[230:233], v[64:67]
	s_barrier
	s_ashr_i32 s5, s31, 31
	s_add_u32 s50, s8, s31
	s_addc_u32 s51, s9, s5
	s_add_i32 s5, s31, 0x8000
	s_mov_b32 m0, s27
	v_lshl_add_u64 v[166:167], s[50:51], 0, v[138:139]
	s_ashr_i32 s34, s5, 31
	ds_read_b128 v[202:205], v172 offset:16384
	ds_read_b128 v[206:209], v172 offset:17408
	ds_read_b128 v[210:213], v172 offset:18432
	ds_read_b128 v[214:217], v172 offset:19456
	ds_read_b128 v[218:221], v172 offset:20480
	ds_read_b128 v[222:225], v172 offset:21504
	ds_read_b128 v[226:229], v172 offset:22528
	ds_read_b128 v[230:233], v172 offset:23552
	global_load_lds_dwordx4 v[166:167], off
	v_lshl_add_u64 v[166:167], s[50:51], 0, v[140:141]
	s_add_u32 s50, s8, s5
	s_mov_b32 m0, vcc_hi
	s_addc_u32 s51, s9, s34
	global_load_lds_dwordx4 v[166:167], off
	v_lshl_add_u64 v[166:167], s[50:51], 0, v[138:139]
	s_mov_b32 m0, s59
	s_nop 0
	global_load_lds_dwordx4 v[166:167], off
	v_lshl_add_u64 v[166:167], s[50:51], 0, v[140:141]
	s_add_u32 s50, s37, s89
	s_mov_b32 m0, s60
	s_addc_u32 s51, s38, 0
	global_load_lds_dwordx4 v[166:167], off
	v_lshl_add_u64 v[166:167], s[50:51], 0, v[138:139]
	s_mov_b32 m0, s63
	s_nop 0
	global_load_lds_dwordx4 v[166:167], off
	v_lshl_add_u64 v[166:167], s[50:51], 0, v[140:141]
	s_mov_b32 m0, s66
	s_nop 0
	global_load_lds_dwordx4 v[166:167], off
	s_waitcnt vmcnt(8)
	s_waitcnt lgkmcnt(0)
	s_barrier
	s_waitcnt lgkmcnt(0)
	v_mfma_f32_16x16x32_bf16 v[60:63], v[132:135], v[202:205], v[60:63]
	v_mfma_f32_16x16x32_bf16 v[56:59], v[178:181], v[202:205], v[56:59]
	v_mfma_f32_16x16x32_bf16 v[52:55], v[132:135], v[210:213], v[52:55]
	v_mfma_f32_16x16x32_bf16 v[48:51], v[178:181], v[210:213], v[48:51]
	v_mfma_f32_16x16x32_bf16 v[44:47], v[132:135], v[218:221], v[44:47]
	v_mfma_f32_16x16x32_bf16 v[40:43], v[178:181], v[218:221], v[40:43]
	v_mfma_f32_16x16x32_bf16 v[36:39], v[132:135], v[226:229], v[36:39]
	v_mfma_f32_16x16x32_bf16 v[32:35], v[178:181], v[226:229], v[32:35]
	v_mfma_f32_16x16x32_bf16 v[60:63], v[162:165], v[206:209], v[60:63]
	v_mfma_f32_16x16x32_bf16 v[56:59], v[182:185], v[206:209], v[56:59]
	v_mfma_f32_16x16x32_bf16 v[52:55], v[162:165], v[214:217], v[52:55]
	v_mfma_f32_16x16x32_bf16 v[48:51], v[182:185], v[214:217], v[48:51]
	v_mfma_f32_16x16x32_bf16 v[44:47], v[162:165], v[222:225], v[44:47]
	v_mfma_f32_16x16x32_bf16 v[40:43], v[182:185], v[222:225], v[40:43]
	v_mfma_f32_16x16x32_bf16 v[36:39], v[162:165], v[230:233], v[36:39]
	v_mfma_f32_16x16x32_bf16 v[32:35], v[182:185], v[230:233], v[32:35]
	v_mfma_f32_16x16x32_bf16 v[28:31], v[186:189], v[202:205], v[28:31]
	v_mfma_f32_16x16x32_bf16 v[24:27], v[194:197], v[202:205], v[24:27]
	v_mfma_f32_16x16x32_bf16 v[20:23], v[186:189], v[210:213], v[20:23]
	v_mfma_f32_16x16x32_bf16 v[16:19], v[194:197], v[210:213], v[16:19]
	v_mfma_f32_16x16x32_bf16 v[4:7], v[186:189], v[226:229], v[4:7]
	v_mfma_f32_16x16x32_bf16 v[0:3], v[194:197], v[226:229], v[0:3]
	v_mfma_f32_16x16x32_bf16 v[28:31], v[190:193], v[206:209], v[28:31]
	v_mfma_f32_16x16x32_bf16 v[24:27], v[198:201], v[206:209], v[24:27]
	v_mfma_f32_16x16x32_bf16 v[20:23], v[190:193], v[214:217], v[20:23]
	v_mfma_f32_16x16x32_bf16 v[16:19], v[198:201], v[214:217], v[16:19]
	v_mfma_f32_16x16x32_bf16 v[12:15], v[186:189], v[218:221], v[12:15]
	v_mfma_f32_16x16x32_bf16 v[8:11], v[194:197], v[218:221], v[8:11]
	v_mfma_f32_16x16x32_bf16 v[4:7], v[190:193], v[230:233], v[4:7]
	v_mfma_f32_16x16x32_bf16 v[0:3], v[198:201], v[230:233], v[0:3]
	v_mfma_f32_16x16x32_bf16 v[12:15], v[190:193], v[222:225], v[12:15]
	v_mfma_f32_16x16x32_bf16 v[8:11], v[198:201], v[222:225], v[8:11]
	s_barrier
	ds_read_b128 v[132:135], v130
	ds_read_b128 v[162:165], v130 offset:1024
	ds_read_b128 v[178:181], v130 offset:2048
	ds_read_b128 v[182:185], v130 offset:3072
	ds_read_b128 v[186:189], v131
	ds_read_b128 v[190:193], v131 offset:1024
	ds_read_b128 v[194:197], v131 offset:2048
	ds_read_b128 v[198:201], v131 offset:3072
	s_add_i32 s5, s89, 0x8000
	s_add_u32 s50, s37, s5
	s_addc_u32 s51, s38, 0
	s_mov_b32 m0, s67
	v_lshl_add_u64 v[166:167], s[50:51], 0, v[138:139]
	ds_read_b128 v[202:205], v172 offset:32768
	ds_read_b128 v[206:209], v172 offset:33792
	ds_read_b128 v[210:213], v172 offset:34816
	ds_read_b128 v[214:217], v172 offset:35840
	ds_read_b128 v[218:221], v172 offset:36864
	ds_read_b128 v[222:225], v172 offset:37888
	ds_read_b128 v[226:229], v172 offset:38912
	ds_read_b128 v[230:233], v172 offset:39936
	global_load_lds_dwordx4 v[166:167], off
	v_lshl_add_u64 v[166:167], s[50:51], 0, v[140:141]
	s_mov_b32 m0, s68
	s_nop 0
	global_load_lds_dwordx4 v[166:167], off
	s_waitcnt vmcnt(8)
	s_waitcnt lgkmcnt(0)
	s_barrier
	s_waitcnt lgkmcnt(0)
	v_mfma_f32_16x16x32_bf16 v[124:127], v[132:135], v[202:205], v[124:127]
	v_mfma_f32_16x16x32_bf16 v[120:123], v[178:181], v[202:205], v[120:123]
	v_mfma_f32_16x16x32_bf16 v[116:119], v[132:135], v[210:213], v[116:119]
	v_mfma_f32_16x16x32_bf16 v[112:115], v[178:181], v[210:213], v[112:115]
	v_mfma_f32_16x16x32_bf16 v[108:111], v[132:135], v[218:221], v[108:111]
	v_mfma_f32_16x16x32_bf16 v[104:107], v[178:181], v[218:221], v[104:107]
	v_mfma_f32_16x16x32_bf16 v[100:103], v[132:135], v[226:229], v[100:103]
	v_mfma_f32_16x16x32_bf16 v[96:99], v[178:181], v[226:229], v[96:99]
	v_mfma_f32_16x16x32_bf16 v[124:127], v[162:165], v[206:209], v[124:127]
	v_mfma_f32_16x16x32_bf16 v[120:123], v[182:185], v[206:209], v[120:123]
	v_mfma_f32_16x16x32_bf16 v[116:119], v[162:165], v[214:217], v[116:119]
	v_mfma_f32_16x16x32_bf16 v[112:115], v[182:185], v[214:217], v[112:115]
	v_mfma_f32_16x16x32_bf16 v[108:111], v[162:165], v[222:225], v[108:111]
	v_mfma_f32_16x16x32_bf16 v[104:107], v[182:185], v[222:225], v[104:107]
	v_mfma_f32_16x16x32_bf16 v[100:103], v[162:165], v[230:233], v[100:103]
	v_mfma_f32_16x16x32_bf16 v[96:99], v[182:185], v[230:233], v[96:99]
	v_mfma_f32_16x16x32_bf16 v[92:95], v[186:189], v[202:205], v[92:95]
	v_mfma_f32_16x16x32_bf16 v[88:91], v[194:197], v[202:205], v[88:91]
	v_mfma_f32_16x16x32_bf16 v[84:87], v[186:189], v[210:213], v[84:87]
	v_mfma_f32_16x16x32_bf16 v[80:83], v[194:197], v[210:213], v[80:83]
	v_mfma_f32_16x16x32_bf16 v[76:79], v[186:189], v[218:221], v[76:79]
	v_mfma_f32_16x16x32_bf16 v[72:75], v[194:197], v[218:221], v[72:75]
	v_mfma_f32_16x16x32_bf16 v[68:71], v[186:189], v[226:229], v[68:71]
	v_mfma_f32_16x16x32_bf16 v[64:67], v[194:197], v[226:229], v[64:67]
	v_mfma_f32_16x16x32_bf16 v[92:95], v[190:193], v[206:209], v[92:95]
	v_mfma_f32_16x16x32_bf16 v[88:91], v[198:201], v[206:209], v[88:91]
	v_mfma_f32_16x16x32_bf16 v[84:87], v[190:193], v[214:217], v[84:87]
	v_mfma_f32_16x16x32_bf16 v[80:83], v[198:201], v[214:217], v[80:83]
	v_mfma_f32_16x16x32_bf16 v[76:79], v[190:193], v[222:225], v[76:79]
	v_mfma_f32_16x16x32_bf16 v[72:75], v[198:201], v[222:225], v[72:75]
	v_mfma_f32_16x16x32_bf16 v[68:71], v[190:193], v[230:233], v[68:71]
	v_mfma_f32_16x16x32_bf16 v[64:67], v[198:201], v[230:233], v[64:67]
	s_barrier
	s_add_i32 s50, s31, 0x80
	s_ashr_i32 s51, s50, 31
	s_add_i32 s5, s31, 0x8080
	s_mov_b32 m0, s61
	v_lshl_add_u64 v[166:167], v[154:155], 0, s[50:51]
	s_ashr_i32 s31, s5, 31
	ds_read_b128 v[202:205], v172 offset:49152
	ds_read_b128 v[206:209], v172 offset:50176
	ds_read_b128 v[210:213], v172 offset:51200
	ds_read_b128 v[214:217], v172 offset:52224
	ds_read_b128 v[218:221], v172 offset:53248
	ds_read_b128 v[222:225], v172 offset:54272
	ds_read_b128 v[226:229], v172 offset:55296
	ds_read_b128 v[230:233], v172 offset:56320
	global_load_lds_dwordx4 v[166:167], off
	v_lshl_add_u64 v[166:167], v[156:157], 0, s[50:51]
	s_add_u32 s50, s8, s5
	s_mov_b32 m0, s49
	s_addc_u32 s51, s9, s31
	global_load_lds_dwordx4 v[166:167], off
	v_lshl_add_u64 v[166:167], s[50:51], 0, v[138:139]
	s_mov_b32 m0, s26
	s_add_i32 s5, s89, 0x80
	global_load_lds_dwordx4 v[166:167], off
	v_lshl_add_u64 v[166:167], s[50:51], 0, v[140:141]
	s_add_u32 s50, s37, s5
	s_mov_b32 m0, s44
	s_addc_u32 s51, s38, 0
	global_load_lds_dwordx4 v[166:167], off
	v_lshl_add_u64 v[166:167], s[50:51], 0, v[138:139]
	s_mov_b32 m0, s71
	s_nop 0
	global_load_lds_dwordx4 v[166:167], off
	v_lshl_add_u64 v[166:167], s[50:51], 0, v[140:141]
	s_mov_b32 m0, s72
	s_nop 0
	global_load_lds_dwordx4 v[166:167], off
	s_waitcnt vmcnt(8)
	s_waitcnt lgkmcnt(0)
	s_barrier
; template <class Epi, class Sched, class Hook = NoHook>
; __device__ __forceinline__ void gemm_phase_w(LAS unsigned char* lds, const Sched& S, const Epi& E, int wave_id, const Hook& HK = Hook()) {
;     ...
;         if constexpr (!SEG2) {
;             for (int tt = 0; tt < nt; tt += 2) {
;                 if constexpr (GATHER) { if (tt == nt - 2) {
;                     if (has_next) { gnxt_00 = S.grow_l(nxt, lds, nbuf, R0) + (unsigned)(C0 * 2); gnxt_01 = S.grow_l(nxt, lds, nbuf, R1) + (unsigned)(C1 * 2); gnxt_10 = S.grow_l(nxt, lds, nbuf, 128 + R0) + (unsigned)(C0 * 2); gnxt_11 = S.grow_l(nxt, lds, nbuf, 128 + R1) + (unsigned)(C1 * 2); }
;                     else { gnxt_00 = gcur_00; gnxt_01 = gcur_01; gnxt_10 = gcur_10; gnxt_11 = gcur_11; } } }
;                 PG_TRIP(tt, false, false, false);
;             }
;         } else {
;             for (int tt = 0; tt < nt - 4; tt += 2) PG_TRIP(tt, false, false, false);
;             PG_TRIP(nt - 4, false, true, false);
;             PG_TRIP(nt - 2, true, false, true);
	s_waitcnt lgkmcnt(0)
	v_mfma_f32_16x16x32_bf16 v[60:63], v[132:135], v[202:205], v[60:63]
	v_mfma_f32_16x16x32_bf16 v[56:59], v[178:181], v[202:205], v[56:59]
	v_mfma_f32_16x16x32_bf16 v[52:55], v[132:135], v[210:213], v[52:55]
	v_mfma_f32_16x16x32_bf16 v[48:51], v[178:181], v[210:213], v[48:51]
	v_mfma_f32_16x16x32_bf16 v[44:47], v[132:135], v[218:221], v[44:47]
	v_mfma_f32_16x16x32_bf16 v[40:43], v[178:181], v[218:221], v[40:43]
	v_mfma_f32_16x16x32_bf16 v[36:39], v[132:135], v[226:229], v[36:39]
	v_mfma_f32_16x16x32_bf16 v[32:35], v[178:181], v[226:229], v[32:35]
	v_mfma_f32_16x16x32_bf16 v[60:63], v[162:165], v[206:209], v[60:63]
	v_mfma_f32_16x16x32_bf16 v[56:59], v[182:185], v[206:209], v[56:59]
	v_mfma_f32_16x16x32_bf16 v[52:55], v[162:165], v[214:217], v[52:55]
	v_mfma_f32_16x16x32_bf16 v[48:51], v[182:185], v[214:217], v[48:51]
	v_mfma_f32_16x16x32_bf16 v[44:47], v[162:165], v[222:225], v[44:47]
	v_mfma_f32_16x16x32_bf16 v[40:43], v[182:185], v[222:225], v[40:43]
	v_mfma_f32_16x16x32_bf16 v[36:39], v[162:165], v[230:233], v[36:39]
	v_mfma_f32_16x16x32_bf16 v[32:35], v[182:185], v[230:233], v[32:35]
	v_mfma_f32_16x16x32_bf16 v[28:31], v[186:189], v[202:205], v[28:31]
	v_mfma_f32_16x16x32_bf16 v[24:27], v[194:197], v[202:205], v[24:27]
	v_mfma_f32_16x16x32_bf16 v[20:23], v[186:189], v[210:213], v[20:23]
	v_mfma_f32_16x16x32_bf16 v[16:19], v[194:197], v[210:213], v[16:19]
	v_mfma_f32_16x16x32_bf16 v[4:7], v[186:189], v[226:229], v[4:7]
	v_mfma_f32_16x16x32_bf16 v[0:3], v[194:197], v[226:229], v[0:3]
	v_mfma_f32_16x16x32_bf16 v[28:31], v[190:193], v[206:209], v[28:31]
	v_mfma_f32_16x16x32_bf16 v[24:27], v[198:201], v[206:209], v[24:27]
	v_mfma_f32_16x16x32_bf16 v[20:23], v[190:193], v[214:217], v[20:23]
	v_mfma_f32_16x16x32_bf16 v[16:19], v[198:201], v[214:217], v[16:19]
	v_mfma_f32_16x16x32_bf16 v[12:15], v[186:189], v[218:221], v[12:15]
	v_mfma_f32_16x16x32_bf16 v[8:11], v[194:197], v[218:221], v[8:11]
	v_mfma_f32_16x16x32_bf16 v[4:7], v[190:193], v[230:233], v[4:7]
	v_mfma_f32_16x16x32_bf16 v[0:3], v[198:201], v[230:233], v[0:3]
	v_mfma_f32_16x16x32_bf16 v[12:15], v[190:193], v[222:225], v[12:15]
	v_mfma_f32_16x16x32_bf16 v[8:11], v[198:201], v[222:225], v[8:11]
	s_barrier
	ds_read_b128 v[132:135], v128
	ds_read_b128 v[162:165], v128 offset:1024
	ds_read_b128 v[178:181], v128 offset:2048
	ds_read_b128 v[182:185], v128 offset:3072
	ds_read_b128 v[186:189], v129
	ds_read_b128 v[190:193], v129 offset:1024
	ds_read_b128 v[194:197], v129 offset:2048
	ds_read_b128 v[198:201], v129 offset:3072
	s_add_i32 s5, s89, 0x8080
	s_add_u32 s50, s37, s5
	s_addc_u32 s51, s38, 0
	s_mov_b32 m0, vcc_lo
	v_lshl_add_u64 v[128:129], s[50:51], 0, v[138:139]
	ds_read_b128 v[202:205], v172
	ds_read_b128 v[206:209], v172 offset:1024
	ds_read_b128 v[210:213], v172 offset:2048
	ds_read_b128 v[214:217], v172 offset:3072
	ds_read_b128 v[218:221], v172 offset:4096
	ds_read_b128 v[222:225], v172 offset:5120
	ds_read_b128 v[226:229], v172 offset:6144
	ds_read_b128 v[230:233], v172 offset:7168
	global_load_lds_dwordx4 v[128:129], off
	v_lshl_add_u64 v[128:129], s[50:51], 0, v[140:141]
	s_mov_b32 m0, s35
	s_nop 0
	global_load_lds_dwordx4 v[128:129], off
	s_waitcnt vmcnt(8)
	s_waitcnt lgkmcnt(0)
	s_barrier
	s_waitcnt lgkmcnt(0)
	v_mfma_f32_16x16x32_bf16 v[124:127], v[132:135], v[202:205], v[124:127]
	v_mfma_f32_16x16x32_bf16 v[120:123], v[178:181], v[202:205], v[120:123]
	v_mfma_f32_16x16x32_bf16 v[116:119], v[132:135], v[210:213], v[116:119]
	v_mfma_f32_16x16x32_bf16 v[112:115], v[178:181], v[210:213], v[112:115]
	v_mfma_f32_16x16x32_bf16 v[108:111], v[132:135], v[218:221], v[108:111]
	v_mfma_f32_16x16x32_bf16 v[104:107], v[178:181], v[218:221], v[104:107]
	v_mfma_f32_16x16x32_bf16 v[124:127], v[162:165], v[206:209], v[124:127]
	v_mfma_f32_16x16x32_bf16 v[120:123], v[182:185], v[206:209], v[120:123]
	v_mfma_f32_16x16x32_bf16 v[116:119], v[162:165], v[214:217], v[116:119]
	v_mfma_f32_16x16x32_bf16 v[112:115], v[182:185], v[214:217], v[112:115]
	v_mfma_f32_16x16x32_bf16 v[108:111], v[162:165], v[222:225], v[108:111]
	v_mfma_f32_16x16x32_bf16 v[104:107], v[182:185], v[222:225], v[104:107]
	v_mfma_f32_16x16x32_bf16 v[100:103], v[132:135], v[226:229], v[100:103]
	v_mfma_f32_16x16x32_bf16 v[96:99], v[178:181], v[226:229], v[96:99]
	v_mfma_f32_16x16x32_bf16 v[234:237], v[162:165], v[230:233], v[100:103]
	v_mfma_f32_16x16x32_bf16 v[238:241], v[182:185], v[230:233], v[96:99]
	v_mfma_f32_16x16x32_bf16 v[92:95], v[186:189], v[202:205], v[92:95]
	v_mfma_f32_16x16x32_bf16 v[88:91], v[194:197], v[202:205], v[88:91]
	v_mfma_f32_16x16x32_bf16 v[76:79], v[186:189], v[218:221], v[76:79]
	v_mfma_f32_16x16x32_bf16 v[72:75], v[194:197], v[218:221], v[72:75]
	v_mfma_f32_16x16x32_bf16 v[68:71], v[186:189], v[226:229], v[68:71]
	v_mfma_f32_16x16x32_bf16 v[64:67], v[194:197], v[226:229], v[64:67]
	v_mfma_f32_16x16x32_bf16 v[92:95], v[190:193], v[206:209], v[92:95]
	v_mfma_f32_16x16x32_bf16 v[88:91], v[198:201], v[206:209], v[88:91]
	v_mfma_f32_16x16x32_bf16 v[84:87], v[186:189], v[210:213], v[84:87]
	v_mfma_f32_16x16x32_bf16 v[80:83], v[194:197], v[210:213], v[80:83]
	v_mfma_f32_16x16x32_bf16 v[76:79], v[190:193], v[222:225], v[76:79]
	v_mfma_f32_16x16x32_bf16 v[72:75], v[198:201], v[222:225], v[72:75]
	v_mfma_f32_16x16x32_bf16 v[68:71], v[190:193], v[230:233], v[68:71]
	v_mfma_f32_16x16x32_bf16 v[64:67], v[198:201], v[230:233], v[64:67]
	v_mfma_f32_16x16x32_bf16 v[202:205], v[190:193], v[214:217], v[84:87]
	v_mfma_f32_16x16x32_bf16 v[206:209], v[198:201], v[214:217], v[80:83]
	s_barrier
	s_ashr_i32 s5, s85, 31
	s_add_u32 s34, s6, s85
	s_addc_u32 s35, s7, s5
	s_add_i32 s5, s85, 0xffffff00
	s_mov_b32 m0, s27
	v_lshl_add_u64 v[128:129], s[34:35], 0, v[144:145]
	s_ashr_i32 s27, s5, 31
	ds_read_b128 v[80:83], v172 offset:16384
	ds_read_b128 v[84:87], v172 offset:17408
	ds_read_b128 v[96:99], v172 offset:18432
	ds_read_b128 v[100:103], v172 offset:19456
	ds_read_b128 v[210:213], v172 offset:20480
	ds_read_b128 v[214:217], v172 offset:21504
	ds_read_b128 v[218:221], v172 offset:22528
	ds_read_b128 v[222:225], v172 offset:23552
	global_load_lds_dwordx4 v[128:129], off
	v_lshl_add_u64 v[128:129], s[34:35], 0, v[142:143]
	s_add_u32 s34, s6, s5
	s_mov_b32 m0, vcc_hi
	s_addc_u32 s35, s7, s27
	global_load_lds_dwordx4 v[128:129], off
	v_lshl_add_u64 v[128:129], s[34:35], 0, v[144:145]
	s_mov_b32 m0, s59
	s_nop 0
	global_load_lds_dwordx4 v[128:129], off
	v_lshl_add_u64 v[128:129], s[34:35], 0, v[142:143]
	s_add_u32 s34, s3, s4
	s_mov_b32 m0, s60
	s_addc_u32 s35, s36, 0
	global_load_lds_dwordx4 v[128:129], off
	v_lshl_add_u64 v[128:129], s[34:35], 0, v[148:149]
	s_mov_b32 m0, s63
	s_nop 0
	global_load_lds_dwordx4 v[128:129], off
	v_lshl_add_u64 v[128:129], s[34:35], 0, v[146:147]
	s_mov_b32 m0, s66
	s_nop 0
	global_load_lds_dwordx4 v[128:129], off
	s_waitcnt vmcnt(8)
	s_waitcnt lgkmcnt(0)
	s_barrier
	s_waitcnt lgkmcnt(0)
	v_mfma_f32_16x16x32_bf16 v[60:63], v[132:135], v[80:83], v[60:63]
	v_mfma_f32_16x16x32_bf16 v[56:59], v[178:181], v[80:83], v[56:59]
	v_mfma_f32_16x16x32_bf16 v[52:55], v[132:135], v[96:99], v[52:55]
	v_mfma_f32_16x16x32_bf16 v[48:51], v[178:181], v[96:99], v[48:51]
	v_mfma_f32_16x16x32_bf16 v[44:47], v[132:135], v[210:213], v[44:47]
	v_mfma_f32_16x16x32_bf16 v[40:43], v[178:181], v[210:213], v[40:43]
	v_mfma_f32_16x16x32_bf16 v[60:63], v[162:165], v[84:87], v[60:63]
	v_mfma_f32_16x16x32_bf16 v[56:59], v[182:185], v[84:87], v[56:59]
	v_mfma_f32_16x16x32_bf16 v[52:55], v[162:165], v[100:103], v[52:55]
	v_mfma_f32_16x16x32_bf16 v[48:51], v[182:185], v[100:103], v[48:51]
	v_mfma_f32_16x16x32_bf16 v[44:47], v[162:165], v[214:217], v[44:47]
	v_mfma_f32_16x16x32_bf16 v[40:43], v[182:185], v[214:217], v[40:43]
	v_mfma_f32_16x16x32_bf16 v[36:39], v[132:135], v[218:221], v[36:39]
	v_mfma_f32_16x16x32_bf16 v[32:35], v[178:181], v[218:221], v[32:35]
	v_mfma_f32_16x16x32_bf16 v[162:165], v[162:165], v[222:225], v[36:39]
	v_mfma_f32_16x16x32_bf16 v[178:181], v[182:185], v[222:225], v[32:35]
	v_mfma_f32_16x16x32_bf16 v[28:31], v[186:189], v[80:83], v[28:31]
	v_mfma_f32_16x16x32_bf16 v[24:27], v[194:197], v[80:83], v[24:27]
	v_mfma_f32_16x16x32_bf16 v[4:7], v[186:189], v[218:221], v[4:7]
	v_mfma_f32_16x16x32_bf16 v[0:3], v[194:197], v[218:221], v[0:3]
	v_mfma_f32_16x16x32_bf16 v[28:31], v[190:193], v[84:87], v[28:31]
	v_mfma_f32_16x16x32_bf16 v[24:27], v[198:201], v[84:87], v[24:27]
	v_mfma_f32_16x16x32_bf16 v[20:23], v[186:189], v[96:99], v[20:23]
	v_mfma_f32_16x16x32_bf16 v[16:19], v[194:197], v[96:99], v[16:19]
	v_mfma_f32_16x16x32_bf16 v[12:15], v[186:189], v[210:213], v[12:15]
	v_mfma_f32_16x16x32_bf16 v[8:11], v[194:197], v[210:213], v[8:11]
	v_mfma_f32_16x16x32_bf16 v[4:7], v[190:193], v[222:225], v[4:7]
	v_mfma_f32_16x16x32_bf16 v[0:3], v[198:201], v[222:225], v[0:3]
	v_mfma_f32_16x16x32_bf16 v[182:185], v[190:193], v[100:103], v[20:23]
	v_mfma_f32_16x16x32_bf16 v[226:229], v[198:201], v[100:103], v[16:19]
	v_mfma_f32_16x16x32_bf16 v[12:15], v[190:193], v[214:217], v[12:15]
	v_mfma_f32_16x16x32_bf16 v[8:11], v[198:201], v[214:217], v[8:11]
	s_barrier
	ds_read_b128 v[16:19], v130
	ds_read_b128 v[20:23], v130 offset:1024
	ds_read_b128 v[186:189], v130 offset:2048
	ds_read_b128 v[190:193], v130 offset:3072
	ds_read_b128 v[194:197], v131
	ds_read_b128 v[198:201], v131 offset:1024
	ds_read_b128 v[210:213], v131 offset:2048
	ds_read_b128 v[214:217], v131 offset:3072
	s_add_i32 s5, s4, 0x20000
	s_add_u32 s34, s3, s5
	s_addc_u32 s35, s36, 0
	s_mov_b32 m0, s67
	v_lshl_add_u64 v[80:81], s[34:35], 0, v[148:149]
	ds_read_b128 v[32:35], v172 offset:32768
	ds_read_b128 v[36:39], v172 offset:33792
	ds_read_b128 v[218:221], v172 offset:34816
	ds_read_b128 v[222:225], v172 offset:35840
	ds_read_b128 v[230:233], v172 offset:36864
	ds_read_b128 v[242:245], v172 offset:37888
	ds_read_b128 v[246:249], v172 offset:38912
	ds_read_b128 v[250:253], v172 offset:39936
	global_load_lds_dwordx4 v[80:81], off
	v_lshl_add_u64 v[80:81], s[34:35], 0, v[146:147]
	s_mov_b32 m0, s68
	s_nop 0
	global_load_lds_dwordx4 v[80:81], off
	s_waitcnt vmcnt(8)
	s_waitcnt lgkmcnt(0)
	s_barrier
; #define PG_BAR __builtin_amdgcn_s_barrier()
; template <class Epi, class Sched, class Hook = NoHook>
; __device__ __forceinline__ void gemm_phase_w(LAS unsigned char* lds, const Sched& S, const Epi& E, int wave_id, const Hook& HK = Hook()) {
;     ...
;         if constexpr (!SEG2) {
;             for (int tt = 0; tt < nt; tt += 2) {
;                 if constexpr (GATHER) { if (tt == nt - 2) {
;                     if (has_next) { gnxt_00 = S.grow_l(nxt, lds, nbuf, R0) + (unsigned)(C0 * 2); gnxt_01 = S.grow_l(nxt, lds, nbuf, R1) + (unsigned)(C1 * 2); gnxt_10 = S.grow_l(nxt, lds, nbuf, 128 + R0) + (unsigned)(C0 * 2); gnxt_11 = S.grow_l(nxt, lds, nbuf, 128 + R1) + (unsigned)(C1 * 2); }
;                     else { gnxt_00 = gcur_00; gnxt_01 = gcur_01; gnxt_10 = gcur_10; gnxt_11 = gcur_11; } } }
;                 PG_TRIP(tt, false, false, false);
;             }
;         } else {
;             for (int tt = 0; tt < nt - 4; tt += 2) PG_TRIP(tt, false, false, false);
;             PG_TRIP(nt - 4, false, true, false);
;             PG_TRIP(nt - 2, true, false, true);
;         }
;     ...
;         if (wr == 0) PG_BAR;
	s_waitcnt lgkmcnt(0)
	v_mfma_f32_16x16x32_bf16 v[80:83], v[16:19], v[32:35], v[124:127]
	v_mfma_f32_16x16x32_bf16 v[132:135], v[20:23], v[36:39], v[80:83]
	v_mfma_f32_16x16x32_bf16 v[80:83], v[186:189], v[32:35], v[120:123]
	v_mfma_f32_16x16x32_bf16 v[128:131], v[190:193], v[36:39], v[80:83]
	v_mfma_f32_16x16x32_bf16 v[80:83], v[16:19], v[218:221], v[116:119]
	v_mfma_f32_16x16x32_bf16 v[116:119], v[20:23], v[222:225], v[80:83]
	v_mfma_f32_16x16x32_bf16 v[80:83], v[186:189], v[218:221], v[112:115]
	v_mfma_f32_16x16x32_bf16 v[112:115], v[190:193], v[222:225], v[80:83]
	v_mfma_f32_16x16x32_bf16 v[80:83], v[16:19], v[230:233], v[108:111]
	v_mfma_f32_16x16x32_bf16 v[100:103], v[20:23], v[242:245], v[80:83]
	v_mfma_f32_16x16x32_bf16 v[80:83], v[186:189], v[230:233], v[104:107]
	v_mfma_f32_16x16x32_bf16 v[96:99], v[190:193], v[242:245], v[80:83]
	v_mfma_f32_16x16x32_bf16 v[80:83], v[16:19], v[246:249], v[234:237]
	v_mfma_f32_16x16x32_bf16 v[84:87], v[20:23], v[250:253], v[80:83]
	v_mfma_f32_16x16x32_bf16 v[80:83], v[186:189], v[246:249], v[238:241]
	v_mfma_f32_16x16x32_bf16 v[80:83], v[190:193], v[250:253], v[80:83]
	v_mfma_f32_16x16x32_bf16 v[92:95], v[194:197], v[32:35], v[92:95]
	v_mfma_f32_16x16x32_bf16 v[32:35], v[210:213], v[32:35], v[88:91]
	v_mfma_f32_16x16x32_bf16 v[120:123], v[214:217], v[36:39], v[32:35]
	v_mfma_f32_16x16x32_bf16 v[32:35], v[194:197], v[218:221], v[202:205]
	v_mfma_f32_16x16x32_bf16 v[108:111], v[198:201], v[222:225], v[32:35]
	v_mfma_f32_16x16x32_bf16 v[32:35], v[210:213], v[218:221], v[206:209]
	v_mfma_f32_16x16x32_bf16 v[104:107], v[214:217], v[222:225], v[32:35]
	v_mfma_f32_16x16x32_bf16 v[32:35], v[194:197], v[230:233], v[76:79]
	v_mfma_f32_16x16x32_bf16 v[124:127], v[198:201], v[36:39], v[92:95]
	v_mfma_f32_16x16x32_bf16 v[92:95], v[198:201], v[242:245], v[32:35]
	v_mfma_f32_16x16x32_bf16 v[32:35], v[210:213], v[230:233], v[72:75]
	v_mfma_f32_16x16x32_bf16 v[88:91], v[214:217], v[242:245], v[32:35]
	v_mfma_f32_16x16x32_bf16 v[32:35], v[194:197], v[246:249], v[68:71]
	v_mfma_f32_16x16x32_bf16 v[76:79], v[198:201], v[250:253], v[32:35]
	v_mfma_f32_16x16x32_bf16 v[32:35], v[210:213], v[246:249], v[64:67]
	v_mfma_f32_16x16x32_bf16 v[72:75], v[214:217], v[250:253], v[32:35]
	s_barrier
	s_add_i32 s34, s85, 0x80
	s_ashr_i32 s35, s34, 31
	s_add_i32 s5, s85, 0xffffff80
	s_mov_b32 m0, s61
	s_nop 0
	v_lshl_add_u64 v[32:33], v[158:159], 0, s[34:35]
	s_ashr_i32 s27, s5, 31
	ds_read_b128 v[202:205], v172 offset:49152
	ds_read_b128 v[206:209], v172 offset:50176
	ds_read_b128 v[218:221], v172 offset:51200
	ds_read_b128 v[222:225], v172 offset:52224
	ds_read_b128 v[230:233], v172 offset:53248
	ds_read_b128 v[234:237], v172 offset:54272
	ds_read_b128 v[238:241], v172 offset:55296
	ds_read_b128 v[242:245], v172 offset:56320
	global_load_lds_dwordx4 v[32:33], off
	v_lshl_add_u64 v[32:33], v[160:161], 0, s[34:35]
	s_add_u32 s34, s6, s5
	s_mov_b32 m0, s49
	s_addc_u32 s35, s7, s27
	s_add_i32 s5, s4, 0x80
	global_load_lds_dwordx4 v[32:33], off
	v_lshl_add_u64 v[32:33], s[34:35], 0, v[144:145]
	s_mov_b32 m0, s26
	s_add_u32 s26, s3, s5
	global_load_lds_dwordx4 v[32:33], off
	v_lshl_add_u64 v[32:33], s[34:35], 0, v[142:143]
	s_mov_b32 m0, s44
	s_addc_u32 s27, s36, 0
	global_load_lds_dwordx4 v[32:33], off
	v_lshl_add_u64 v[32:33], s[26:27], 0, v[148:149]
	s_mov_b32 m0, s71
	s_nop 0
	global_load_lds_dwordx4 v[32:33], off
	v_lshl_add_u64 v[32:33], s[26:27], 0, v[146:147]
	s_mov_b32 m0, s72
	s_nop 0
	global_load_lds_dwordx4 v[32:33], off
	s_waitcnt vmcnt(8)
	s_waitcnt lgkmcnt(0)
	s_barrier
	s_waitcnt lgkmcnt(0)
	v_mfma_f32_16x16x32_bf16 v[32:35], v[16:19], v[202:205], v[60:63]
	v_mfma_f32_16x16x32_bf16 v[68:71], v[20:23], v[206:209], v[32:35]
	v_mfma_f32_16x16x32_bf16 v[32:35], v[186:189], v[202:205], v[56:59]
	v_mfma_f32_16x16x32_bf16 v[64:67], v[190:193], v[206:209], v[32:35]
	v_mfma_f32_16x16x32_bf16 v[32:35], v[16:19], v[218:221], v[52:55]
	v_mfma_f32_16x16x32_bf16 v[52:55], v[20:23], v[222:225], v[32:35]
	v_mfma_f32_16x16x32_bf16 v[32:35], v[186:189], v[218:221], v[48:51]
	v_mfma_f32_16x16x32_bf16 v[48:51], v[190:193], v[222:225], v[32:35]
	v_mfma_f32_16x16x32_bf16 v[32:35], v[16:19], v[230:233], v[44:47]
	v_mfma_f32_16x16x32_bf16 v[16:19], v[16:19], v[238:241], v[162:165]
	v_mfma_f32_16x16x32_bf16 v[36:39], v[20:23], v[234:237], v[32:35]
	v_mfma_f32_16x16x32_bf16 v[32:35], v[186:189], v[230:233], v[40:43]
	v_mfma_f32_16x16x32_bf16 v[20:23], v[20:23], v[242:245], v[16:19]
	v_mfma_f32_16x16x32_bf16 v[16:19], v[186:189], v[238:241], v[178:181]
	v_mfma_f32_16x16x32_bf16 v[32:35], v[190:193], v[234:237], v[32:35]
	v_mfma_f32_16x16x32_bf16 v[16:19], v[190:193], v[242:245], v[16:19]
	v_mfma_f32_16x16x32_bf16 v[24:27], v[210:213], v[202:205], v[24:27]
	v_mfma_f32_16x16x32_bf16 v[56:59], v[214:217], v[206:209], v[24:27]
	v_mfma_f32_16x16x32_bf16 v[24:27], v[194:197], v[218:221], v[182:185]
	v_mfma_f32_16x16x32_bf16 v[28:31], v[194:197], v[202:205], v[28:31]
	v_mfma_f32_16x16x32_bf16 v[44:47], v[198:201], v[222:225], v[24:27]
	v_mfma_f32_16x16x32_bf16 v[24:27], v[210:213], v[218:221], v[226:229]
	v_mfma_f32_16x16x32_bf16 v[12:15], v[194:197], v[230:233], v[12:15]
	v_mfma_f32_16x16x32_bf16 v[8:11], v[210:213], v[230:233], v[8:11]
	v_mfma_f32_16x16x32_bf16 v[4:7], v[194:197], v[238:241], v[4:7]
	v_mfma_f32_16x16x32_bf16 v[0:3], v[210:213], v[238:241], v[0:3]
	v_mfma_f32_16x16x32_bf16 v[60:63], v[198:201], v[206:209], v[28:31]
	v_mfma_f32_16x16x32_bf16 v[40:43], v[214:217], v[222:225], v[24:27]
	v_mfma_f32_16x16x32_bf16 v[28:31], v[198:201], v[234:237], v[12:15]
	v_mfma_f32_16x16x32_bf16 v[24:27], v[214:217], v[234:237], v[8:11]
	v_mfma_f32_16x16x32_bf16 v[4:7], v[198:201], v[242:245], v[4:7]
	v_mfma_f32_16x16x32_bf16 v[0:3], v[214:217], v[242:245], v[0:3]
	s_barrier
	s_and_b64 vcc, exec, s[64:65]
	s_cbranch_vccz .LBB0_1779
	s_barrier

.LBB0_1854:
	ds_read_b128 v[100:103], v197
	ds_read_b128 v[132:135], v197 offset:1024
	ds_read_b128 v[136:139], v197 offset:2048
	ds_read_b128 v[140:143], v197 offset:3072
	ds_read_b128 v[144:147], v198
	ds_read_b128 v[148:151], v198 offset:1024
	ds_read_b128 v[152:155], v198 offset:2048
	ds_read_b128 v[156:159], v198 offset:3072
	s_add_i32 s53, s21, 2
	s_cmp_eq_u32 s20, 0x9f000
	s_cselect_b32 s59, s48, s51
	s_cselect_b32 s60, 0, s53
	s_cselect_b32 s58, s49, s52
	s_add_i32 s61, s52, s20
	s_add_u32 s62, s3, s61
	s_addc_u32 s63, s30, 0
	v_lshl_add_u64 v[190:191], s[62:63], 0, v[164:165]
	s_add_i32 m0, s23, 0xc000
	ds_read_b128 v[160:163], v199
	ds_read_b128 v[174:177], v199 offset:1024
	ds_read_b128 v[178:181], v199 offset:2048
	ds_read_b128 v[182:185], v199 offset:3072
	ds_read_b128 v[186:189], v199 offset:4096
	ds_read_b128 v[200:203], v199 offset:5120
	ds_read_b128 v[204:207], v199 offset:6144
	ds_read_b128 v[208:211], v199 offset:7168
	global_load_lds_dwordx4 v[190:191], off
	v_lshl_add_u64 v[190:191], s[62:63], 0, v[166:167]
	s_add_i32 m0, s23, 0xe000
	s_nop 0
	global_load_lds_dwordx4 v[190:191], off
	s_waitcnt vmcnt(8)
	s_waitcnt lgkmcnt(0)
	s_barrier
	s_waitcnt lgkmcnt(0)
	v_mfma_f32_16x16x32_bf16 v[128:131], v[100:103], v[160:163], v[128:131]
	v_mfma_f32_16x16x32_bf16 v[124:127], v[136:139], v[160:163], v[124:127]
	v_mfma_f32_16x16x32_bf16 v[116:119], v[100:103], v[178:181], v[116:119]
	v_mfma_f32_16x16x32_bf16 v[108:111], v[136:139], v[178:181], v[108:111]
	v_mfma_f32_16x16x32_bf16 v[92:95], v[100:103], v[186:189], v[92:95]
	v_mfma_f32_16x16x32_bf16 v[84:87], v[136:139], v[186:189], v[84:87]
	v_mfma_f32_16x16x32_bf16 v[76:79], v[100:103], v[204:207], v[76:79]
	v_mfma_f32_16x16x32_bf16 v[68:71], v[136:139], v[204:207], v[68:71]
	v_mfma_f32_16x16x32_bf16 v[128:131], v[132:135], v[174:177], v[128:131]
	v_mfma_f32_16x16x32_bf16 v[124:127], v[140:143], v[174:177], v[124:127]
	v_mfma_f32_16x16x32_bf16 v[116:119], v[132:135], v[182:185], v[116:119]
	v_mfma_f32_16x16x32_bf16 v[108:111], v[140:143], v[182:185], v[108:111]
	v_mfma_f32_16x16x32_bf16 v[92:95], v[132:135], v[200:203], v[92:95]
	v_mfma_f32_16x16x32_bf16 v[84:87], v[140:143], v[200:203], v[84:87]
	v_mfma_f32_16x16x32_bf16 v[76:79], v[132:135], v[208:211], v[76:79]
	v_mfma_f32_16x16x32_bf16 v[68:71], v[140:143], v[208:211], v[68:71]
	v_mfma_f32_16x16x32_bf16 v[96:99], v[144:147], v[160:163], v[96:99]
	v_mfma_f32_16x16x32_bf16 v[120:123], v[152:155], v[160:163], v[120:123]
	v_mfma_f32_16x16x32_bf16 v[112:115], v[144:147], v[178:181], v[112:115]
	v_mfma_f32_16x16x32_bf16 v[104:107], v[152:155], v[178:181], v[104:107]
	v_mfma_f32_16x16x32_bf16 v[88:91], v[144:147], v[186:189], v[88:91]
	v_mfma_f32_16x16x32_bf16 v[80:83], v[152:155], v[186:189], v[80:83]
	v_mfma_f32_16x16x32_bf16 v[72:75], v[144:147], v[204:207], v[72:75]
	v_mfma_f32_16x16x32_bf16 v[64:67], v[152:155], v[204:207], v[64:67]
	v_mfma_f32_16x16x32_bf16 v[96:99], v[148:151], v[174:177], v[96:99]
	v_mfma_f32_16x16x32_bf16 v[120:123], v[156:159], v[174:177], v[120:123]
	v_mfma_f32_16x16x32_bf16 v[112:115], v[148:151], v[182:185], v[112:115]
	v_mfma_f32_16x16x32_bf16 v[104:107], v[156:159], v[182:185], v[104:107]
	v_mfma_f32_16x16x32_bf16 v[88:91], v[148:151], v[200:203], v[88:91]
	v_mfma_f32_16x16x32_bf16 v[80:83], v[156:159], v[200:203], v[80:83]
	v_mfma_f32_16x16x32_bf16 v[72:75], v[148:151], v[208:211], v[72:75]
	v_mfma_f32_16x16x32_bf16 v[64:67], v[156:159], v[208:211], v[64:67]
	s_barrier
	s_lshl_b32 s61, s60, 7
	s_add_i32 s62, s61, s59
	s_ashr_i32 s63, s62, 31
	s_add_u32 s62, s4, s62
	s_addc_u32 s63, s5, s63
	s_add_i32 s66, s42, s31
	v_lshl_add_u64 v[190:191], s[62:63], 0, v[168:169]
	s_mov_b32 m0, s66
	ds_read_b128 v[160:163], v199 offset:16384
	ds_read_b128 v[174:177], v199 offset:17408
	ds_read_b128 v[178:181], v199 offset:18432
	ds_read_b128 v[182:185], v199 offset:19456
	ds_read_b128 v[186:189], v199 offset:20480
	ds_read_b128 v[200:203], v199 offset:21504
	ds_read_b128 v[204:207], v199 offset:22528
	ds_read_b128 v[208:211], v199 offset:23552
	global_load_lds_dwordx4 v[190:191], off
	s_add_i32 m0, s66, 0x2000
	s_add_i32 s66, s59, 0x80000
	s_add_i32 s61, s66, s61
	v_lshl_add_u64 v[190:191], s[62:63], 0, v[170:171]
	s_ashr_i32 s63, s61, 31
	s_add_u32 s62, s4, s61
	s_addc_u32 s63, s5, s63
	s_add_i32 s61, s43, s31
	global_load_lds_dwordx4 v[190:191], off
	v_lshl_add_u64 v[190:191], s[62:63], 0, v[168:169]
	s_mov_b32 m0, s61
	s_nop 0
	global_load_lds_dwordx4 v[190:191], off
	s_add_i32 m0, s61, 0x2000
	s_lshl_b32 s61, s60, 12
	s_add_i32 s61, s61, s58
	v_lshl_add_u64 v[190:191], s[62:63], 0, v[170:171]
	s_add_u32 s62, s3, s61
	s_addc_u32 s63, s30, 0
	global_load_lds_dwordx4 v[190:191], off
	v_lshl_add_u64 v[190:191], s[62:63], 0, v[164:165]
	s_mov_b32 m0, s23
	s_nop 0
	global_load_lds_dwordx4 v[190:191], off
	v_lshl_add_u64 v[190:191], s[62:63], 0, v[166:167]
	s_mov_b32 m0, s24
	s_nop 0
	global_load_lds_dwordx4 v[190:191], off
	s_waitcnt vmcnt(8)
	s_waitcnt lgkmcnt(0)
	s_barrier
	s_waitcnt lgkmcnt(0)
	v_mfma_f32_16x16x32_bf16 v[60:63], v[100:103], v[160:163], v[60:63]
	v_mfma_f32_16x16x32_bf16 v[52:55], v[136:139], v[160:163], v[52:55]
	v_mfma_f32_16x16x32_bf16 v[44:47], v[100:103], v[178:181], v[44:47]
	v_mfma_f32_16x16x32_bf16 v[36:39], v[136:139], v[178:181], v[36:39]
	v_mfma_f32_16x16x32_bf16 v[28:31], v[100:103], v[186:189], v[28:31]
	v_mfma_f32_16x16x32_bf16 v[20:23], v[136:139], v[186:189], v[20:23]
	v_mfma_f32_16x16x32_bf16 v[12:15], v[100:103], v[204:207], v[12:15]
	v_mfma_f32_16x16x32_bf16 v[4:7], v[136:139], v[204:207], v[4:7]
	v_mfma_f32_16x16x32_bf16 v[60:63], v[132:135], v[174:177], v[60:63]
	v_mfma_f32_16x16x32_bf16 v[52:55], v[140:143], v[174:177], v[52:55]
	v_mfma_f32_16x16x32_bf16 v[44:47], v[132:135], v[182:185], v[44:47]
	v_mfma_f32_16x16x32_bf16 v[36:39], v[140:143], v[182:185], v[36:39]
	v_mfma_f32_16x16x32_bf16 v[28:31], v[132:135], v[200:203], v[28:31]
	v_mfma_f32_16x16x32_bf16 v[20:23], v[140:143], v[200:203], v[20:23]
	v_mfma_f32_16x16x32_bf16 v[12:15], v[132:135], v[208:211], v[12:15]
	v_mfma_f32_16x16x32_bf16 v[4:7], v[140:143], v[208:211], v[4:7]
	v_mfma_f32_16x16x32_bf16 v[56:59], v[144:147], v[160:163], v[56:59]
	v_mfma_f32_16x16x32_bf16 v[48:51], v[152:155], v[160:163], v[48:51]
	v_mfma_f32_16x16x32_bf16 v[40:43], v[144:147], v[178:181], v[40:43]
	v_mfma_f32_16x16x32_bf16 v[32:35], v[152:155], v[178:181], v[32:35]
	v_mfma_f32_16x16x32_bf16 v[24:27], v[144:147], v[186:189], v[24:27]
	v_mfma_f32_16x16x32_bf16 v[16:19], v[152:155], v[186:189], v[16:19]
	v_mfma_f32_16x16x32_bf16 v[8:11], v[144:147], v[204:207], v[8:11]
	v_mfma_f32_16x16x32_bf16 v[0:3], v[152:155], v[204:207], v[0:3]
	v_mfma_f32_16x16x32_bf16 v[56:59], v[148:151], v[174:177], v[56:59]
	v_mfma_f32_16x16x32_bf16 v[48:51], v[156:159], v[174:177], v[48:51]
	v_mfma_f32_16x16x32_bf16 v[40:43], v[148:151], v[182:185], v[40:43]
	v_mfma_f32_16x16x32_bf16 v[32:35], v[156:159], v[182:185], v[32:35]
	v_mfma_f32_16x16x32_bf16 v[24:27], v[148:151], v[200:203], v[24:27]
	v_mfma_f32_16x16x32_bf16 v[16:19], v[156:159], v[200:203], v[16:19]
	v_mfma_f32_16x16x32_bf16 v[8:11], v[148:151], v[208:211], v[8:11]
	v_mfma_f32_16x16x32_bf16 v[0:3], v[156:159], v[208:211], v[0:3]
	s_barrier
	s_add_i32 s67, 0, 0x18000
	s_add_i32 s68, 0, 0x1c000
	v_add_u32_e32 v140, s67, v195
	v_add_u32_e32 v156, s68, v195
	ds_read_b128 v[100:103], v140
	ds_read_b128 v[132:135], v140 offset:1024
	ds_read_b128 v[136:139], v140 offset:2048
	ds_read_b128 v[140:143], v140 offset:3072
	ds_read_b128 v[144:147], v156
	ds_read_b128 v[148:151], v156 offset:1024
	ds_read_b128 v[152:155], v156 offset:2048
	ds_read_b128 v[156:159], v156 offset:3072
	s_add_i32 s61, s61, 0x80000
	s_add_u32 s62, s3, s61
	s_addc_u32 s63, s30, 0
	s_mov_b32 m0, s25
	v_lshl_add_u64 v[190:191], s[62:63], 0, v[164:165]
	ds_read_b128 v[160:163], v199 offset:32768
	ds_read_b128 v[174:177], v199 offset:33792
	ds_read_b128 v[178:181], v199 offset:34816
	ds_read_b128 v[182:185], v199 offset:35840
	ds_read_b128 v[186:189], v199 offset:36864
	ds_read_b128 v[200:203], v199 offset:37888
	ds_read_b128 v[204:207], v199 offset:38912
	ds_read_b128 v[208:211], v199 offset:39936
	global_load_lds_dwordx4 v[190:191], off
	v_lshl_add_u64 v[190:191], s[62:63], 0, v[166:167]
	s_mov_b32 m0, s26
	s_nop 0
	global_load_lds_dwordx4 v[190:191], off
	s_waitcnt vmcnt(8)
	s_waitcnt lgkmcnt(0)
	s_barrier
	s_waitcnt lgkmcnt(0)
	v_mfma_f32_16x16x32_bf16 v[128:131], v[100:103], v[160:163], v[128:131]
	v_mfma_f32_16x16x32_bf16 v[124:127], v[136:139], v[160:163], v[124:127]
	v_mfma_f32_16x16x32_bf16 v[116:119], v[100:103], v[178:181], v[116:119]
	v_mfma_f32_16x16x32_bf16 v[108:111], v[136:139], v[178:181], v[108:111]
	v_mfma_f32_16x16x32_bf16 v[92:95], v[100:103], v[186:189], v[92:95]
	v_mfma_f32_16x16x32_bf16 v[84:87], v[136:139], v[186:189], v[84:87]
	v_mfma_f32_16x16x32_bf16 v[76:79], v[100:103], v[204:207], v[76:79]
	v_mfma_f32_16x16x32_bf16 v[68:71], v[136:139], v[204:207], v[68:71]
	v_mfma_f32_16x16x32_bf16 v[128:131], v[132:135], v[174:177], v[128:131]
	v_mfma_f32_16x16x32_bf16 v[124:127], v[140:143], v[174:177], v[124:127]
	v_mfma_f32_16x16x32_bf16 v[116:119], v[132:135], v[182:185], v[116:119]
	v_mfma_f32_16x16x32_bf16 v[108:111], v[140:143], v[182:185], v[108:111]
	v_mfma_f32_16x16x32_bf16 v[92:95], v[132:135], v[200:203], v[92:95]
	v_mfma_f32_16x16x32_bf16 v[84:87], v[140:143], v[200:203], v[84:87]
	v_mfma_f32_16x16x32_bf16 v[76:79], v[132:135], v[208:211], v[76:79]
	v_mfma_f32_16x16x32_bf16 v[68:71], v[140:143], v[208:211], v[68:71]
	v_mfma_f32_16x16x32_bf16 v[96:99], v[144:147], v[160:163], v[96:99]
	v_mfma_f32_16x16x32_bf16 v[120:123], v[152:155], v[160:163], v[120:123]
	v_mfma_f32_16x16x32_bf16 v[112:115], v[144:147], v[178:181], v[112:115]
	v_mfma_f32_16x16x32_bf16 v[104:107], v[152:155], v[178:181], v[104:107]
	v_mfma_f32_16x16x32_bf16 v[88:91], v[144:147], v[186:189], v[88:91]
	v_mfma_f32_16x16x32_bf16 v[80:83], v[152:155], v[186:189], v[80:83]
	v_mfma_f32_16x16x32_bf16 v[72:75], v[144:147], v[204:207], v[72:75]
	v_mfma_f32_16x16x32_bf16 v[64:67], v[152:155], v[204:207], v[64:67]
	v_mfma_f32_16x16x32_bf16 v[96:99], v[148:151], v[174:177], v[96:99]
	v_mfma_f32_16x16x32_bf16 v[120:123], v[156:159], v[174:177], v[120:123]
	v_mfma_f32_16x16x32_bf16 v[112:115], v[148:151], v[182:185], v[112:115]
	v_mfma_f32_16x16x32_bf16 v[104:107], v[156:159], v[182:185], v[104:107]
	v_mfma_f32_16x16x32_bf16 v[88:91], v[148:151], v[200:203], v[88:91]
	v_mfma_f32_16x16x32_bf16 v[80:83], v[156:159], v[200:203], v[80:83]
	v_mfma_f32_16x16x32_bf16 v[72:75], v[148:151], v[208:211], v[72:75]
	v_mfma_f32_16x16x32_bf16 v[64:67], v[156:159], v[208:211], v[64:67]
	s_barrier
; #define PG_BAR __builtin_amdgcn_s_barrier()
; template <class Epi, class Sched, class Hook = NoHook>
; __device__ __forceinline__ void gemm_phase_w(LAS unsigned char* lds, const Sched& S, const Epi& E, int wave_id, const Hook& HK = Hook()) {
;     ...
;         if constexpr (!SEG2) {
;             for (int tt = 0; tt < nt; tt += 2) {
;                 if constexpr (GATHER) { if (tt == nt - 2) {
;                     if (has_next) { gnxt_00 = S.grow_l(nxt, lds, nbuf, R0) + (unsigned)(C0 * 2); gnxt_01 = S.grow_l(nxt, lds, nbuf, R1) + (unsigned)(C1 * 2); gnxt_10 = S.grow_l(nxt, lds, nbuf, 128 + R0) + (unsigned)(C0 * 2); gnxt_11 = S.grow_l(nxt, lds, nbuf, 128 + R1) + (unsigned)(C1 * 2); }
;                     else { gnxt_00 = gcur_00; gnxt_01 = gcur_01; gnxt_10 = gcur_10; gnxt_11 = gcur_11; } } }
;                 PG_TRIP(tt, false, false, false);
;             }
;         } else {
;             for (int tt = 0; tt < nt - 4; tt += 2) PG_TRIP(tt, false, false, false);
;             PG_TRIP(nt - 4, false, true, false);
;             PG_TRIP(nt - 2, true, false, true);
;         }
;     ...
;         if (wr == 0) PG_BAR;
	s_or_b32 s62, s60, 1
	s_lshl_b32 s63, s62, 7
	s_add_i32 s59, s63, s59
	s_ashr_i32 s61, s59, 31
	s_add_u32 s60, s4, s59
	s_addc_u32 s61, s5, s61
	s_add_i32 s59, s67, s31
	v_lshl_add_u64 v[190:191], s[60:61], 0, v[168:169]
	s_mov_b32 m0, s59
	s_add_i32 s63, s63, s66
	ds_read_b128 v[160:163], v199 offset:49152
	ds_read_b128 v[174:177], v199 offset:50176
	ds_read_b128 v[178:181], v199 offset:51200
	ds_read_b128 v[182:185], v199 offset:52224
	ds_read_b128 v[186:189], v199 offset:53248
	ds_read_b128 v[200:203], v199 offset:54272
	ds_read_b128 v[204:207], v199 offset:55296
	ds_read_b128 v[208:211], v199 offset:56320
	global_load_lds_dwordx4 v[190:191], off
	s_add_i32 m0, s59, 0x2000
	s_ashr_i32 s59, s63, 31
	v_lshl_add_u64 v[190:191], s[60:61], 0, v[170:171]
	s_add_u32 s60, s4, s63
	s_addc_u32 s61, s5, s59
	s_add_i32 s59, s68, s31
	global_load_lds_dwordx4 v[190:191], off
	v_lshl_add_u64 v[190:191], s[60:61], 0, v[168:169]
	s_mov_b32 m0, s59
	s_nop 0
	global_load_lds_dwordx4 v[190:191], off
	s_add_i32 m0, s59, 0x2000
	s_lshl_b32 s59, s62, 12
	s_add_i32 s59, s59, s58
	s_add_u32 s58, s3, s59
	v_lshl_add_u64 v[190:191], s[60:61], 0, v[170:171]
	s_addc_u32 s59, s30, 0
	global_load_lds_dwordx4 v[190:191], off
	v_lshl_add_u64 v[190:191], s[58:59], 0, v[164:165]
	s_mov_b32 m0, s28
	s_nop 0
	global_load_lds_dwordx4 v[190:191], off
	v_lshl_add_u64 v[190:191], s[58:59], 0, v[166:167]
	s_mov_b32 m0, s29
	s_nop 0
	global_load_lds_dwordx4 v[190:191], off
	s_waitcnt vmcnt(8)
	s_waitcnt lgkmcnt(0)
	s_barrier
	s_waitcnt lgkmcnt(0)
	v_mfma_f32_16x16x32_bf16 v[60:63], v[100:103], v[160:163], v[60:63]
	v_mfma_f32_16x16x32_bf16 v[52:55], v[136:139], v[160:163], v[52:55]
	v_mfma_f32_16x16x32_bf16 v[44:47], v[100:103], v[178:181], v[44:47]
	v_mfma_f32_16x16x32_bf16 v[36:39], v[136:139], v[178:181], v[36:39]
	v_mfma_f32_16x16x32_bf16 v[28:31], v[100:103], v[186:189], v[28:31]
	v_mfma_f32_16x16x32_bf16 v[20:23], v[136:139], v[186:189], v[20:23]
	v_mfma_f32_16x16x32_bf16 v[12:15], v[100:103], v[204:207], v[12:15]
	v_mfma_f32_16x16x32_bf16 v[4:7], v[136:139], v[204:207], v[4:7]
	v_mfma_f32_16x16x32_bf16 v[60:63], v[132:135], v[174:177], v[60:63]
	v_mfma_f32_16x16x32_bf16 v[52:55], v[140:143], v[174:177], v[52:55]
	v_mfma_f32_16x16x32_bf16 v[44:47], v[132:135], v[182:185], v[44:47]
	v_mfma_f32_16x16x32_bf16 v[36:39], v[140:143], v[182:185], v[36:39]
	v_mfma_f32_16x16x32_bf16 v[28:31], v[132:135], v[200:203], v[28:31]
	v_mfma_f32_16x16x32_bf16 v[20:23], v[140:143], v[200:203], v[20:23]
	v_mfma_f32_16x16x32_bf16 v[12:15], v[132:135], v[208:211], v[12:15]
	v_mfma_f32_16x16x32_bf16 v[4:7], v[140:143], v[208:211], v[4:7]
	v_mfma_f32_16x16x32_bf16 v[56:59], v[144:147], v[160:163], v[56:59]
	v_mfma_f32_16x16x32_bf16 v[48:51], v[152:155], v[160:163], v[48:51]
	v_mfma_f32_16x16x32_bf16 v[40:43], v[144:147], v[178:181], v[40:43]
	v_mfma_f32_16x16x32_bf16 v[32:35], v[152:155], v[178:181], v[32:35]
	v_mfma_f32_16x16x32_bf16 v[24:27], v[144:147], v[186:189], v[24:27]
	v_mfma_f32_16x16x32_bf16 v[16:19], v[152:155], v[186:189], v[16:19]
	v_mfma_f32_16x16x32_bf16 v[8:11], v[144:147], v[204:207], v[8:11]
	v_mfma_f32_16x16x32_bf16 v[0:3], v[152:155], v[204:207], v[0:3]
	v_mfma_f32_16x16x32_bf16 v[56:59], v[148:151], v[174:177], v[56:59]
	v_mfma_f32_16x16x32_bf16 v[48:51], v[156:159], v[174:177], v[48:51]
	v_mfma_f32_16x16x32_bf16 v[40:43], v[148:151], v[182:185], v[40:43]
	v_mfma_f32_16x16x32_bf16 v[32:35], v[156:159], v[182:185], v[32:35]
	v_mfma_f32_16x16x32_bf16 v[24:27], v[148:151], v[200:203], v[24:27]
	v_mfma_f32_16x16x32_bf16 v[16:19], v[156:159], v[200:203], v[16:19]
	v_mfma_f32_16x16x32_bf16 v[8:11], v[148:151], v[208:211], v[8:11]
	v_mfma_f32_16x16x32_bf16 v[0:3], v[156:159], v[208:211], v[0:3]
	s_addk_i32 s20, 0x2000
	s_cmp_gt_u32 s21, 29
	s_mov_b32 s21, s53
	s_barrier
	s_cbranch_scc0 .LBB0_1854
	s_and_b64 vcc, exec, s[16:17]
	s_cbranch_vccz .LBB0_1857
	s_barrier

.LBB0_1983:
	ds_read_b128 v[100:103], v195
	ds_read_b128 v[132:135], v195 offset:1024
	ds_read_b128 v[136:139], v195 offset:2048
	ds_read_b128 v[140:143], v195 offset:3072
	ds_read_b128 v[144:147], v196
	ds_read_b128 v[148:151], v196 offset:1024
	ds_read_b128 v[152:155], v196 offset:2048
	ds_read_b128 v[156:159], v196 offset:3072
	s_add_i32 s45, s21, 2
	s_cmp_eq_u32 s20, 0x9f000
	s_cselect_b32 s49, s40, s43
	s_cselect_b32 s50, 0, s45
	s_cselect_b32 s48, s41, s44
	s_add_i32 s51, s44, s20
	s_add_u32 s52, s3, s51
	s_addc_u32 s53, s30, 0
	v_lshl_add_u64 v[190:191], s[52:53], 0, v[164:165]
	s_add_i32 m0, s24, 0xc000
	ds_read_b128 v[160:163], v197
	ds_read_b128 v[174:177], v197 offset:1024
	ds_read_b128 v[178:181], v197 offset:2048
	ds_read_b128 v[182:185], v197 offset:3072
	ds_read_b128 v[186:189], v197 offset:4096
	ds_read_b128 v[198:201], v197 offset:5120
	ds_read_b128 v[202:205], v197 offset:6144
	ds_read_b128 v[206:209], v197 offset:7168
	global_load_lds_dwordx4 v[190:191], off
	v_lshl_add_u64 v[190:191], s[52:53], 0, v[166:167]
	s_add_i32 m0, s24, 0xe000
	s_nop 0
	global_load_lds_dwordx4 v[190:191], off
	s_waitcnt vmcnt(8)
	s_waitcnt lgkmcnt(0)
	s_barrier
	s_waitcnt lgkmcnt(0)
	v_mfma_f32_16x16x32_bf16 v[128:131], v[100:103], v[160:163], v[128:131]
	v_mfma_f32_16x16x32_bf16 v[124:127], v[136:139], v[160:163], v[124:127]
	v_mfma_f32_16x16x32_bf16 v[116:119], v[100:103], v[178:181], v[116:119]
	v_mfma_f32_16x16x32_bf16 v[108:111], v[136:139], v[178:181], v[108:111]
	v_mfma_f32_16x16x32_bf16 v[92:95], v[100:103], v[186:189], v[92:95]
	v_mfma_f32_16x16x32_bf16 v[84:87], v[136:139], v[186:189], v[84:87]
	v_mfma_f32_16x16x32_bf16 v[76:79], v[100:103], v[202:205], v[76:79]
	v_mfma_f32_16x16x32_bf16 v[68:71], v[136:139], v[202:205], v[68:71]
	v_mfma_f32_16x16x32_bf16 v[128:131], v[132:135], v[174:177], v[128:131]
	v_mfma_f32_16x16x32_bf16 v[124:127], v[140:143], v[174:177], v[124:127]
	v_mfma_f32_16x16x32_bf16 v[116:119], v[132:135], v[182:185], v[116:119]
	v_mfma_f32_16x16x32_bf16 v[108:111], v[140:143], v[182:185], v[108:111]
	v_mfma_f32_16x16x32_bf16 v[92:95], v[132:135], v[198:201], v[92:95]
	v_mfma_f32_16x16x32_bf16 v[84:87], v[140:143], v[198:201], v[84:87]
	v_mfma_f32_16x16x32_bf16 v[76:79], v[132:135], v[206:209], v[76:79]
	v_mfma_f32_16x16x32_bf16 v[68:71], v[140:143], v[206:209], v[68:71]
	v_mfma_f32_16x16x32_bf16 v[96:99], v[144:147], v[160:163], v[96:99]
	v_mfma_f32_16x16x32_bf16 v[120:123], v[152:155], v[160:163], v[120:123]
	v_mfma_f32_16x16x32_bf16 v[112:115], v[144:147], v[178:181], v[112:115]
	v_mfma_f32_16x16x32_bf16 v[104:107], v[152:155], v[178:181], v[104:107]
	v_mfma_f32_16x16x32_bf16 v[88:91], v[144:147], v[186:189], v[88:91]
	v_mfma_f32_16x16x32_bf16 v[80:83], v[152:155], v[186:189], v[80:83]
	v_mfma_f32_16x16x32_bf16 v[72:75], v[144:147], v[202:205], v[72:75]
	v_mfma_f32_16x16x32_bf16 v[64:67], v[152:155], v[202:205], v[64:67]
	v_mfma_f32_16x16x32_bf16 v[96:99], v[148:151], v[174:177], v[96:99]
	v_mfma_f32_16x16x32_bf16 v[120:123], v[156:159], v[174:177], v[120:123]
	v_mfma_f32_16x16x32_bf16 v[112:115], v[148:151], v[182:185], v[112:115]
	v_mfma_f32_16x16x32_bf16 v[104:107], v[156:159], v[182:185], v[104:107]
	v_mfma_f32_16x16x32_bf16 v[88:91], v[148:151], v[198:201], v[88:91]
	v_mfma_f32_16x16x32_bf16 v[80:83], v[156:159], v[198:201], v[80:83]
	v_mfma_f32_16x16x32_bf16 v[72:75], v[148:151], v[206:209], v[72:75]
	v_mfma_f32_16x16x32_bf16 v[64:67], v[156:159], v[206:209], v[64:67]
	s_barrier
	s_lshl_b32 s51, s50, 7
	s_add_i32 s52, s51, s49
	s_ashr_i32 s53, s52, 31
	s_add_u32 s52, s4, s52
	s_addc_u32 s53, s5, s53
	s_add_i32 s58, s34, s31
	v_lshl_add_u64 v[190:191], s[52:53], 0, v[168:169]
	s_mov_b32 m0, s58
	ds_read_b128 v[160:163], v197 offset:16384
	ds_read_b128 v[174:177], v197 offset:17408
	ds_read_b128 v[178:181], v197 offset:18432
	ds_read_b128 v[182:185], v197 offset:19456
	ds_read_b128 v[186:189], v197 offset:20480
	ds_read_b128 v[198:201], v197 offset:21504
	ds_read_b128 v[202:205], v197 offset:22528
	ds_read_b128 v[206:209], v197 offset:23552
	global_load_lds_dwordx4 v[190:191], off
	s_add_i32 m0, s58, 0x2000
	s_add_i32 s58, s49, 0x80000
	s_add_i32 s51, s58, s51
	v_lshl_add_u64 v[190:191], s[52:53], 0, v[170:171]
	s_ashr_i32 s53, s51, 31
	s_add_u32 s52, s4, s51
	s_addc_u32 s53, s5, s53
	s_add_i32 s51, s36, s31
	global_load_lds_dwordx4 v[190:191], off
	v_lshl_add_u64 v[190:191], s[52:53], 0, v[168:169]
	s_mov_b32 m0, s51
	s_nop 0
	global_load_lds_dwordx4 v[190:191], off
	s_add_i32 m0, s51, 0x2000
	s_lshl_b32 s51, s50, 12
	s_add_i32 s51, s51, s48
	v_lshl_add_u64 v[190:191], s[52:53], 0, v[170:171]
	s_add_u32 s52, s3, s51
	s_addc_u32 s53, s30, 0
	global_load_lds_dwordx4 v[190:191], off
	v_lshl_add_u64 v[190:191], s[52:53], 0, v[164:165]
	s_mov_b32 m0, s24
	s_nop 0
	global_load_lds_dwordx4 v[190:191], off
	v_lshl_add_u64 v[190:191], s[52:53], 0, v[166:167]
	s_mov_b32 m0, s25
	s_nop 0
	global_load_lds_dwordx4 v[190:191], off
	s_waitcnt vmcnt(8)
	s_waitcnt lgkmcnt(0)
	s_barrier
	s_waitcnt lgkmcnt(0)
	v_mfma_f32_16x16x32_bf16 v[60:63], v[100:103], v[160:163], v[60:63]
	v_mfma_f32_16x16x32_bf16 v[52:55], v[136:139], v[160:163], v[52:55]
	v_mfma_f32_16x16x32_bf16 v[44:47], v[100:103], v[178:181], v[44:47]
	v_mfma_f32_16x16x32_bf16 v[36:39], v[136:139], v[178:181], v[36:39]
	v_mfma_f32_16x16x32_bf16 v[28:31], v[100:103], v[186:189], v[28:31]
	v_mfma_f32_16x16x32_bf16 v[20:23], v[136:139], v[186:189], v[20:23]
	v_mfma_f32_16x16x32_bf16 v[12:15], v[100:103], v[202:205], v[12:15]
	v_mfma_f32_16x16x32_bf16 v[4:7], v[136:139], v[202:205], v[4:7]
	v_mfma_f32_16x16x32_bf16 v[60:63], v[132:135], v[174:177], v[60:63]
	v_mfma_f32_16x16x32_bf16 v[52:55], v[140:143], v[174:177], v[52:55]
	v_mfma_f32_16x16x32_bf16 v[44:47], v[132:135], v[182:185], v[44:47]
	v_mfma_f32_16x16x32_bf16 v[36:39], v[140:143], v[182:185], v[36:39]
	v_mfma_f32_16x16x32_bf16 v[28:31], v[132:135], v[198:201], v[28:31]
	v_mfma_f32_16x16x32_bf16 v[20:23], v[140:143], v[198:201], v[20:23]
	v_mfma_f32_16x16x32_bf16 v[12:15], v[132:135], v[206:209], v[12:15]
	v_mfma_f32_16x16x32_bf16 v[4:7], v[140:143], v[206:209], v[4:7]
	v_mfma_f32_16x16x32_bf16 v[56:59], v[144:147], v[160:163], v[56:59]
	v_mfma_f32_16x16x32_bf16 v[48:51], v[152:155], v[160:163], v[48:51]
	v_mfma_f32_16x16x32_bf16 v[40:43], v[144:147], v[178:181], v[40:43]
	v_mfma_f32_16x16x32_bf16 v[32:35], v[152:155], v[178:181], v[32:35]
	v_mfma_f32_16x16x32_bf16 v[24:27], v[144:147], v[186:189], v[24:27]
	v_mfma_f32_16x16x32_bf16 v[16:19], v[152:155], v[186:189], v[16:19]
	v_mfma_f32_16x16x32_bf16 v[8:11], v[144:147], v[202:205], v[8:11]
	v_mfma_f32_16x16x32_bf16 v[0:3], v[152:155], v[202:205], v[0:3]
	v_mfma_f32_16x16x32_bf16 v[56:59], v[148:151], v[174:177], v[56:59]
	v_mfma_f32_16x16x32_bf16 v[48:51], v[156:159], v[174:177], v[48:51]
	v_mfma_f32_16x16x32_bf16 v[40:43], v[148:151], v[182:185], v[40:43]
	v_mfma_f32_16x16x32_bf16 v[32:35], v[156:159], v[182:185], v[32:35]
	v_mfma_f32_16x16x32_bf16 v[24:27], v[148:151], v[198:201], v[24:27]
	v_mfma_f32_16x16x32_bf16 v[16:19], v[156:159], v[198:201], v[16:19]
	v_mfma_f32_16x16x32_bf16 v[8:11], v[148:151], v[206:209], v[8:11]
	v_mfma_f32_16x16x32_bf16 v[0:3], v[156:159], v[206:209], v[0:3]
	s_barrier
	s_add_i32 s59, 0, 0x18000
	s_add_i32 s60, 0, 0x1c000
	v_add_u32_e32 v140, s59, v193
	v_add_u32_e32 v156, s60, v193
	ds_read_b128 v[100:103], v140
	ds_read_b128 v[132:135], v140 offset:1024
	ds_read_b128 v[136:139], v140 offset:2048
	ds_read_b128 v[140:143], v140 offset:3072
	ds_read_b128 v[144:147], v156
	ds_read_b128 v[148:151], v156 offset:1024
	ds_read_b128 v[152:155], v156 offset:2048
	ds_read_b128 v[156:159], v156 offset:3072
	s_add_i32 s51, s51, 0x80000
	s_add_u32 s52, s3, s51
	s_addc_u32 s53, s30, 0
	s_mov_b32 m0, s26
	v_lshl_add_u64 v[190:191], s[52:53], 0, v[164:165]
	ds_read_b128 v[160:163], v197 offset:32768
	ds_read_b128 v[174:177], v197 offset:33792
	ds_read_b128 v[178:181], v197 offset:34816
	ds_read_b128 v[182:185], v197 offset:35840
	ds_read_b128 v[186:189], v197 offset:36864
	ds_read_b128 v[198:201], v197 offset:37888
	ds_read_b128 v[202:205], v197 offset:38912
	ds_read_b128 v[206:209], v197 offset:39936
	global_load_lds_dwordx4 v[190:191], off
	v_lshl_add_u64 v[190:191], s[52:53], 0, v[166:167]
	s_mov_b32 m0, s27
	s_nop 0
	global_load_lds_dwordx4 v[190:191], off
	s_waitcnt vmcnt(8)
	s_waitcnt lgkmcnt(0)
	s_barrier
	s_waitcnt lgkmcnt(0)
	v_mfma_f32_16x16x32_bf16 v[128:131], v[100:103], v[160:163], v[128:131]
	v_mfma_f32_16x16x32_bf16 v[124:127], v[136:139], v[160:163], v[124:127]
	v_mfma_f32_16x16x32_bf16 v[116:119], v[100:103], v[178:181], v[116:119]
	v_mfma_f32_16x16x32_bf16 v[108:111], v[136:139], v[178:181], v[108:111]
	v_mfma_f32_16x16x32_bf16 v[92:95], v[100:103], v[186:189], v[92:95]
	v_mfma_f32_16x16x32_bf16 v[84:87], v[136:139], v[186:189], v[84:87]
	v_mfma_f32_16x16x32_bf16 v[76:79], v[100:103], v[202:205], v[76:79]
	v_mfma_f32_16x16x32_bf16 v[68:71], v[136:139], v[202:205], v[68:71]
	v_mfma_f32_16x16x32_bf16 v[128:131], v[132:135], v[174:177], v[128:131]
	v_mfma_f32_16x16x32_bf16 v[124:127], v[140:143], v[174:177], v[124:127]
	v_mfma_f32_16x16x32_bf16 v[116:119], v[132:135], v[182:185], v[116:119]
	v_mfma_f32_16x16x32_bf16 v[108:111], v[140:143], v[182:185], v[108:111]
	v_mfma_f32_16x16x32_bf16 v[92:95], v[132:135], v[198:201], v[92:95]
	v_mfma_f32_16x16x32_bf16 v[84:87], v[140:143], v[198:201], v[84:87]
	v_mfma_f32_16x16x32_bf16 v[76:79], v[132:135], v[206:209], v[76:79]
	v_mfma_f32_16x16x32_bf16 v[68:71], v[140:143], v[206:209], v[68:71]
	v_mfma_f32_16x16x32_bf16 v[96:99], v[144:147], v[160:163], v[96:99]
	v_mfma_f32_16x16x32_bf16 v[120:123], v[152:155], v[160:163], v[120:123]
	v_mfma_f32_16x16x32_bf16 v[112:115], v[144:147], v[178:181], v[112:115]
	v_mfma_f32_16x16x32_bf16 v[104:107], v[152:155], v[178:181], v[104:107]
	v_mfma_f32_16x16x32_bf16 v[88:91], v[144:147], v[186:189], v[88:91]
	v_mfma_f32_16x16x32_bf16 v[80:83], v[152:155], v[186:189], v[80:83]
	v_mfma_f32_16x16x32_bf16 v[72:75], v[144:147], v[202:205], v[72:75]
	v_mfma_f32_16x16x32_bf16 v[64:67], v[152:155], v[202:205], v[64:67]
	v_mfma_f32_16x16x32_bf16 v[96:99], v[148:151], v[174:177], v[96:99]
	v_mfma_f32_16x16x32_bf16 v[120:123], v[156:159], v[174:177], v[120:123]
	v_mfma_f32_16x16x32_bf16 v[112:115], v[148:151], v[182:185], v[112:115]
	v_mfma_f32_16x16x32_bf16 v[104:107], v[156:159], v[182:185], v[104:107]
	v_mfma_f32_16x16x32_bf16 v[88:91], v[148:151], v[198:201], v[88:91]
	v_mfma_f32_16x16x32_bf16 v[80:83], v[156:159], v[198:201], v[80:83]
	v_mfma_f32_16x16x32_bf16 v[72:75], v[148:151], v[206:209], v[72:75]
	v_mfma_f32_16x16x32_bf16 v[64:67], v[156:159], v[206:209], v[64:67]
	s_barrier
; #define PG_BAR __builtin_amdgcn_s_barrier()
; template <class Epi, class Sched, class Hook = NoHook>
; __device__ __forceinline__ void gemm_phase_w(LAS unsigned char* lds, const Sched& S, const Epi& E, int wave_id, const Hook& HK = Hook()) {
;     ...
;         if constexpr (!SEG2) {
;             for (int tt = 0; tt < nt; tt += 2) {
;                 if constexpr (GATHER) { if (tt == nt - 2) {
;                     if (has_next) { gnxt_00 = S.grow_l(nxt, lds, nbuf, R0) + (unsigned)(C0 * 2); gnxt_01 = S.grow_l(nxt, lds, nbuf, R1) + (unsigned)(C1 * 2); gnxt_10 = S.grow_l(nxt, lds, nbuf, 128 + R0) + (unsigned)(C0 * 2); gnxt_11 = S.grow_l(nxt, lds, nbuf, 128 + R1) + (unsigned)(C1 * 2); }
;                     else { gnxt_00 = gcur_00; gnxt_01 = gcur_01; gnxt_10 = gcur_10; gnxt_11 = gcur_11; } } }
;                 PG_TRIP(tt, false, false, false);
;             }
;         } else {
;             for (int tt = 0; tt < nt - 4; tt += 2) PG_TRIP(tt, false, false, false);
;             PG_TRIP(nt - 4, false, true, false);
;             PG_TRIP(nt - 2, true, false, true);
;         }
;     ...
;         if (wr == 0) PG_BAR;
	s_or_b32 s52, s50, 1
	s_lshl_b32 s53, s52, 7
	s_add_i32 s49, s53, s49
	s_ashr_i32 s51, s49, 31
	s_add_u32 s50, s4, s49
	s_addc_u32 s51, s5, s51
	s_add_i32 s49, s59, s31
	v_lshl_add_u64 v[190:191], s[50:51], 0, v[168:169]
	s_mov_b32 m0, s49
	s_add_i32 s53, s53, s58
	ds_read_b128 v[160:163], v197 offset:49152
	ds_read_b128 v[174:177], v197 offset:50176
	ds_read_b128 v[178:181], v197 offset:51200
	ds_read_b128 v[182:185], v197 offset:52224
	ds_read_b128 v[186:189], v197 offset:53248
	ds_read_b128 v[198:201], v197 offset:54272
	ds_read_b128 v[202:205], v197 offset:55296
	ds_read_b128 v[206:209], v197 offset:56320
	global_load_lds_dwordx4 v[190:191], off
	s_add_i32 m0, s49, 0x2000
	s_ashr_i32 s49, s53, 31
	v_lshl_add_u64 v[190:191], s[50:51], 0, v[170:171]
	s_add_u32 s50, s4, s53
	s_addc_u32 s51, s5, s49
	s_add_i32 s49, s60, s31
	global_load_lds_dwordx4 v[190:191], off
	v_lshl_add_u64 v[190:191], s[50:51], 0, v[168:169]
	s_mov_b32 m0, s49
	s_nop 0
	global_load_lds_dwordx4 v[190:191], off
	s_add_i32 m0, s49, 0x2000
	s_lshl_b32 s49, s52, 12
	s_add_i32 s49, s49, s48
	s_add_u32 s48, s3, s49
	v_lshl_add_u64 v[190:191], s[50:51], 0, v[170:171]
	s_addc_u32 s49, s30, 0
	global_load_lds_dwordx4 v[190:191], off
	v_lshl_add_u64 v[190:191], s[48:49], 0, v[164:165]
	s_mov_b32 m0, s29
	s_nop 0
	global_load_lds_dwordx4 v[190:191], off
	v_lshl_add_u64 v[190:191], s[48:49], 0, v[166:167]
	s_mov_b32 m0, s38
	s_nop 0
	global_load_lds_dwordx4 v[190:191], off
	s_waitcnt vmcnt(8)
	s_waitcnt lgkmcnt(0)
	s_barrier
	s_waitcnt lgkmcnt(0)
	v_mfma_f32_16x16x32_bf16 v[60:63], v[100:103], v[160:163], v[60:63]
	v_mfma_f32_16x16x32_bf16 v[52:55], v[136:139], v[160:163], v[52:55]
	v_mfma_f32_16x16x32_bf16 v[44:47], v[100:103], v[178:181], v[44:47]
	v_mfma_f32_16x16x32_bf16 v[36:39], v[136:139], v[178:181], v[36:39]
	v_mfma_f32_16x16x32_bf16 v[28:31], v[100:103], v[186:189], v[28:31]
	v_mfma_f32_16x16x32_bf16 v[20:23], v[136:139], v[186:189], v[20:23]
	v_mfma_f32_16x16x32_bf16 v[12:15], v[100:103], v[202:205], v[12:15]
	v_mfma_f32_16x16x32_bf16 v[4:7], v[136:139], v[202:205], v[4:7]
	v_mfma_f32_16x16x32_bf16 v[60:63], v[132:135], v[174:177], v[60:63]
	v_mfma_f32_16x16x32_bf16 v[52:55], v[140:143], v[174:177], v[52:55]
	v_mfma_f32_16x16x32_bf16 v[44:47], v[132:135], v[182:185], v[44:47]
	v_mfma_f32_16x16x32_bf16 v[36:39], v[140:143], v[182:185], v[36:39]
	v_mfma_f32_16x16x32_bf16 v[28:31], v[132:135], v[198:201], v[28:31]
	v_mfma_f32_16x16x32_bf16 v[20:23], v[140:143], v[198:201], v[20:23]
	v_mfma_f32_16x16x32_bf16 v[12:15], v[132:135], v[206:209], v[12:15]
	v_mfma_f32_16x16x32_bf16 v[4:7], v[140:143], v[206:209], v[4:7]
	v_mfma_f32_16x16x32_bf16 v[56:59], v[144:147], v[160:163], v[56:59]
	v_mfma_f32_16x16x32_bf16 v[48:51], v[152:155], v[160:163], v[48:51]
	v_mfma_f32_16x16x32_bf16 v[40:43], v[144:147], v[178:181], v[40:43]
	v_mfma_f32_16x16x32_bf16 v[32:35], v[152:155], v[178:181], v[32:35]
	v_mfma_f32_16x16x32_bf16 v[24:27], v[144:147], v[186:189], v[24:27]
	v_mfma_f32_16x16x32_bf16 v[16:19], v[152:155], v[186:189], v[16:19]
	v_mfma_f32_16x16x32_bf16 v[8:11], v[144:147], v[202:205], v[8:11]
	v_mfma_f32_16x16x32_bf16 v[0:3], v[152:155], v[202:205], v[0:3]
	v_mfma_f32_16x16x32_bf16 v[56:59], v[148:151], v[174:177], v[56:59]
	v_mfma_f32_16x16x32_bf16 v[48:51], v[156:159], v[174:177], v[48:51]
	v_mfma_f32_16x16x32_bf16 v[40:43], v[148:151], v[182:185], v[40:43]
	v_mfma_f32_16x16x32_bf16 v[32:35], v[156:159], v[182:185], v[32:35]
	v_mfma_f32_16x16x32_bf16 v[24:27], v[148:151], v[198:201], v[24:27]
	v_mfma_f32_16x16x32_bf16 v[16:19], v[156:159], v[198:201], v[16:19]
	v_mfma_f32_16x16x32_bf16 v[8:11], v[148:151], v[206:209], v[8:11]
	v_mfma_f32_16x16x32_bf16 v[0:3], v[156:159], v[206:209], v[0:3]
	s_addk_i32 s20, 0x2000
	s_cmp_gt_u32 s21, 29
	s_mov_b32 s21, s45
	s_barrier
	s_cbranch_scc0 .LBB0_1983
	s_and_b64 vcc, exec, s[16:17]
	s_cbranch_vccz .LBB0_1986
	s_barrier

.LBB0_2156:
	v_add_u32_e32 v147, s69, v166
	ds_read_b128 v[186:189], v147
	ds_read_b128 v[190:193], v147 offset:1024
	ds_read_b128 v[194:197], v147 offset:2048
	ds_read_b128 v[198:201], v147 offset:3072
	v_add_u32_e32 v147, s70, v166
	ds_read_b128 v[202:205], v147
	ds_read_b128 v[206:209], v147 offset:1024
	ds_read_b128 v[210:213], v147 offset:2048
	ds_read_b128 v[214:217], v147 offset:3072
	v_lshl_add_u64 v[250:251], s[38:39], 0, v[130:131]
	s_add_i32 m0, s58, 0xc000
	ds_read_b128 v[218:221], v182
	ds_read_b128 v[222:225], v182 offset:1024
	ds_read_b128 v[226:229], v182 offset:2048
	ds_read_b128 v[230:233], v182 offset:3072
	ds_read_b128 v[234:237], v182 offset:4096
	ds_read_b128 v[238:241], v182 offset:5120
	ds_read_b128 v[242:245], v182 offset:6144
	ds_read_b128 v[246:249], v182 offset:7168
	global_load_lds_dwordx4 v[250:251], off
	v_lshl_add_u64 v[250:251], s[38:39], 0, v[132:133]
	s_add_i32 m0, s58, 0xe000
	s_nop 0
	global_load_lds_dwordx4 v[250:251], off
	s_waitcnt vmcnt(8)
	s_waitcnt lgkmcnt(0)
	s_barrier
	s_waitcnt lgkmcnt(0)
	v_mfma_f32_16x16x32_bf16 v[124:127], v[186:189], v[218:221], v[124:127]
	v_mfma_f32_16x16x32_bf16 v[120:123], v[194:197], v[218:221], v[120:123]
	v_mfma_f32_16x16x32_bf16 v[108:111], v[186:189], v[226:229], v[108:111]
	v_mfma_f32_16x16x32_bf16 v[104:107], v[194:197], v[226:229], v[104:107]
	v_mfma_f32_16x16x32_bf16 v[92:95], v[186:189], v[234:237], v[92:95]
	v_mfma_f32_16x16x32_bf16 v[88:91], v[194:197], v[234:237], v[88:91]
	v_mfma_f32_16x16x32_bf16 v[76:79], v[186:189], v[242:245], v[76:79]
	v_mfma_f32_16x16x32_bf16 v[72:75], v[194:197], v[242:245], v[72:75]
	v_mfma_f32_16x16x32_bf16 v[124:127], v[190:193], v[222:225], v[124:127]
	v_mfma_f32_16x16x32_bf16 v[120:123], v[198:201], v[222:225], v[120:123]
	v_mfma_f32_16x16x32_bf16 v[108:111], v[190:193], v[230:233], v[108:111]
	v_mfma_f32_16x16x32_bf16 v[104:107], v[198:201], v[230:233], v[104:107]
	v_mfma_f32_16x16x32_bf16 v[92:95], v[190:193], v[238:241], v[92:95]
	v_mfma_f32_16x16x32_bf16 v[88:91], v[198:201], v[238:241], v[88:91]
	v_mfma_f32_16x16x32_bf16 v[76:79], v[190:193], v[246:249], v[76:79]
	v_mfma_f32_16x16x32_bf16 v[72:75], v[198:201], v[246:249], v[72:75]
	v_mfma_f32_16x16x32_bf16 v[116:119], v[202:205], v[218:221], v[116:119]
	v_mfma_f32_16x16x32_bf16 v[112:115], v[210:213], v[218:221], v[112:115]
	v_mfma_f32_16x16x32_bf16 v[100:103], v[202:205], v[226:229], v[100:103]
	v_mfma_f32_16x16x32_bf16 v[96:99], v[210:213], v[226:229], v[96:99]
	v_mfma_f32_16x16x32_bf16 v[84:87], v[202:205], v[234:237], v[84:87]
	v_mfma_f32_16x16x32_bf16 v[80:83], v[210:213], v[234:237], v[80:83]
	v_mfma_f32_16x16x32_bf16 v[68:71], v[202:205], v[242:245], v[68:71]
	v_mfma_f32_16x16x32_bf16 v[64:67], v[210:213], v[242:245], v[64:67]
	v_mfma_f32_16x16x32_bf16 v[116:119], v[206:209], v[222:225], v[116:119]
	v_mfma_f32_16x16x32_bf16 v[112:115], v[214:217], v[222:225], v[112:115]
	v_mfma_f32_16x16x32_bf16 v[100:103], v[206:209], v[230:233], v[100:103]
	v_mfma_f32_16x16x32_bf16 v[96:99], v[214:217], v[230:233], v[96:99]
	v_mfma_f32_16x16x32_bf16 v[84:87], v[206:209], v[238:241], v[84:87]
	v_mfma_f32_16x16x32_bf16 v[80:83], v[214:217], v[238:241], v[80:83]
	v_mfma_f32_16x16x32_bf16 v[68:71], v[206:209], v[246:249], v[68:71]
	v_mfma_f32_16x16x32_bf16 v[64:67], v[214:217], v[246:249], v[64:67]
	s_barrier
	s_and_b64 s[40:41], s[40:41], exec
	s_cselect_b32 s22, 0, s80
	s_add_i32 s84, s81, s22
	s_ashr_i32 s41, s84, 31
	s_add_u32 s40, s16, s84
	s_addc_u32 s41, s17, s41
	s_add_i32 s85, s69, s44
	v_lshl_add_u64 v[250:251], s[40:41], 0, v[136:137]
	s_mov_b32 m0, s85
	s_add_i32 s84, s84, 0x80000
	ds_read_b128 v[218:221], v182 offset:16384
	ds_read_b128 v[222:225], v182 offset:17408
	ds_read_b128 v[226:229], v182 offset:18432
	ds_read_b128 v[230:233], v182 offset:19456
	ds_read_b128 v[234:237], v182 offset:20480
	ds_read_b128 v[238:241], v182 offset:21504
	ds_read_b128 v[242:245], v182 offset:22528
	ds_read_b128 v[246:249], v182 offset:23552
	global_load_lds_dwordx4 v[250:251], off
	v_lshl_add_u64 v[250:251], s[40:41], 0, v[138:139]
	s_add_i32 m0, s85, 0x2000
	s_ashr_i32 s41, s84, 31
	s_add_u32 s40, s16, s84
	s_addc_u32 s41, s17, s41
	s_add_i32 s84, s70, s44
	global_load_lds_dwordx4 v[250:251], off
	v_lshl_add_u64 v[250:251], s[40:41], 0, v[136:137]
	s_mov_b32 m0, s84
	v_mov_b32_e32 v147, v141
	global_load_lds_dwordx4 v[250:251], off
	s_add_i32 m0, s84, 0x2000
	v_lshl_add_u64 v[250:251], s[40:41], 0, v[138:139]
	s_add_u32 s40, s14, s22
	global_load_lds_dwordx4 v[250:251], off
	s_addc_u32 s41, s15, 0
	s_mov_b32 m0, s58
	s_nop 0
	global_load_lds_dwordx4 v140, s[40:41]
	s_mov_b32 m0, s59
	s_nop 0
	global_load_lds_dwordx4 v146, s[40:41]
	s_waitcnt vmcnt(8)
	s_waitcnt lgkmcnt(0)
	s_barrier
	s_waitcnt lgkmcnt(0)
	v_mfma_f32_16x16x32_bf16 v[60:63], v[186:189], v[218:221], v[60:63]
	v_mfma_f32_16x16x32_bf16 v[56:59], v[194:197], v[218:221], v[56:59]
	v_mfma_f32_16x16x32_bf16 v[44:47], v[186:189], v[226:229], v[44:47]
	v_mfma_f32_16x16x32_bf16 v[40:43], v[194:197], v[226:229], v[40:43]
	v_mfma_f32_16x16x32_bf16 v[28:31], v[186:189], v[234:237], v[28:31]
	v_mfma_f32_16x16x32_bf16 v[24:27], v[194:197], v[234:237], v[24:27]
	v_mfma_f32_16x16x32_bf16 v[12:15], v[186:189], v[242:245], v[12:15]
	v_mfma_f32_16x16x32_bf16 v[8:11], v[194:197], v[242:245], v[8:11]
	v_mfma_f32_16x16x32_bf16 v[60:63], v[190:193], v[222:225], v[60:63]
	v_mfma_f32_16x16x32_bf16 v[56:59], v[198:201], v[222:225], v[56:59]
	v_mfma_f32_16x16x32_bf16 v[44:47], v[190:193], v[230:233], v[44:47]
	v_mfma_f32_16x16x32_bf16 v[40:43], v[198:201], v[230:233], v[40:43]
	v_mfma_f32_16x16x32_bf16 v[28:31], v[190:193], v[238:241], v[28:31]
	v_mfma_f32_16x16x32_bf16 v[24:27], v[198:201], v[238:241], v[24:27]
	v_mfma_f32_16x16x32_bf16 v[12:15], v[190:193], v[246:249], v[12:15]
	v_mfma_f32_16x16x32_bf16 v[8:11], v[198:201], v[246:249], v[8:11]
	v_mfma_f32_16x16x32_bf16 v[52:55], v[202:205], v[218:221], v[52:55]
	v_mfma_f32_16x16x32_bf16 v[48:51], v[210:213], v[218:221], v[48:51]
	v_mfma_f32_16x16x32_bf16 v[36:39], v[202:205], v[226:229], v[36:39]
	v_mfma_f32_16x16x32_bf16 v[32:35], v[210:213], v[226:229], v[32:35]
	v_mfma_f32_16x16x32_bf16 v[20:23], v[202:205], v[234:237], v[20:23]
	v_mfma_f32_16x16x32_bf16 v[16:19], v[210:213], v[234:237], v[16:19]
	v_mfma_f32_16x16x32_bf16 v[4:7], v[202:205], v[242:245], v[4:7]
	v_mfma_f32_16x16x32_bf16 v[0:3], v[210:213], v[242:245], v[0:3]
	v_mfma_f32_16x16x32_bf16 v[52:55], v[206:209], v[222:225], v[52:55]
	v_mfma_f32_16x16x32_bf16 v[48:51], v[214:217], v[222:225], v[48:51]
	v_mfma_f32_16x16x32_bf16 v[36:39], v[206:209], v[230:233], v[36:39]
	v_mfma_f32_16x16x32_bf16 v[32:35], v[214:217], v[230:233], v[32:35]
	v_mfma_f32_16x16x32_bf16 v[20:23], v[206:209], v[238:241], v[20:23]
	v_mfma_f32_16x16x32_bf16 v[16:19], v[214:217], v[238:241], v[16:19]
	v_mfma_f32_16x16x32_bf16 v[4:7], v[206:209], v[246:249], v[4:7]
	v_mfma_f32_16x16x32_bf16 v[0:3], v[214:217], v[246:249], v[0:3]
	s_barrier
	s_add_i32 s84, 0, 0x18000
	v_add_u32_e32 v185, s84, v166
	s_add_i32 s85, 0, 0x1c000
	ds_read_b128 v[186:189], v185
	ds_read_b128 v[190:193], v185 offset:1024
	ds_read_b128 v[194:197], v185 offset:2048
	ds_read_b128 v[198:201], v185 offset:3072
	v_add_u32_e32 v185, s85, v166
	ds_read_b128 v[202:205], v185
	ds_read_b128 v[206:209], v185 offset:1024
	ds_read_b128 v[210:213], v185 offset:2048
	ds_read_b128 v[214:217], v185 offset:3072
	s_mov_b32 m0, s60
	v_lshl_add_u64 v[148:149], s[40:41], 0, v[148:149]
	ds_read_b128 v[218:221], v182 offset:32768
	ds_read_b128 v[222:225], v182 offset:33792
	ds_read_b128 v[226:229], v182 offset:34816
	ds_read_b128 v[230:233], v182 offset:35840
	ds_read_b128 v[234:237], v182 offset:36864
	ds_read_b128 v[238:241], v182 offset:37888
	ds_read_b128 v[242:245], v182 offset:38912
	ds_read_b128 v[246:249], v182 offset:39936
	global_load_lds_dwordx4 v[148:149], off
	v_lshl_add_u64 v[148:149], s[40:41], 0, v[150:151]
	s_mov_b32 m0, s61
	s_nop 0
	global_load_lds_dwordx4 v[148:149], off
	s_waitcnt vmcnt(8)
	s_waitcnt lgkmcnt(0)
	s_barrier
	s_waitcnt lgkmcnt(0)
	v_mfma_f32_16x16x32_bf16 v[124:127], v[186:189], v[218:221], v[124:127]
	v_mfma_f32_16x16x32_bf16 v[120:123], v[194:197], v[218:221], v[120:123]
	v_mfma_f32_16x16x32_bf16 v[108:111], v[186:189], v[226:229], v[108:111]
	v_mfma_f32_16x16x32_bf16 v[104:107], v[194:197], v[226:229], v[104:107]
	v_mfma_f32_16x16x32_bf16 v[92:95], v[186:189], v[234:237], v[92:95]
	v_mfma_f32_16x16x32_bf16 v[88:91], v[194:197], v[234:237], v[88:91]
	v_mfma_f32_16x16x32_bf16 v[76:79], v[186:189], v[242:245], v[76:79]
	v_mfma_f32_16x16x32_bf16 v[72:75], v[194:197], v[242:245], v[72:75]
	v_mfma_f32_16x16x32_bf16 v[124:127], v[190:193], v[222:225], v[124:127]
	v_mfma_f32_16x16x32_bf16 v[120:123], v[198:201], v[222:225], v[120:123]
	v_mfma_f32_16x16x32_bf16 v[108:111], v[190:193], v[230:233], v[108:111]
	v_mfma_f32_16x16x32_bf16 v[104:107], v[198:201], v[230:233], v[104:107]
	v_mfma_f32_16x16x32_bf16 v[92:95], v[190:193], v[238:241], v[92:95]
	v_mfma_f32_16x16x32_bf16 v[88:91], v[198:201], v[238:241], v[88:91]
	v_mfma_f32_16x16x32_bf16 v[76:79], v[190:193], v[246:249], v[76:79]
	v_mfma_f32_16x16x32_bf16 v[72:75], v[198:201], v[246:249], v[72:75]
	v_mfma_f32_16x16x32_bf16 v[116:119], v[202:205], v[218:221], v[116:119]
	v_mfma_f32_16x16x32_bf16 v[112:115], v[210:213], v[218:221], v[112:115]
	v_mfma_f32_16x16x32_bf16 v[100:103], v[202:205], v[226:229], v[100:103]
	v_mfma_f32_16x16x32_bf16 v[96:99], v[210:213], v[226:229], v[96:99]
	v_mfma_f32_16x16x32_bf16 v[84:87], v[202:205], v[234:237], v[84:87]
	v_mfma_f32_16x16x32_bf16 v[80:83], v[210:213], v[234:237], v[80:83]
	v_mfma_f32_16x16x32_bf16 v[68:71], v[202:205], v[242:245], v[68:71]
	v_mfma_f32_16x16x32_bf16 v[64:67], v[210:213], v[242:245], v[64:67]
	v_mfma_f32_16x16x32_bf16 v[116:119], v[206:209], v[222:225], v[116:119]
	v_mfma_f32_16x16x32_bf16 v[112:115], v[214:217], v[222:225], v[112:115]
	v_mfma_f32_16x16x32_bf16 v[100:103], v[206:209], v[230:233], v[100:103]
	v_mfma_f32_16x16x32_bf16 v[96:99], v[214:217], v[230:233], v[96:99]
	v_mfma_f32_16x16x32_bf16 v[84:87], v[206:209], v[238:241], v[84:87]
	v_mfma_f32_16x16x32_bf16 v[80:83], v[214:217], v[238:241], v[80:83]
	v_mfma_f32_16x16x32_bf16 v[68:71], v[206:209], v[246:249], v[68:71]
	v_mfma_f32_16x16x32_bf16 v[64:67], v[214:217], v[246:249], v[64:67]
	s_barrier
; template <class Epi, class Sched, class Hook = NoHook>
; __device__ __forceinline__ void gemm_phase_w(LAS unsigned char* lds, const Sched& S, const Epi& E, int wave_id, const Hook& HK = Hook()) {
;     ...
;         if constexpr (!SEG2) {
;             for (int tt = 0; tt < nt; tt += 2) {
;                 if constexpr (GATHER) { if (tt == nt - 2) {
;                     if (has_next) { gnxt_00 = S.grow_l(nxt, lds, nbuf, R0) + (unsigned)(C0 * 2); gnxt_01 = S.grow_l(nxt, lds, nbuf, R1) + (unsigned)(C1 * 2); gnxt_10 = S.grow_l(nxt, lds, nbuf, 128 + R0) + (unsigned)(C0 * 2); gnxt_11 = S.grow_l(nxt, lds, nbuf, 128 + R1) + (unsigned)(C1 * 2); }
;                     else { gnxt_00 = gcur_00; gnxt_01 = gcur_01; gnxt_10 = gcur_10; gnxt_11 = gcur_11; } } }
;                 PG_TRIP(tt, false, false, false);
;             }
	s_bitset1_b32 s22, 7
	s_add_i32 s81, s81, s22
	s_ashr_i32 s41, s81, 31
	s_add_u32 s40, s16, s81
	s_addc_u32 s41, s17, s41
	s_add_i32 s84, s84, s44
	v_lshl_add_u64 v[246:247], s[40:41], 0, v[136:137]
	s_mov_b32 m0, s84
	s_add_i32 s81, s81, 0x80000
	ds_read_b128 v[148:151], v182 offset:49152
	ds_read_b128 v[218:221], v182 offset:50176
	ds_read_b128 v[222:225], v182 offset:51200
	ds_read_b128 v[226:229], v182 offset:52224
	ds_read_b128 v[230:233], v182 offset:53248
	ds_read_b128 v[234:237], v182 offset:54272
	ds_read_b128 v[238:241], v182 offset:55296
	ds_read_b128 v[242:245], v182 offset:56320
	global_load_lds_dwordx4 v[246:247], off
	v_lshl_add_u64 v[246:247], s[40:41], 0, v[138:139]
	s_add_i32 m0, s84, 0x2000
	s_ashr_i32 s41, s81, 31
	s_add_u32 s40, s16, s81
	s_addc_u32 s41, s17, s41
	s_add_i32 s81, s85, s44
	global_load_lds_dwordx4 v[246:247], off
	v_lshl_add_u64 v[246:247], s[40:41], 0, v[136:137]
	s_mov_b32 m0, s81
	v_lshl_add_u64 v[146:147], s[14:15], 0, v[146:147]
	global_load_lds_dwordx4 v[246:247], off
	v_lshl_add_u64 v[246:247], s[40:41], 0, v[138:139]
	s_add_i32 m0, s81, 0x2000
	v_lshl_add_u64 v[146:147], v[146:147], 0, s[22:23]
	global_load_lds_dwordx4 v[246:247], off
	v_lshl_add_u64 v[246:247], s[14:15], 0, v[140:141]
	v_lshl_add_u64 v[246:247], v[246:247], 0, s[22:23]
	s_mov_b32 m0, s62
	s_nop 0
	global_load_lds_dwordx4 v[246:247], off
	s_mov_b32 m0, s63
	s_nop 0
	global_load_lds_dwordx4 v[146:147], off
	s_waitcnt vmcnt(8)
	s_waitcnt lgkmcnt(0)
	s_barrier
	s_waitcnt lgkmcnt(0)
	v_mfma_f32_16x16x32_bf16 v[60:63], v[186:189], v[148:151], v[60:63]
	v_mfma_f32_16x16x32_bf16 v[56:59], v[194:197], v[148:151], v[56:59]
	v_mfma_f32_16x16x32_bf16 v[44:47], v[186:189], v[222:225], v[44:47]
	v_mfma_f32_16x16x32_bf16 v[40:43], v[194:197], v[222:225], v[40:43]
	v_mfma_f32_16x16x32_bf16 v[28:31], v[186:189], v[230:233], v[28:31]
	v_mfma_f32_16x16x32_bf16 v[24:27], v[194:197], v[230:233], v[24:27]
	v_mfma_f32_16x16x32_bf16 v[12:15], v[186:189], v[238:241], v[12:15]
	v_mfma_f32_16x16x32_bf16 v[8:11], v[194:197], v[238:241], v[8:11]
	v_mfma_f32_16x16x32_bf16 v[60:63], v[190:193], v[218:221], v[60:63]
	v_mfma_f32_16x16x32_bf16 v[56:59], v[198:201], v[218:221], v[56:59]
	v_mfma_f32_16x16x32_bf16 v[44:47], v[190:193], v[226:229], v[44:47]
	v_mfma_f32_16x16x32_bf16 v[40:43], v[198:201], v[226:229], v[40:43]
	v_mfma_f32_16x16x32_bf16 v[28:31], v[190:193], v[234:237], v[28:31]
	v_mfma_f32_16x16x32_bf16 v[24:27], v[198:201], v[234:237], v[24:27]
	v_mfma_f32_16x16x32_bf16 v[12:15], v[190:193], v[242:245], v[12:15]
	v_mfma_f32_16x16x32_bf16 v[8:11], v[198:201], v[242:245], v[8:11]
	v_mfma_f32_16x16x32_bf16 v[52:55], v[202:205], v[148:151], v[52:55]
	v_mfma_f32_16x16x32_bf16 v[48:51], v[210:213], v[148:151], v[48:51]
	v_mfma_f32_16x16x32_bf16 v[36:39], v[202:205], v[222:225], v[36:39]
	v_mfma_f32_16x16x32_bf16 v[32:35], v[210:213], v[222:225], v[32:35]
	v_mfma_f32_16x16x32_bf16 v[20:23], v[202:205], v[230:233], v[20:23]
	v_mfma_f32_16x16x32_bf16 v[16:19], v[210:213], v[230:233], v[16:19]
	v_mfma_f32_16x16x32_bf16 v[4:7], v[202:205], v[238:241], v[4:7]
	v_mfma_f32_16x16x32_bf16 v[0:3], v[210:213], v[238:241], v[0:3]
	v_mfma_f32_16x16x32_bf16 v[52:55], v[206:209], v[218:221], v[52:55]
	v_mfma_f32_16x16x32_bf16 v[48:51], v[214:217], v[218:221], v[48:51]
	v_mfma_f32_16x16x32_bf16 v[36:39], v[206:209], v[226:229], v[36:39]
	v_mfma_f32_16x16x32_bf16 v[32:35], v[214:217], v[226:229], v[32:35]
	v_mfma_f32_16x16x32_bf16 v[20:23], v[206:209], v[234:237], v[20:23]
	v_mfma_f32_16x16x32_bf16 v[16:19], v[214:217], v[234:237], v[16:19]
	v_mfma_f32_16x16x32_bf16 v[4:7], v[206:209], v[242:245], v[4:7]
	v_mfma_f32_16x16x32_bf16 v[0:3], v[214:217], v[242:245], v[0:3]
	s_add_i32 s79, s79, 2
	s_addk_i32 s80, 0x100
	s_add_u32 s38, s38, 0x100
	s_addc_u32 s39, s39, 0
	s_cmp_gt_u32 s79, 29
	s_barrier
	s_cbranch_scc1 .LBB0_2160

.LBB0_2410:
	v_add_u32_e32 v147, s49, v163
	ds_read_b128 v[182:185], v147
	ds_read_b128 v[186:189], v147 offset:1024
	ds_read_b128 v[190:193], v147 offset:2048
	ds_read_b128 v[194:197], v147 offset:3072
	v_add_u32_e32 v147, s50, v163
	ds_read_b128 v[198:201], v147
	ds_read_b128 v[202:205], v147 offset:1024
	ds_read_b128 v[206:209], v147 offset:2048
	ds_read_b128 v[210:213], v147 offset:3072
	v_lshl_add_u64 v[246:247], s[38:39], 0, v[130:131]
	s_add_i32 m0, s57, 0xc000
	ds_read_b128 v[214:217], v179
	ds_read_b128 v[218:221], v179 offset:1024
	ds_read_b128 v[222:225], v179 offset:2048
	ds_read_b128 v[226:229], v179 offset:3072
	ds_read_b128 v[230:233], v179 offset:4096
	ds_read_b128 v[234:237], v179 offset:5120
	ds_read_b128 v[238:241], v179 offset:6144
	ds_read_b128 v[242:245], v179 offset:7168
	global_load_lds_dwordx4 v[246:247], off
	v_lshl_add_u64 v[246:247], s[38:39], 0, v[132:133]
	s_add_i32 m0, s57, 0xe000
	s_nop 0
	global_load_lds_dwordx4 v[246:247], off
	s_waitcnt vmcnt(8)
	s_waitcnt lgkmcnt(0)
	s_barrier
	s_waitcnt lgkmcnt(0)
	v_mfma_f32_16x16x32_bf16 v[124:127], v[182:185], v[214:217], v[124:127]
	v_mfma_f32_16x16x32_bf16 v[120:123], v[190:193], v[214:217], v[120:123]
	v_mfma_f32_16x16x32_bf16 v[108:111], v[182:185], v[222:225], v[108:111]
	v_mfma_f32_16x16x32_bf16 v[104:107], v[190:193], v[222:225], v[104:107]
	v_mfma_f32_16x16x32_bf16 v[92:95], v[182:185], v[230:233], v[92:95]
	v_mfma_f32_16x16x32_bf16 v[88:91], v[190:193], v[230:233], v[88:91]
	v_mfma_f32_16x16x32_bf16 v[76:79], v[182:185], v[238:241], v[76:79]
	v_mfma_f32_16x16x32_bf16 v[72:75], v[190:193], v[238:241], v[72:75]
	v_mfma_f32_16x16x32_bf16 v[124:127], v[186:189], v[218:221], v[124:127]
	v_mfma_f32_16x16x32_bf16 v[120:123], v[194:197], v[218:221], v[120:123]
	v_mfma_f32_16x16x32_bf16 v[108:111], v[186:189], v[226:229], v[108:111]
	v_mfma_f32_16x16x32_bf16 v[104:107], v[194:197], v[226:229], v[104:107]
	v_mfma_f32_16x16x32_bf16 v[92:95], v[186:189], v[234:237], v[92:95]
	v_mfma_f32_16x16x32_bf16 v[88:91], v[194:197], v[234:237], v[88:91]
	v_mfma_f32_16x16x32_bf16 v[76:79], v[186:189], v[242:245], v[76:79]
	v_mfma_f32_16x16x32_bf16 v[72:75], v[194:197], v[242:245], v[72:75]
	v_mfma_f32_16x16x32_bf16 v[116:119], v[198:201], v[214:217], v[116:119]
	v_mfma_f32_16x16x32_bf16 v[112:115], v[206:209], v[214:217], v[112:115]
	v_mfma_f32_16x16x32_bf16 v[100:103], v[198:201], v[222:225], v[100:103]
	v_mfma_f32_16x16x32_bf16 v[96:99], v[206:209], v[222:225], v[96:99]
	v_mfma_f32_16x16x32_bf16 v[84:87], v[198:201], v[230:233], v[84:87]
	v_mfma_f32_16x16x32_bf16 v[80:83], v[206:209], v[230:233], v[80:83]
	v_mfma_f32_16x16x32_bf16 v[68:71], v[198:201], v[238:241], v[68:71]
	v_mfma_f32_16x16x32_bf16 v[64:67], v[206:209], v[238:241], v[64:67]
	v_mfma_f32_16x16x32_bf16 v[116:119], v[202:205], v[218:221], v[116:119]
	v_mfma_f32_16x16x32_bf16 v[112:115], v[210:213], v[218:221], v[112:115]
	v_mfma_f32_16x16x32_bf16 v[100:103], v[202:205], v[226:229], v[100:103]
	v_mfma_f32_16x16x32_bf16 v[96:99], v[210:213], v[226:229], v[96:99]
	v_mfma_f32_16x16x32_bf16 v[84:87], v[202:205], v[234:237], v[84:87]
	v_mfma_f32_16x16x32_bf16 v[80:83], v[210:213], v[234:237], v[80:83]
	v_mfma_f32_16x16x32_bf16 v[68:71], v[202:205], v[242:245], v[68:71]
	v_mfma_f32_16x16x32_bf16 v[64:67], v[210:213], v[242:245], v[64:67]
	s_barrier
	s_and_b64 s[40:41], s[40:41], exec
	s_cselect_b32 s22, 0, s70
	s_add_i32 s72, s71, s22
	s_ashr_i32 s41, s72, 31
	s_add_u32 s40, s16, s72
	s_addc_u32 s41, s17, s41
	s_add_i32 s73, s49, s44
	v_lshl_add_u64 v[246:247], s[40:41], 0, v[136:137]
	s_mov_b32 m0, s73
	s_add_i32 s72, s72, 0x80000
	ds_read_b128 v[214:217], v179 offset:16384
	ds_read_b128 v[218:221], v179 offset:17408
	ds_read_b128 v[222:225], v179 offset:18432
	ds_read_b128 v[226:229], v179 offset:19456
	ds_read_b128 v[230:233], v179 offset:20480
	ds_read_b128 v[234:237], v179 offset:21504
	ds_read_b128 v[238:241], v179 offset:22528
	ds_read_b128 v[242:245], v179 offset:23552
	global_load_lds_dwordx4 v[246:247], off
	v_lshl_add_u64 v[246:247], s[40:41], 0, v[138:139]
	s_add_i32 m0, s73, 0x2000
	s_ashr_i32 s41, s72, 31
	s_add_u32 s40, s16, s72
	s_addc_u32 s41, s17, s41
	s_add_i32 s72, s50, s44
	global_load_lds_dwordx4 v[246:247], off
	v_lshl_add_u64 v[246:247], s[40:41], 0, v[136:137]
	s_mov_b32 m0, s72
	v_mov_b32_e32 v147, v141
	global_load_lds_dwordx4 v[246:247], off
	s_add_i32 m0, s72, 0x2000
	v_lshl_add_u64 v[246:247], s[40:41], 0, v[138:139]
	s_add_u32 s40, s14, s22
	global_load_lds_dwordx4 v[246:247], off
	s_addc_u32 s41, s15, 0
	s_mov_b32 m0, s57
	s_nop 0
	global_load_lds_dwordx4 v140, s[40:41]
	s_mov_b32 m0, s58
	s_nop 0
	global_load_lds_dwordx4 v146, s[40:41]
	s_waitcnt vmcnt(8)
	s_waitcnt lgkmcnt(0)
	s_barrier
	s_waitcnt lgkmcnt(0)
	v_mfma_f32_16x16x32_bf16 v[60:63], v[182:185], v[214:217], v[60:63]
	v_mfma_f32_16x16x32_bf16 v[56:59], v[190:193], v[214:217], v[56:59]
	v_mfma_f32_16x16x32_bf16 v[44:47], v[182:185], v[222:225], v[44:47]
	v_mfma_f32_16x16x32_bf16 v[40:43], v[190:193], v[222:225], v[40:43]
	v_mfma_f32_16x16x32_bf16 v[28:31], v[182:185], v[230:233], v[28:31]
	v_mfma_f32_16x16x32_bf16 v[24:27], v[190:193], v[230:233], v[24:27]
	v_mfma_f32_16x16x32_bf16 v[12:15], v[182:185], v[238:241], v[12:15]
	v_mfma_f32_16x16x32_bf16 v[8:11], v[190:193], v[238:241], v[8:11]
	v_mfma_f32_16x16x32_bf16 v[60:63], v[186:189], v[218:221], v[60:63]
	v_mfma_f32_16x16x32_bf16 v[56:59], v[194:197], v[218:221], v[56:59]
	v_mfma_f32_16x16x32_bf16 v[44:47], v[186:189], v[226:229], v[44:47]
	v_mfma_f32_16x16x32_bf16 v[40:43], v[194:197], v[226:229], v[40:43]
	v_mfma_f32_16x16x32_bf16 v[28:31], v[186:189], v[234:237], v[28:31]
	v_mfma_f32_16x16x32_bf16 v[24:27], v[194:197], v[234:237], v[24:27]
	v_mfma_f32_16x16x32_bf16 v[12:15], v[186:189], v[242:245], v[12:15]
	v_mfma_f32_16x16x32_bf16 v[8:11], v[194:197], v[242:245], v[8:11]
	v_mfma_f32_16x16x32_bf16 v[52:55], v[198:201], v[214:217], v[52:55]
	v_mfma_f32_16x16x32_bf16 v[48:51], v[206:209], v[214:217], v[48:51]
	v_mfma_f32_16x16x32_bf16 v[36:39], v[198:201], v[222:225], v[36:39]
	v_mfma_f32_16x16x32_bf16 v[32:35], v[206:209], v[222:225], v[32:35]
	v_mfma_f32_16x16x32_bf16 v[20:23], v[198:201], v[230:233], v[20:23]
	v_mfma_f32_16x16x32_bf16 v[16:19], v[206:209], v[230:233], v[16:19]
	v_mfma_f32_16x16x32_bf16 v[4:7], v[198:201], v[238:241], v[4:7]
	v_mfma_f32_16x16x32_bf16 v[0:3], v[206:209], v[238:241], v[0:3]
	v_mfma_f32_16x16x32_bf16 v[52:55], v[202:205], v[218:221], v[52:55]
	v_mfma_f32_16x16x32_bf16 v[48:51], v[210:213], v[218:221], v[48:51]
	v_mfma_f32_16x16x32_bf16 v[36:39], v[202:205], v[226:229], v[36:39]
	v_mfma_f32_16x16x32_bf16 v[32:35], v[210:213], v[226:229], v[32:35]
	v_mfma_f32_16x16x32_bf16 v[20:23], v[202:205], v[234:237], v[20:23]
	v_mfma_f32_16x16x32_bf16 v[16:19], v[210:213], v[234:237], v[16:19]
	v_mfma_f32_16x16x32_bf16 v[4:7], v[202:205], v[242:245], v[4:7]
	v_mfma_f32_16x16x32_bf16 v[0:3], v[210:213], v[242:245], v[0:3]
	s_barrier
	s_add_i32 s72, 0, 0x18000
	s_add_i32 s73, 0, 0x1c000
	v_add_u32_e32 v194, s72, v163
	v_add_u32_e32 v210, s73, v163
	ds_read_b128 v[182:185], v194
	ds_read_b128 v[186:189], v194 offset:1024
	ds_read_b128 v[190:193], v194 offset:2048
	ds_read_b128 v[194:197], v194 offset:3072
	ds_read_b128 v[198:201], v210
	ds_read_b128 v[202:205], v210 offset:1024
	ds_read_b128 v[206:209], v210 offset:2048
	ds_read_b128 v[210:213], v210 offset:3072
	s_mov_b32 m0, s59
	v_lshl_add_u64 v[148:149], s[40:41], 0, v[148:149]
	ds_read_b128 v[214:217], v179 offset:32768
	ds_read_b128 v[218:221], v179 offset:33792
	ds_read_b128 v[222:225], v179 offset:34816
	ds_read_b128 v[226:229], v179 offset:35840
	ds_read_b128 v[230:233], v179 offset:36864
	ds_read_b128 v[234:237], v179 offset:37888
	ds_read_b128 v[238:241], v179 offset:38912
	ds_read_b128 v[242:245], v179 offset:39936
	global_load_lds_dwordx4 v[148:149], off
	v_lshl_add_u64 v[148:149], s[40:41], 0, v[150:151]
	s_mov_b32 m0, s60
	s_nop 0
	global_load_lds_dwordx4 v[148:149], off
	s_waitcnt vmcnt(8)
	s_waitcnt lgkmcnt(0)
	s_barrier
	s_waitcnt lgkmcnt(0)
	v_mfma_f32_16x16x32_bf16 v[124:127], v[182:185], v[214:217], v[124:127]
	v_mfma_f32_16x16x32_bf16 v[120:123], v[190:193], v[214:217], v[120:123]
	v_mfma_f32_16x16x32_bf16 v[108:111], v[182:185], v[222:225], v[108:111]
	v_mfma_f32_16x16x32_bf16 v[104:107], v[190:193], v[222:225], v[104:107]
	v_mfma_f32_16x16x32_bf16 v[92:95], v[182:185], v[230:233], v[92:95]
	v_mfma_f32_16x16x32_bf16 v[88:91], v[190:193], v[230:233], v[88:91]
	v_mfma_f32_16x16x32_bf16 v[76:79], v[182:185], v[238:241], v[76:79]
	v_mfma_f32_16x16x32_bf16 v[72:75], v[190:193], v[238:241], v[72:75]
	v_mfma_f32_16x16x32_bf16 v[124:127], v[186:189], v[218:221], v[124:127]
	v_mfma_f32_16x16x32_bf16 v[120:123], v[194:197], v[218:221], v[120:123]
	v_mfma_f32_16x16x32_bf16 v[108:111], v[186:189], v[226:229], v[108:111]
	v_mfma_f32_16x16x32_bf16 v[104:107], v[194:197], v[226:229], v[104:107]
	v_mfma_f32_16x16x32_bf16 v[92:95], v[186:189], v[234:237], v[92:95]
	v_mfma_f32_16x16x32_bf16 v[88:91], v[194:197], v[234:237], v[88:91]
	v_mfma_f32_16x16x32_bf16 v[76:79], v[186:189], v[242:245], v[76:79]
	v_mfma_f32_16x16x32_bf16 v[72:75], v[194:197], v[242:245], v[72:75]
	v_mfma_f32_16x16x32_bf16 v[116:119], v[198:201], v[214:217], v[116:119]
	v_mfma_f32_16x16x32_bf16 v[112:115], v[206:209], v[214:217], v[112:115]
	v_mfma_f32_16x16x32_bf16 v[100:103], v[198:201], v[222:225], v[100:103]
	v_mfma_f32_16x16x32_bf16 v[96:99], v[206:209], v[222:225], v[96:99]
	v_mfma_f32_16x16x32_bf16 v[84:87], v[198:201], v[230:233], v[84:87]
	v_mfma_f32_16x16x32_bf16 v[80:83], v[206:209], v[230:233], v[80:83]
	v_mfma_f32_16x16x32_bf16 v[68:71], v[198:201], v[238:241], v[68:71]
	v_mfma_f32_16x16x32_bf16 v[64:67], v[206:209], v[238:241], v[64:67]
	v_mfma_f32_16x16x32_bf16 v[116:119], v[202:205], v[218:221], v[116:119]
	v_mfma_f32_16x16x32_bf16 v[112:115], v[210:213], v[218:221], v[112:115]
	v_mfma_f32_16x16x32_bf16 v[100:103], v[202:205], v[226:229], v[100:103]
	v_mfma_f32_16x16x32_bf16 v[96:99], v[210:213], v[226:229], v[96:99]
	v_mfma_f32_16x16x32_bf16 v[84:87], v[202:205], v[234:237], v[84:87]
	v_mfma_f32_16x16x32_bf16 v[80:83], v[210:213], v[234:237], v[80:83]
	v_mfma_f32_16x16x32_bf16 v[68:71], v[202:205], v[242:245], v[68:71]
	v_mfma_f32_16x16x32_bf16 v[64:67], v[210:213], v[242:245], v[64:67]
	s_barrier
; template <class Epi, class Sched, class Hook = NoHook>
; __device__ __forceinline__ void gemm_phase_w(LAS unsigned char* lds, const Sched& S, const Epi& E, int wave_id, const Hook& HK = Hook()) {
;     ...
;         if constexpr (!SEG2) {
;             for (int tt = 0; tt < nt; tt += 2) {
;                 if constexpr (GATHER) { if (tt == nt - 2) {
;                     if (has_next) { gnxt_00 = S.grow_l(nxt, lds, nbuf, R0) + (unsigned)(C0 * 2); gnxt_01 = S.grow_l(nxt, lds, nbuf, R1) + (unsigned)(C1 * 2); gnxt_10 = S.grow_l(nxt, lds, nbuf, 128 + R0) + (unsigned)(C0 * 2); gnxt_11 = S.grow_l(nxt, lds, nbuf, 128 + R1) + (unsigned)(C1 * 2); }
;                     else { gnxt_00 = gcur_00; gnxt_01 = gcur_01; gnxt_10 = gcur_10; gnxt_11 = gcur_11; } } }
;                 PG_TRIP(tt, false, false, false);
;             }
	s_bitset1_b32 s22, 7
	s_add_i32 s71, s71, s22
	s_ashr_i32 s41, s71, 31
	s_add_u32 s40, s16, s71
	s_addc_u32 s41, s17, s41
	s_add_i32 s72, s72, s44
	v_lshl_add_u64 v[242:243], s[40:41], 0, v[136:137]
	s_mov_b32 m0, s72
	s_add_i32 s71, s71, 0x80000
	ds_read_b128 v[148:151], v179 offset:49152
	ds_read_b128 v[214:217], v179 offset:50176
	ds_read_b128 v[218:221], v179 offset:51200
	ds_read_b128 v[222:225], v179 offset:52224
	ds_read_b128 v[226:229], v179 offset:53248
	ds_read_b128 v[230:233], v179 offset:54272
	ds_read_b128 v[234:237], v179 offset:55296
	ds_read_b128 v[238:241], v179 offset:56320
	global_load_lds_dwordx4 v[242:243], off
	v_lshl_add_u64 v[242:243], s[40:41], 0, v[138:139]
	s_add_i32 m0, s72, 0x2000
	s_ashr_i32 s41, s71, 31
	s_add_u32 s40, s16, s71
	s_addc_u32 s41, s17, s41
	s_add_i32 s71, s73, s44
	global_load_lds_dwordx4 v[242:243], off
	v_lshl_add_u64 v[242:243], s[40:41], 0, v[136:137]
	s_mov_b32 m0, s71
	v_lshl_add_u64 v[146:147], s[14:15], 0, v[146:147]
	global_load_lds_dwordx4 v[242:243], off
	v_lshl_add_u64 v[242:243], s[40:41], 0, v[138:139]
	s_add_i32 m0, s71, 0x2000
	v_lshl_add_u64 v[146:147], v[146:147], 0, s[22:23]
	global_load_lds_dwordx4 v[242:243], off
	v_lshl_add_u64 v[242:243], s[14:15], 0, v[140:141]
	v_lshl_add_u64 v[242:243], v[242:243], 0, s[22:23]
	s_mov_b32 m0, s51
	s_nop 0
	global_load_lds_dwordx4 v[242:243], off
	s_mov_b32 m0, s61
	s_nop 0
	global_load_lds_dwordx4 v[146:147], off
	s_waitcnt vmcnt(8)
	s_waitcnt lgkmcnt(0)
	s_barrier
	s_waitcnt lgkmcnt(0)
	v_mfma_f32_16x16x32_bf16 v[60:63], v[182:185], v[148:151], v[60:63]
	v_mfma_f32_16x16x32_bf16 v[56:59], v[190:193], v[148:151], v[56:59]
	v_mfma_f32_16x16x32_bf16 v[44:47], v[182:185], v[218:221], v[44:47]
	v_mfma_f32_16x16x32_bf16 v[40:43], v[190:193], v[218:221], v[40:43]
	v_mfma_f32_16x16x32_bf16 v[28:31], v[182:185], v[226:229], v[28:31]
	v_mfma_f32_16x16x32_bf16 v[24:27], v[190:193], v[226:229], v[24:27]
	v_mfma_f32_16x16x32_bf16 v[12:15], v[182:185], v[234:237], v[12:15]
	v_mfma_f32_16x16x32_bf16 v[8:11], v[190:193], v[234:237], v[8:11]
	v_mfma_f32_16x16x32_bf16 v[60:63], v[186:189], v[214:217], v[60:63]
	v_mfma_f32_16x16x32_bf16 v[56:59], v[194:197], v[214:217], v[56:59]
	v_mfma_f32_16x16x32_bf16 v[44:47], v[186:189], v[222:225], v[44:47]
	v_mfma_f32_16x16x32_bf16 v[40:43], v[194:197], v[222:225], v[40:43]
	v_mfma_f32_16x16x32_bf16 v[28:31], v[186:189], v[230:233], v[28:31]
	v_mfma_f32_16x16x32_bf16 v[24:27], v[194:197], v[230:233], v[24:27]
	v_mfma_f32_16x16x32_bf16 v[12:15], v[186:189], v[238:241], v[12:15]
	v_mfma_f32_16x16x32_bf16 v[8:11], v[194:197], v[238:241], v[8:11]
	v_mfma_f32_16x16x32_bf16 v[52:55], v[198:201], v[148:151], v[52:55]
	v_mfma_f32_16x16x32_bf16 v[48:51], v[206:209], v[148:151], v[48:51]
	v_mfma_f32_16x16x32_bf16 v[36:39], v[198:201], v[218:221], v[36:39]
	v_mfma_f32_16x16x32_bf16 v[32:35], v[206:209], v[218:221], v[32:35]
	v_mfma_f32_16x16x32_bf16 v[20:23], v[198:201], v[226:229], v[20:23]
	v_mfma_f32_16x16x32_bf16 v[16:19], v[206:209], v[226:229], v[16:19]
	v_mfma_f32_16x16x32_bf16 v[4:7], v[198:201], v[234:237], v[4:7]
	v_mfma_f32_16x16x32_bf16 v[0:3], v[206:209], v[234:237], v[0:3]
	v_mfma_f32_16x16x32_bf16 v[52:55], v[202:205], v[214:217], v[52:55]
	v_mfma_f32_16x16x32_bf16 v[48:51], v[210:213], v[214:217], v[48:51]
	v_mfma_f32_16x16x32_bf16 v[36:39], v[202:205], v[222:225], v[36:39]
	v_mfma_f32_16x16x32_bf16 v[32:35], v[210:213], v[222:225], v[32:35]
	v_mfma_f32_16x16x32_bf16 v[20:23], v[202:205], v[230:233], v[20:23]
	v_mfma_f32_16x16x32_bf16 v[16:19], v[210:213], v[230:233], v[16:19]
	v_mfma_f32_16x16x32_bf16 v[4:7], v[202:205], v[238:241], v[4:7]
	v_mfma_f32_16x16x32_bf16 v[0:3], v[210:213], v[238:241], v[0:3]
	s_add_i32 s69, s69, 2
	s_addk_i32 s70, 0x100
	s_add_u32 s38, s38, 0x100
	s_addc_u32 s39, s39, 0
	s_cmp_gt_u32 s69, 29
	s_barrier
	s_cbranch_scc1 .LBB0_2414

.LBB0_2522:
	ds_read_b128 v[156:159], v153
	ds_read_b128 v[160:163], v153 offset:1024
	ds_read_b128 v[164:167], v153 offset:2048
	ds_read_b128 v[168:171], v153 offset:3072
	ds_read_b128 v[172:175], v154
	ds_read_b128 v[176:179], v154 offset:1024
	ds_read_b128 v[180:183], v154 offset:2048
	ds_read_b128 v[184:187], v154 offset:3072
	s_add_i32 s22, s53, s10
	s_add_u32 s58, s28, s22
	s_addc_u32 s59, s29, 0
	s_add_i32 m0, s31, 0xc000
	s_add_i32 s60, s31, 0xe000
	s_add_i32 s61, s10, 0xfffc0080
	s_cmp_eq_u32 s19, 12
	s_cselect_b32 s22, s50, s53
	s_cselect_b32 s23, s51, s56
	v_lshl_add_u64 v[220:221], s[58:59], 0, v[130:131]
	ds_read_b128 v[188:191], v155
	ds_read_b128 v[192:195], v155 offset:1024
	ds_read_b128 v[196:199], v155 offset:2048
	ds_read_b128 v[200:203], v155 offset:3072
	ds_read_b128 v[204:207], v155 offset:4096
	ds_read_b128 v[208:211], v155 offset:5120
	ds_read_b128 v[212:215], v155 offset:6144
	ds_read_b128 v[216:219], v155 offset:7168
	global_load_lds_dwordx4 v[220:221], off
	v_lshl_add_u64 v[220:221], s[58:59], 0, v[132:133]
	s_mov_b32 m0, s60
	s_nop 0
	global_load_lds_dwordx4 v[220:221], off
	s_waitcnt vmcnt(8)
	s_waitcnt lgkmcnt(0)
	s_barrier
	s_waitcnt lgkmcnt(0)
	v_mfma_f32_16x16x32_bf16 v[124:127], v[156:159], v[188:191], v[124:127]
	v_mfma_f32_16x16x32_bf16 v[120:123], v[164:167], v[188:191], v[120:123]
	v_mfma_f32_16x16x32_bf16 v[108:111], v[156:159], v[196:199], v[108:111]
	v_mfma_f32_16x16x32_bf16 v[104:107], v[164:167], v[196:199], v[104:107]
	v_mfma_f32_16x16x32_bf16 v[92:95], v[156:159], v[204:207], v[92:95]
	v_mfma_f32_16x16x32_bf16 v[88:91], v[164:167], v[204:207], v[88:91]
	v_mfma_f32_16x16x32_bf16 v[76:79], v[156:159], v[212:215], v[76:79]
	v_mfma_f32_16x16x32_bf16 v[72:75], v[164:167], v[212:215], v[72:75]
	v_mfma_f32_16x16x32_bf16 v[124:127], v[160:163], v[192:195], v[124:127]
	v_mfma_f32_16x16x32_bf16 v[120:123], v[168:171], v[192:195], v[120:123]
	v_mfma_f32_16x16x32_bf16 v[108:111], v[160:163], v[200:203], v[108:111]
	v_mfma_f32_16x16x32_bf16 v[104:107], v[168:171], v[200:203], v[104:107]
	v_mfma_f32_16x16x32_bf16 v[92:95], v[160:163], v[208:211], v[92:95]
	v_mfma_f32_16x16x32_bf16 v[88:91], v[168:171], v[208:211], v[88:91]
	v_mfma_f32_16x16x32_bf16 v[76:79], v[160:163], v[216:219], v[76:79]
	v_mfma_f32_16x16x32_bf16 v[72:75], v[168:171], v[216:219], v[72:75]
	v_mfma_f32_16x16x32_bf16 v[116:119], v[172:175], v[188:191], v[116:119]
	v_mfma_f32_16x16x32_bf16 v[112:115], v[180:183], v[188:191], v[112:115]
	v_mfma_f32_16x16x32_bf16 v[100:103], v[172:175], v[196:199], v[100:103]
	v_mfma_f32_16x16x32_bf16 v[96:99], v[180:183], v[196:199], v[96:99]
	v_mfma_f32_16x16x32_bf16 v[84:87], v[172:175], v[204:207], v[84:87]
	v_mfma_f32_16x16x32_bf16 v[80:83], v[180:183], v[204:207], v[80:83]
	v_mfma_f32_16x16x32_bf16 v[68:71], v[172:175], v[212:215], v[68:71]
	v_mfma_f32_16x16x32_bf16 v[64:67], v[180:183], v[212:215], v[64:67]
	v_mfma_f32_16x16x32_bf16 v[116:119], v[176:179], v[192:195], v[116:119]
	v_mfma_f32_16x16x32_bf16 v[112:115], v[184:187], v[192:195], v[112:115]
	v_mfma_f32_16x16x32_bf16 v[100:103], v[176:179], v[200:203], v[100:103]
	v_mfma_f32_16x16x32_bf16 v[96:99], v[184:187], v[200:203], v[96:99]
	v_mfma_f32_16x16x32_bf16 v[84:87], v[176:179], v[208:211], v[84:87]
	v_mfma_f32_16x16x32_bf16 v[80:83], v[184:187], v[208:211], v[80:83]
	v_mfma_f32_16x16x32_bf16 v[68:71], v[176:179], v[216:219], v[68:71]
	v_mfma_f32_16x16x32_bf16 v[64:67], v[184:187], v[216:219], v[64:67]
	s_barrier
	s_cselect_b32 s60, 0, s61
	s_add_i32 s58, s60, s23
	s_ashr_i32 s59, s58, 31
	s_add_u32 s58, s8, s58
	s_addc_u32 s59, s9, s59
	s_add_i32 s61, s42, s26
	v_lshl_add_u64 v[220:221], s[58:59], 0, v[130:131]
	s_mov_b32 m0, s61
	ds_read_b128 v[188:191], v155 offset:16384
	ds_read_b128 v[192:195], v155 offset:17408
	ds_read_b128 v[196:199], v155 offset:18432
	ds_read_b128 v[200:203], v155 offset:19456
	ds_read_b128 v[204:207], v155 offset:20480
	ds_read_b128 v[208:211], v155 offset:21504
	ds_read_b128 v[212:215], v155 offset:22528
	ds_read_b128 v[216:219], v155 offset:23552
	global_load_lds_dwordx4 v[220:221], off
	s_add_i32 m0, s61, 0x2000
	s_add_i32 s61, s23, 0x40000
	v_lshl_add_u64 v[220:221], s[58:59], 0, v[132:133]
	s_add_i32 s58, s61, s60
	s_ashr_i32 s59, s58, 31
	s_add_u32 s58, s8, s58
	s_addc_u32 s59, s9, s59
	s_add_i32 s62, s43, s26
	global_load_lds_dwordx4 v[220:221], off
	v_lshl_add_u64 v[220:221], s[58:59], 0, v[130:131]
	s_mov_b32 m0, s62
	s_nop 0
	global_load_lds_dwordx4 v[220:221], off
	s_add_i32 m0, s62, 0x2000
	s_add_i32 s62, s60, s22
	v_lshl_add_u64 v[220:221], s[58:59], 0, v[132:133]
	s_add_u32 s58, s28, s62
	s_addc_u32 s59, s29, 0
	global_load_lds_dwordx4 v[220:221], off
	v_lshl_add_u64 v[220:221], s[58:59], 0, v[130:131]
	s_mov_b32 m0, s31
	s_nop 0
	global_load_lds_dwordx4 v[220:221], off
	v_lshl_add_u64 v[220:221], s[58:59], 0, v[132:133]
	s_mov_b32 m0, s33
	s_nop 0
	global_load_lds_dwordx4 v[220:221], off
	s_waitcnt vmcnt(8)
	s_waitcnt lgkmcnt(0)
	s_barrier
	s_waitcnt lgkmcnt(0)
	v_mfma_f32_16x16x32_bf16 v[60:63], v[156:159], v[188:191], v[60:63]
	v_mfma_f32_16x16x32_bf16 v[56:59], v[164:167], v[188:191], v[56:59]
	v_mfma_f32_16x16x32_bf16 v[44:47], v[156:159], v[196:199], v[44:47]
	v_mfma_f32_16x16x32_bf16 v[40:43], v[164:167], v[196:199], v[40:43]
	v_mfma_f32_16x16x32_bf16 v[28:31], v[156:159], v[204:207], v[28:31]
	v_mfma_f32_16x16x32_bf16 v[24:27], v[164:167], v[204:207], v[24:27]
	v_mfma_f32_16x16x32_bf16 v[12:15], v[156:159], v[212:215], v[12:15]
	v_mfma_f32_16x16x32_bf16 v[8:11], v[164:167], v[212:215], v[8:11]
	v_mfma_f32_16x16x32_bf16 v[60:63], v[160:163], v[192:195], v[60:63]
	v_mfma_f32_16x16x32_bf16 v[56:59], v[168:171], v[192:195], v[56:59]
	v_mfma_f32_16x16x32_bf16 v[44:47], v[160:163], v[200:203], v[44:47]
	v_mfma_f32_16x16x32_bf16 v[40:43], v[168:171], v[200:203], v[40:43]
	v_mfma_f32_16x16x32_bf16 v[28:31], v[160:163], v[208:211], v[28:31]
	v_mfma_f32_16x16x32_bf16 v[24:27], v[168:171], v[208:211], v[24:27]
	v_mfma_f32_16x16x32_bf16 v[12:15], v[160:163], v[216:219], v[12:15]
	v_mfma_f32_16x16x32_bf16 v[8:11], v[168:171], v[216:219], v[8:11]
	v_mfma_f32_16x16x32_bf16 v[52:55], v[172:175], v[188:191], v[52:55]
	v_mfma_f32_16x16x32_bf16 v[48:51], v[180:183], v[188:191], v[48:51]
	v_mfma_f32_16x16x32_bf16 v[36:39], v[172:175], v[196:199], v[36:39]
	v_mfma_f32_16x16x32_bf16 v[32:35], v[180:183], v[196:199], v[32:35]
	v_mfma_f32_16x16x32_bf16 v[20:23], v[172:175], v[204:207], v[20:23]
	v_mfma_f32_16x16x32_bf16 v[16:19], v[180:183], v[204:207], v[16:19]
	v_mfma_f32_16x16x32_bf16 v[4:7], v[172:175], v[212:215], v[4:7]
	v_mfma_f32_16x16x32_bf16 v[0:3], v[180:183], v[212:215], v[0:3]
	v_mfma_f32_16x16x32_bf16 v[52:55], v[176:179], v[192:195], v[52:55]
	v_mfma_f32_16x16x32_bf16 v[48:51], v[184:187], v[192:195], v[48:51]
	v_mfma_f32_16x16x32_bf16 v[36:39], v[176:179], v[200:203], v[36:39]
	v_mfma_f32_16x16x32_bf16 v[32:35], v[184:187], v[200:203], v[32:35]
	v_mfma_f32_16x16x32_bf16 v[20:23], v[176:179], v[208:211], v[20:23]
	v_mfma_f32_16x16x32_bf16 v[16:19], v[184:187], v[208:211], v[16:19]
	v_mfma_f32_16x16x32_bf16 v[4:7], v[176:179], v[216:219], v[4:7]
	v_mfma_f32_16x16x32_bf16 v[0:3], v[184:187], v[216:219], v[0:3]
	s_barrier
	s_add_i32 s63, 0, 0x18000
	s_add_i32 s64, 0, 0x1c000
	v_add_u32_e32 v168, s63, v137
	v_add_u32_e32 v184, s64, v137
	ds_read_b128 v[156:159], v168
	ds_read_b128 v[160:163], v168 offset:1024
	ds_read_b128 v[164:167], v168 offset:2048
	ds_read_b128 v[168:171], v168 offset:3072
	ds_read_b128 v[172:175], v184
	ds_read_b128 v[176:179], v184 offset:1024
	ds_read_b128 v[180:183], v184 offset:2048
	ds_read_b128 v[184:187], v184 offset:3072
	s_add_i32 s62, s62, 0x40000
	s_add_u32 s58, s28, s62
	s_addc_u32 s59, s29, 0
	s_mov_b32 m0, s34
	v_lshl_add_u64 v[220:221], s[58:59], 0, v[130:131]
	ds_read_b128 v[188:191], v155 offset:32768
	ds_read_b128 v[192:195], v155 offset:33792
	ds_read_b128 v[196:199], v155 offset:34816
	ds_read_b128 v[200:203], v155 offset:35840
	ds_read_b128 v[204:207], v155 offset:36864
	ds_read_b128 v[208:211], v155 offset:37888
	ds_read_b128 v[212:215], v155 offset:38912
	ds_read_b128 v[216:219], v155 offset:39936
	global_load_lds_dwordx4 v[220:221], off
	v_lshl_add_u64 v[220:221], s[58:59], 0, v[132:133]
	s_mov_b32 m0, s35
	s_nop 0
	global_load_lds_dwordx4 v[220:221], off
	s_waitcnt vmcnt(8)
	s_waitcnt lgkmcnt(0)
	s_barrier
	s_waitcnt lgkmcnt(0)
	v_mfma_f32_16x16x32_bf16 v[124:127], v[156:159], v[188:191], v[124:127]
	v_mfma_f32_16x16x32_bf16 v[120:123], v[164:167], v[188:191], v[120:123]
	v_mfma_f32_16x16x32_bf16 v[108:111], v[156:159], v[196:199], v[108:111]
	v_mfma_f32_16x16x32_bf16 v[104:107], v[164:167], v[196:199], v[104:107]
	v_mfma_f32_16x16x32_bf16 v[92:95], v[156:159], v[204:207], v[92:95]
	v_mfma_f32_16x16x32_bf16 v[88:91], v[164:167], v[204:207], v[88:91]
	v_mfma_f32_16x16x32_bf16 v[76:79], v[156:159], v[212:215], v[76:79]
	v_mfma_f32_16x16x32_bf16 v[72:75], v[164:167], v[212:215], v[72:75]
	v_mfma_f32_16x16x32_bf16 v[124:127], v[160:163], v[192:195], v[124:127]
	v_mfma_f32_16x16x32_bf16 v[120:123], v[168:171], v[192:195], v[120:123]
	v_mfma_f32_16x16x32_bf16 v[108:111], v[160:163], v[200:203], v[108:111]
	v_mfma_f32_16x16x32_bf16 v[104:107], v[168:171], v[200:203], v[104:107]
	v_mfma_f32_16x16x32_bf16 v[92:95], v[160:163], v[208:211], v[92:95]
	v_mfma_f32_16x16x32_bf16 v[88:91], v[168:171], v[208:211], v[88:91]
	v_mfma_f32_16x16x32_bf16 v[76:79], v[160:163], v[216:219], v[76:79]
	v_mfma_f32_16x16x32_bf16 v[72:75], v[168:171], v[216:219], v[72:75]
	v_mfma_f32_16x16x32_bf16 v[116:119], v[172:175], v[188:191], v[116:119]
	v_mfma_f32_16x16x32_bf16 v[112:115], v[180:183], v[188:191], v[112:115]
	v_mfma_f32_16x16x32_bf16 v[100:103], v[172:175], v[196:199], v[100:103]
	v_mfma_f32_16x16x32_bf16 v[96:99], v[180:183], v[196:199], v[96:99]
	v_mfma_f32_16x16x32_bf16 v[84:87], v[172:175], v[204:207], v[84:87]
	v_mfma_f32_16x16x32_bf16 v[80:83], v[180:183], v[204:207], v[80:83]
	v_mfma_f32_16x16x32_bf16 v[68:71], v[172:175], v[212:215], v[68:71]
	v_mfma_f32_16x16x32_bf16 v[64:67], v[180:183], v[212:215], v[64:67]
	v_mfma_f32_16x16x32_bf16 v[116:119], v[176:179], v[192:195], v[116:119]
	v_mfma_f32_16x16x32_bf16 v[112:115], v[184:187], v[192:195], v[112:115]
	v_mfma_f32_16x16x32_bf16 v[100:103], v[176:179], v[200:203], v[100:103]
	v_mfma_f32_16x16x32_bf16 v[96:99], v[184:187], v[200:203], v[96:99]
	v_mfma_f32_16x16x32_bf16 v[84:87], v[176:179], v[208:211], v[84:87]
	v_mfma_f32_16x16x32_bf16 v[80:83], v[184:187], v[208:211], v[80:83]
	v_mfma_f32_16x16x32_bf16 v[68:71], v[176:179], v[216:219], v[68:71]
	v_mfma_f32_16x16x32_bf16 v[64:67], v[184:187], v[216:219], v[64:67]
	s_barrier
; template <class Epi, class Sched, class Hook = NoHook>
; __device__ __forceinline__ void gemm_phase_w(LAS unsigned char* lds, const Sched& S, const Epi& E, int wave_id, const Hook& HK = Hook()) {
;     ...
;         if constexpr (!SEG2) {
;             for (int tt = 0; tt < nt; tt += 2) {
;                 if constexpr (GATHER) { if (tt == nt - 2) {
;                     if (has_next) { gnxt_00 = S.grow_l(nxt, lds, nbuf, R0) + (unsigned)(C0 * 2); gnxt_01 = S.grow_l(nxt, lds, nbuf, R1) + (unsigned)(C1 * 2); gnxt_10 = S.grow_l(nxt, lds, nbuf, 128 + R0) + (unsigned)(C0 * 2); gnxt_11 = S.grow_l(nxt, lds, nbuf, 128 + R1) + (unsigned)(C1 * 2); }
;                     else { gnxt_00 = gcur_00; gnxt_01 = gcur_01; gnxt_10 = gcur_10; gnxt_11 = gcur_11; } } }
;                 PG_TRIP(tt, false, false, false);
;             }
	s_bitset1_b32 s60, 7
	s_add_i32 s23, s60, s23
	s_ashr_i32 s59, s23, 31
	s_add_u32 s58, s8, s23
	s_addc_u32 s59, s9, s59
	s_add_i32 s23, s63, s26
	v_lshl_add_u64 v[220:221], s[58:59], 0, v[130:131]
	s_mov_b32 m0, s23
	ds_read_b128 v[188:191], v155 offset:49152
	ds_read_b128 v[192:195], v155 offset:50176
	ds_read_b128 v[196:199], v155 offset:51200
	ds_read_b128 v[200:203], v155 offset:52224
	ds_read_b128 v[204:207], v155 offset:53248
	ds_read_b128 v[208:211], v155 offset:54272
	ds_read_b128 v[212:215], v155 offset:55296
	ds_read_b128 v[216:219], v155 offset:56320
	global_load_lds_dwordx4 v[220:221], off
	s_add_i32 m0, s23, 0x2000
	s_add_i32 s23, s60, s61
	v_lshl_add_u64 v[220:221], s[58:59], 0, v[132:133]
	s_ashr_i32 s59, s23, 31
	s_add_u32 s58, s8, s23
	s_addc_u32 s59, s9, s59
	s_add_i32 s23, s64, s26
	global_load_lds_dwordx4 v[220:221], off
	v_lshl_add_u64 v[220:221], s[58:59], 0, v[130:131]
	s_mov_b32 m0, s23
	s_add_i32 s60, s60, s22
	global_load_lds_dwordx4 v[220:221], off
	s_add_i32 m0, s23, 0x2000
	s_add_u32 s22, s28, s60
	v_lshl_add_u64 v[220:221], s[58:59], 0, v[132:133]
	s_addc_u32 s23, s29, 0
	global_load_lds_dwordx4 v[220:221], off
	v_lshl_add_u64 v[220:221], s[22:23], 0, v[130:131]
	s_mov_b32 m0, s37
	s_nop 0
	global_load_lds_dwordx4 v[220:221], off
	v_lshl_add_u64 v[220:221], s[22:23], 0, v[132:133]
	s_mov_b32 m0, s38
	s_nop 0
	global_load_lds_dwordx4 v[220:221], off
	s_waitcnt vmcnt(8)
	s_waitcnt lgkmcnt(0)
	s_barrier
	s_waitcnt lgkmcnt(0)
	v_mfma_f32_16x16x32_bf16 v[60:63], v[156:159], v[188:191], v[60:63]
	v_mfma_f32_16x16x32_bf16 v[56:59], v[164:167], v[188:191], v[56:59]
	v_mfma_f32_16x16x32_bf16 v[44:47], v[156:159], v[196:199], v[44:47]
	v_mfma_f32_16x16x32_bf16 v[40:43], v[164:167], v[196:199], v[40:43]
	v_mfma_f32_16x16x32_bf16 v[28:31], v[156:159], v[204:207], v[28:31]
	v_mfma_f32_16x16x32_bf16 v[24:27], v[164:167], v[204:207], v[24:27]
	v_mfma_f32_16x16x32_bf16 v[12:15], v[156:159], v[212:215], v[12:15]
	v_mfma_f32_16x16x32_bf16 v[8:11], v[164:167], v[212:215], v[8:11]
	v_mfma_f32_16x16x32_bf16 v[60:63], v[160:163], v[192:195], v[60:63]
	v_mfma_f32_16x16x32_bf16 v[56:59], v[168:171], v[192:195], v[56:59]
	v_mfma_f32_16x16x32_bf16 v[44:47], v[160:163], v[200:203], v[44:47]
	v_mfma_f32_16x16x32_bf16 v[40:43], v[168:171], v[200:203], v[40:43]
	v_mfma_f32_16x16x32_bf16 v[28:31], v[160:163], v[208:211], v[28:31]
	v_mfma_f32_16x16x32_bf16 v[24:27], v[168:171], v[208:211], v[24:27]
	v_mfma_f32_16x16x32_bf16 v[12:15], v[160:163], v[216:219], v[12:15]
	v_mfma_f32_16x16x32_bf16 v[8:11], v[168:171], v[216:219], v[8:11]
	v_mfma_f32_16x16x32_bf16 v[52:55], v[172:175], v[188:191], v[52:55]
	v_mfma_f32_16x16x32_bf16 v[48:51], v[180:183], v[188:191], v[48:51]
	v_mfma_f32_16x16x32_bf16 v[36:39], v[172:175], v[196:199], v[36:39]
	v_mfma_f32_16x16x32_bf16 v[32:35], v[180:183], v[196:199], v[32:35]
	v_mfma_f32_16x16x32_bf16 v[20:23], v[172:175], v[204:207], v[20:23]
	v_mfma_f32_16x16x32_bf16 v[16:19], v[180:183], v[204:207], v[16:19]
	v_mfma_f32_16x16x32_bf16 v[4:7], v[172:175], v[212:215], v[4:7]
	v_mfma_f32_16x16x32_bf16 v[0:3], v[180:183], v[212:215], v[0:3]
	v_mfma_f32_16x16x32_bf16 v[52:55], v[176:179], v[192:195], v[52:55]
	v_mfma_f32_16x16x32_bf16 v[48:51], v[184:187], v[192:195], v[48:51]
	v_mfma_f32_16x16x32_bf16 v[36:39], v[176:179], v[200:203], v[36:39]
	v_mfma_f32_16x16x32_bf16 v[32:35], v[184:187], v[200:203], v[32:35]
	v_mfma_f32_16x16x32_bf16 v[20:23], v[176:179], v[208:211], v[20:23]
	v_mfma_f32_16x16x32_bf16 v[16:19], v[184:187], v[208:211], v[16:19]
	v_mfma_f32_16x16x32_bf16 v[4:7], v[176:179], v[216:219], v[4:7]
	v_mfma_f32_16x16x32_bf16 v[0:3], v[184:187], v[216:219], v[0:3]
	s_addk_i32 s10, 0x100
	s_add_i32 s19, s19, 2
	s_cmp_gt_u32 s19, 13
	s_barrier
	s_cbranch_scc0 .LBB0_2522
	s_and_b64 vcc, exec, s[6:7]
	s_cbranch_vccz .LBB0_2525
	s_barrier
